# one static s_setprio 1 for waves 4-7 at kernel entry, all 240 per-segment s_setprio deleted (on top of the diff tile loop rewrite)
# speedup vs baseline: 1.0117x; 1.0025x over previous
_Z6mk_fwd4Args:
	s_load_dword s3, s[0:1], 0xb8
	s_add_u32 s4, s0, 0xb8
	s_addc_u32 s5, s1, 0
	v_readfirstlane_b32 s52, v0
	v_writelane_b32 v252, s4, 0
	s_nop 1
	v_writelane_b32 v252, s5, 1
	s_waitcnt lgkmcnt(0)
	s_cmp_lt_u32 s52, 0x100
	s_cbranch_scc1 .Lprio_skip
	s_setprio 1
.Lprio_skip:
	s_and_b32 s4, s3, 7
	s_cmp_lg_u32 s4, 0
	v_writelane_b32 v252, s2, 2
	s_cbranch_scc1 .LBB0_2
	s_ashr_i32 s5, s2, 31
	s_lshr_b32 s5, s5, 29
	s_add_i32 s5, s2, s5
	s_and_b32 s6, s5, -8
	s_ashr_i32 s4, s3, 3
	s_sub_i32 s6, s2, s6
	s_mul_i32 s4, s4, s6
	s_ashr_i32 s5, s5, 3
	s_add_i32 s4, s4, s5
	v_writelane_b32 v252, s4, 2

.Lnobar_e1o:
.LBB0_417:
	s_add_u32 s28, s6, 0xfffc0080
	s_addc_u32 s29, s7, -1
	s_add_i32 s43, 0, 0x10000
	s_cmp_eq_u32 s42, 12
	s_cselect_b32 s31, s5, s29
	s_cselect_b32 s30, s8, s28
	s_cselect_b32 s29, s9, s33
	s_cselect_b32 s28, s21, s23
	s_add_i32 s63, 0, 0x14000
	v_add_u32_e32 v142, s43, v186
	v_add_u32_e32 v168, s63, v186
	ds_read_b128 v[130:133], v142
	ds_read_b128 v[134:137], v142 offset:1024
	ds_read_b128 v[138:141], v142 offset:2048
	ds_read_b128 v[142:145], v142 offset:3072
	ds_read_b128 v[146:149], v168
	ds_read_b128 v[150:153], v168 offset:1024
	ds_read_b128 v[154:157], v168 offset:2048
	ds_read_b128 v[168:171], v168 offset:3072
	v_lshl_add_u64 v[216:217], s[6:7], 0, v[166:167]
	s_add_i32 m0, s45, 0xc000
	ds_read_b128 v[172:175], v188
	ds_read_b128 v[176:179], v188 offset:1024
	ds_read_b128 v[180:183], v188 offset:2048
	ds_read_b128 v[190:193], v188 offset:3072
	ds_read_b128 v[194:197], v188 offset:4096
	ds_read_b128 v[198:201], v188 offset:5120
	ds_read_b128 v[202:205], v188 offset:6144
	ds_read_b128 v[206:209], v188 offset:7168
	global_load_lds_dwordx4 v[216:217], off
	s_add_i32 m0, s45, 0xe000
	v_lshl_add_u64 v[216:217], s[6:7], 0, v[164:165]
	global_load_lds_dwordx4 v[216:217], off
	s_waitcnt vmcnt(8)
	s_waitcnt lgkmcnt(0)
	s_barrier
	s_waitcnt lgkmcnt(0)
	v_mfma_f32_16x16x32_bf16 v[126:129], v[130:133], v[172:175], v[126:129]
	v_mfma_f32_16x16x32_bf16 v[122:125], v[138:141], v[172:175], v[122:125]
	v_mfma_f32_16x16x32_bf16 v[114:117], v[130:133], v[180:183], v[114:117]
	v_mfma_f32_16x16x32_bf16 v[106:109], v[138:141], v[180:183], v[106:109]
	v_mfma_f32_16x16x32_bf16 v[98:101], v[130:133], v[194:197], v[98:101]
	v_mfma_f32_16x16x32_bf16 v[90:93], v[138:141], v[194:197], v[90:93]
	v_mfma_f32_16x16x32_bf16 v[82:85], v[130:133], v[202:205], v[82:85]
	v_mfma_f32_16x16x32_bf16 v[74:77], v[138:141], v[202:205], v[74:77]
	v_mfma_f32_16x16x32_bf16 v[126:129], v[134:137], v[176:179], v[126:129]
	v_mfma_f32_16x16x32_bf16 v[122:125], v[142:145], v[176:179], v[122:125]
	v_mfma_f32_16x16x32_bf16 v[114:117], v[134:137], v[190:193], v[114:117]
	v_mfma_f32_16x16x32_bf16 v[106:109], v[142:145], v[190:193], v[106:109]
	v_mfma_f32_16x16x32_bf16 v[98:101], v[134:137], v[198:201], v[98:101]
	v_mfma_f32_16x16x32_bf16 v[90:93], v[142:145], v[198:201], v[90:93]
	v_mfma_f32_16x16x32_bf16 v[82:85], v[134:137], v[206:209], v[82:85]
	v_mfma_f32_16x16x32_bf16 v[74:77], v[142:145], v[206:209], v[74:77]
	v_mfma_f32_16x16x32_bf16 v[118:121], v[146:149], v[172:175], v[118:121]
	v_mfma_f32_16x16x32_bf16 v[110:113], v[154:157], v[172:175], v[110:113]
	v_mfma_f32_16x16x32_bf16 v[102:105], v[146:149], v[180:183], v[102:105]
	v_mfma_f32_16x16x32_bf16 v[94:97], v[154:157], v[180:183], v[94:97]
	v_mfma_f32_16x16x32_bf16 v[86:89], v[146:149], v[194:197], v[86:89]
	v_mfma_f32_16x16x32_bf16 v[78:81], v[154:157], v[194:197], v[78:81]
	v_mfma_f32_16x16x32_bf16 v[70:73], v[146:149], v[202:205], v[70:73]
	v_mfma_f32_16x16x32_bf16 v[66:69], v[154:157], v[202:205], v[66:69]
	v_mfma_f32_16x16x32_bf16 v[118:121], v[150:153], v[176:179], v[118:121]
	v_mfma_f32_16x16x32_bf16 v[110:113], v[168:171], v[176:179], v[110:113]
	v_mfma_f32_16x16x32_bf16 v[102:105], v[150:153], v[190:193], v[102:105]
	v_mfma_f32_16x16x32_bf16 v[94:97], v[168:171], v[190:193], v[94:97]
	v_mfma_f32_16x16x32_bf16 v[86:89], v[150:153], v[198:201], v[86:89]
	v_mfma_f32_16x16x32_bf16 v[78:81], v[168:171], v[198:201], v[78:81]
	v_mfma_f32_16x16x32_bf16 v[70:73], v[150:153], v[206:209], v[70:73]
	v_mfma_f32_16x16x32_bf16 v[66:69], v[168:171], v[206:209], v[66:69]
	s_barrier
	s_add_i32 s43, s43, s44
	v_lshl_add_u64 v[216:217], s[28:29], 0, v[0:1]
	s_mov_b32 m0, s43
	ds_read_b128 v[172:175], v188 offset:16384
	ds_read_b128 v[176:179], v188 offset:17408
	ds_read_b128 v[180:183], v188 offset:18432
	ds_read_b128 v[190:193], v188 offset:19456
	ds_read_b128 v[194:197], v188 offset:20480
	ds_read_b128 v[198:201], v188 offset:21504
	ds_read_b128 v[202:205], v188 offset:22528
	ds_read_b128 v[206:209], v188 offset:23552
	global_load_lds_dwordx4 v[216:217], off
	s_add_i32 m0, s43, 0x2000
	s_add_u32 s58, s28, 0x40000
	v_lshl_add_u64 v[218:219], s[28:29], 0, v[158:159]
	s_addc_u32 s59, s29, 0
	s_add_i32 s43, s63, s44
	global_load_lds_dwordx4 v[218:219], off
	v_lshl_add_u64 v[220:221], s[58:59], 0, v[0:1]
	s_mov_b32 m0, s43
	v_lshl_add_u64 v[222:223], s[30:31], 0, v[160:161]
	global_load_lds_dwordx4 v[220:221], off
	s_add_i32 m0, s43, 0x2000
	v_lshl_add_u64 v[220:221], s[58:59], 0, v[158:159]
	global_load_lds_dwordx4 v[220:221], off
	s_mov_b32 m0, s45
	v_lshl_add_u64 v[220:221], s[30:31], 0, v[162:163]
	global_load_lds_dwordx4 v[220:221], off
	s_mov_b32 m0, s46
	s_nop 0
	global_load_lds_dwordx4 v[222:223], off
	s_waitcnt vmcnt(8)
	s_waitcnt lgkmcnt(0)
	s_barrier
	s_waitcnt lgkmcnt(0)
	v_mfma_f32_16x16x32_bf16 v[62:65], v[130:133], v[172:175], v[62:65]
	v_mfma_f32_16x16x32_bf16 v[58:61], v[138:141], v[172:175], v[58:61]
	v_mfma_f32_16x16x32_bf16 v[50:53], v[130:133], v[180:183], v[50:53]
	v_mfma_f32_16x16x32_bf16 v[42:45], v[138:141], v[180:183], v[42:45]
	v_mfma_f32_16x16x32_bf16 v[34:37], v[130:133], v[194:197], v[34:37]
	v_mfma_f32_16x16x32_bf16 v[26:29], v[138:141], v[194:197], v[26:29]
	v_mfma_f32_16x16x32_bf16 v[18:21], v[130:133], v[202:205], v[18:21]
	v_mfma_f32_16x16x32_bf16 v[10:13], v[138:141], v[202:205], v[10:13]
	v_mfma_f32_16x16x32_bf16 v[62:65], v[134:137], v[176:179], v[62:65]
	v_mfma_f32_16x16x32_bf16 v[58:61], v[142:145], v[176:179], v[58:61]
	v_mfma_f32_16x16x32_bf16 v[50:53], v[134:137], v[190:193], v[50:53]
	v_mfma_f32_16x16x32_bf16 v[42:45], v[142:145], v[190:193], v[42:45]
	v_mfma_f32_16x16x32_bf16 v[34:37], v[134:137], v[198:201], v[34:37]
	v_mfma_f32_16x16x32_bf16 v[26:29], v[142:145], v[198:201], v[26:29]
	v_mfma_f32_16x16x32_bf16 v[18:21], v[134:137], v[206:209], v[18:21]
	v_mfma_f32_16x16x32_bf16 v[10:13], v[142:145], v[206:209], v[10:13]
	v_mfma_f32_16x16x32_bf16 v[54:57], v[146:149], v[172:175], v[54:57]
	v_mfma_f32_16x16x32_bf16 v[46:49], v[154:157], v[172:175], v[46:49]
	v_mfma_f32_16x16x32_bf16 v[38:41], v[146:149], v[180:183], v[38:41]
	v_mfma_f32_16x16x32_bf16 v[30:33], v[154:157], v[180:183], v[30:33]
	v_mfma_f32_16x16x32_bf16 v[22:25], v[146:149], v[194:197], v[22:25]
	v_mfma_f32_16x16x32_bf16 v[14:17], v[154:157], v[194:197], v[14:17]
	v_mfma_f32_16x16x32_bf16 v[6:9], v[146:149], v[202:205], v[6:9]
	v_mfma_f32_16x16x32_bf16 v[2:5], v[154:157], v[202:205], v[2:5]
	v_mfma_f32_16x16x32_bf16 v[54:57], v[150:153], v[176:179], v[54:57]
	v_mfma_f32_16x16x32_bf16 v[46:49], v[168:171], v[176:179], v[46:49]
	v_mfma_f32_16x16x32_bf16 v[38:41], v[150:153], v[190:193], v[38:41]
	v_mfma_f32_16x16x32_bf16 v[30:33], v[168:171], v[190:193], v[30:33]
	v_mfma_f32_16x16x32_bf16 v[22:25], v[150:153], v[198:201], v[22:25]
	v_mfma_f32_16x16x32_bf16 v[14:17], v[168:171], v[198:201], v[14:17]
	v_mfma_f32_16x16x32_bf16 v[6:9], v[150:153], v[206:209], v[6:9]
	v_mfma_f32_16x16x32_bf16 v[2:5], v[168:171], v[206:209], v[2:5]
	s_barrier
	s_add_i32 s43, 0, 0x18000
	s_add_i32 s58, 0, 0x1c000
	v_add_u32_e32 v142, s43, v186
	v_add_u32_e32 v168, s58, v186
	ds_read_b128 v[130:133], v142
	ds_read_b128 v[134:137], v142 offset:1024
	ds_read_b128 v[138:141], v142 offset:2048
	ds_read_b128 v[142:145], v142 offset:3072
	ds_read_b128 v[146:149], v168
	ds_read_b128 v[150:153], v168 offset:1024
	ds_read_b128 v[154:157], v168 offset:2048
	ds_read_b128 v[168:171], v168 offset:3072
	s_add_u32 s30, s30, 0x40000
	s_addc_u32 s31, s31, 0
	s_mov_b32 m0, s47
	v_lshl_add_u64 v[224:225], s[30:31], 0, v[162:163]
	ds_read_b128 v[172:175], v188 offset:32768
	ds_read_b128 v[176:179], v188 offset:33792
	ds_read_b128 v[180:183], v188 offset:34816
	ds_read_b128 v[190:193], v188 offset:35840
	ds_read_b128 v[194:197], v188 offset:36864
	ds_read_b128 v[198:201], v188 offset:37888
	ds_read_b128 v[202:205], v188 offset:38912
	ds_read_b128 v[206:209], v188 offset:39936
	global_load_lds_dwordx4 v[224:225], off
	s_mov_b32 m0, s48
	v_lshl_add_u64 v[224:225], s[30:31], 0, v[160:161]
	global_load_lds_dwordx4 v[224:225], off
	s_waitcnt vmcnt(8)
	s_waitcnt lgkmcnt(0)
	s_barrier
	s_waitcnt lgkmcnt(0)
	v_mfma_f32_16x16x32_bf16 v[126:129], v[130:133], v[172:175], v[126:129]
	v_mfma_f32_16x16x32_bf16 v[122:125], v[138:141], v[172:175], v[122:125]
	v_mfma_f32_16x16x32_bf16 v[114:117], v[130:133], v[180:183], v[114:117]
	v_mfma_f32_16x16x32_bf16 v[106:109], v[138:141], v[180:183], v[106:109]
	v_mfma_f32_16x16x32_bf16 v[98:101], v[130:133], v[194:197], v[98:101]
	v_mfma_f32_16x16x32_bf16 v[90:93], v[138:141], v[194:197], v[90:93]
	v_mfma_f32_16x16x32_bf16 v[82:85], v[130:133], v[202:205], v[82:85]
	v_mfma_f32_16x16x32_bf16 v[74:77], v[138:141], v[202:205], v[74:77]
	v_mfma_f32_16x16x32_bf16 v[126:129], v[134:137], v[176:179], v[126:129]
	v_mfma_f32_16x16x32_bf16 v[122:125], v[142:145], v[176:179], v[122:125]
	v_mfma_f32_16x16x32_bf16 v[114:117], v[134:137], v[190:193], v[114:117]
	v_mfma_f32_16x16x32_bf16 v[106:109], v[142:145], v[190:193], v[106:109]
	v_mfma_f32_16x16x32_bf16 v[98:101], v[134:137], v[198:201], v[98:101]
	v_mfma_f32_16x16x32_bf16 v[90:93], v[142:145], v[198:201], v[90:93]
	v_mfma_f32_16x16x32_bf16 v[82:85], v[134:137], v[206:209], v[82:85]
	v_mfma_f32_16x16x32_bf16 v[74:77], v[142:145], v[206:209], v[74:77]
	v_mfma_f32_16x16x32_bf16 v[118:121], v[146:149], v[172:175], v[118:121]
	v_mfma_f32_16x16x32_bf16 v[110:113], v[154:157], v[172:175], v[110:113]
	v_mfma_f32_16x16x32_bf16 v[102:105], v[146:149], v[180:183], v[102:105]
	v_mfma_f32_16x16x32_bf16 v[94:97], v[154:157], v[180:183], v[94:97]
	v_mfma_f32_16x16x32_bf16 v[86:89], v[146:149], v[194:197], v[86:89]
	v_mfma_f32_16x16x32_bf16 v[78:81], v[154:157], v[194:197], v[78:81]
	v_mfma_f32_16x16x32_bf16 v[70:73], v[146:149], v[202:205], v[70:73]
	v_mfma_f32_16x16x32_bf16 v[66:69], v[154:157], v[202:205], v[66:69]
	v_mfma_f32_16x16x32_bf16 v[118:121], v[150:153], v[176:179], v[118:121]
	v_mfma_f32_16x16x32_bf16 v[110:113], v[168:171], v[176:179], v[110:113]
	v_mfma_f32_16x16x32_bf16 v[102:105], v[150:153], v[190:193], v[102:105]
	v_mfma_f32_16x16x32_bf16 v[94:97], v[168:171], v[190:193], v[94:97]
	v_mfma_f32_16x16x32_bf16 v[86:89], v[150:153], v[198:201], v[86:89]
	v_mfma_f32_16x16x32_bf16 v[78:81], v[168:171], v[198:201], v[78:81]
	v_mfma_f32_16x16x32_bf16 v[70:73], v[150:153], v[206:209], v[70:73]
	v_mfma_f32_16x16x32_bf16 v[66:69], v[168:171], v[206:209], v[66:69]
	s_barrier
	s_add_i32 s30, s43, s44
	v_lshl_add_u64 v[216:217], v[216:217], 0, s[56:57]
	s_mov_b32 m0, s30
	ds_read_b128 v[172:175], v188 offset:49152
	ds_read_b128 v[176:179], v188 offset:50176
	ds_read_b128 v[180:183], v188 offset:51200
	ds_read_b128 v[190:193], v188 offset:52224
	ds_read_b128 v[194:197], v188 offset:53248
	ds_read_b128 v[198:201], v188 offset:54272
	ds_read_b128 v[202:205], v188 offset:55296
	ds_read_b128 v[206:209], v188 offset:56320
	global_load_lds_dwordx4 v[216:217], off
	s_add_i32 m0, s30, 0x2000
	s_add_u32 s28, s28, 0x40080
	v_lshl_add_u64 v[216:217], v[218:219], 0, s[56:57]
	s_addc_u32 s29, s29, 0
	s_add_i32 s30, s58, s44
	global_load_lds_dwordx4 v[216:217], off
	s_mov_b32 m0, s30
	v_lshl_add_u64 v[216:217], s[28:29], 0, v[0:1]
	global_load_lds_dwordx4 v[216:217], off
	s_add_i32 m0, s30, 0x2000
	v_lshl_add_u64 v[216:217], s[28:29], 0, v[158:159]
	global_load_lds_dwordx4 v[216:217], off
	s_mov_b32 m0, s49
	v_lshl_add_u64 v[216:217], v[220:221], 0, s[56:57]
	global_load_lds_dwordx4 v[216:217], off
	s_mov_b32 m0, s52
	v_lshl_add_u64 v[216:217], v[222:223], 0, s[56:57]
	global_load_lds_dwordx4 v[216:217], off
	s_waitcnt vmcnt(8)
	s_waitcnt lgkmcnt(0)
	s_barrier
	s_waitcnt lgkmcnt(0)
	v_mfma_f32_16x16x32_bf16 v[62:65], v[130:133], v[172:175], v[62:65]
	v_mfma_f32_16x16x32_bf16 v[58:61], v[138:141], v[172:175], v[58:61]
	v_mfma_f32_16x16x32_bf16 v[50:53], v[130:133], v[180:183], v[50:53]
	v_mfma_f32_16x16x32_bf16 v[42:45], v[138:141], v[180:183], v[42:45]
	v_mfma_f32_16x16x32_bf16 v[34:37], v[130:133], v[194:197], v[34:37]
	v_mfma_f32_16x16x32_bf16 v[26:29], v[138:141], v[194:197], v[26:29]
	v_mfma_f32_16x16x32_bf16 v[18:21], v[130:133], v[202:205], v[18:21]
	v_mfma_f32_16x16x32_bf16 v[10:13], v[138:141], v[202:205], v[10:13]
	v_mfma_f32_16x16x32_bf16 v[62:65], v[134:137], v[176:179], v[62:65]
	v_mfma_f32_16x16x32_bf16 v[58:61], v[142:145], v[176:179], v[58:61]
	v_mfma_f32_16x16x32_bf16 v[50:53], v[134:137], v[190:193], v[50:53]
	v_mfma_f32_16x16x32_bf16 v[42:45], v[142:145], v[190:193], v[42:45]
	v_mfma_f32_16x16x32_bf16 v[34:37], v[134:137], v[198:201], v[34:37]
	v_mfma_f32_16x16x32_bf16 v[26:29], v[142:145], v[198:201], v[26:29]
	v_mfma_f32_16x16x32_bf16 v[18:21], v[134:137], v[206:209], v[18:21]
	v_mfma_f32_16x16x32_bf16 v[10:13], v[142:145], v[206:209], v[10:13]
	v_mfma_f32_16x16x32_bf16 v[54:57], v[146:149], v[172:175], v[54:57]
	v_mfma_f32_16x16x32_bf16 v[46:49], v[154:157], v[172:175], v[46:49]
	v_mfma_f32_16x16x32_bf16 v[38:41], v[146:149], v[180:183], v[38:41]
	v_mfma_f32_16x16x32_bf16 v[30:33], v[154:157], v[180:183], v[30:33]
	v_mfma_f32_16x16x32_bf16 v[22:25], v[146:149], v[194:197], v[22:25]
	v_mfma_f32_16x16x32_bf16 v[14:17], v[154:157], v[194:197], v[14:17]
	v_mfma_f32_16x16x32_bf16 v[6:9], v[146:149], v[202:205], v[6:9]
	v_mfma_f32_16x16x32_bf16 v[2:5], v[154:157], v[202:205], v[2:5]
	v_mfma_f32_16x16x32_bf16 v[54:57], v[150:153], v[176:179], v[54:57]
	v_mfma_f32_16x16x32_bf16 v[46:49], v[168:171], v[176:179], v[46:49]
	v_mfma_f32_16x16x32_bf16 v[38:41], v[150:153], v[190:193], v[38:41]
	v_mfma_f32_16x16x32_bf16 v[30:33], v[168:171], v[190:193], v[30:33]
	v_mfma_f32_16x16x32_bf16 v[22:25], v[150:153], v[198:201], v[22:25]
	v_mfma_f32_16x16x32_bf16 v[14:17], v[168:171], v[198:201], v[14:17]
	v_mfma_f32_16x16x32_bf16 v[6:9], v[150:153], v[206:209], v[6:9]
	v_mfma_f32_16x16x32_bf16 v[2:5], v[168:171], v[206:209], v[2:5]
	s_barrier
	s_add_i32 s42, s42, 2
	s_add_u32 s23, s23, 0x100
	s_addc_u32 s33, s33, 0
	s_add_u32 s6, s6, 0x100
	s_addc_u32 s7, s7, 0
	s_cmp_gt_u32 s42, 13
	s_cbranch_scc0 .LBB0_417
	s_and_b64 vcc, exec, s[18:19]
	s_cbranch_vccz .LBB0_420
	s_barrier

.LBB0_587:
	s_add_u32 s18, s34, s62
	s_addc_u32 s19, s35, s63
	s_add_u32 s18, s18, 0x100
	s_addc_u32 s19, s19, 0
	s_add_u32 s70, s8, s62
	s_addc_u32 s71, s9, s63
	s_add_i32 s26, 0, 0x10000
	s_cmpk_eq_i32 s62, 0x700
	s_cselect_b32 s77, s47, s19
	s_cselect_b32 s76, s59, s18
	s_cselect_b32 s71, s37, s71
	s_cselect_b32 s70, vcc_lo, s70
	s_add_i32 s27, 0, 0x14000
	v_add_u32_e32 v158, s26, v144
	v_add_u32_e32 v176, s27, v144
	ds_read_b128 v[146:149], v158
	ds_read_b128 v[150:153], v158 offset:1024
	ds_read_b128 v[154:157], v158 offset:2048
	ds_read_b128 v[158:161], v158 offset:3072
	ds_read_b128 v[162:165], v176
	ds_read_b128 v[168:171], v176 offset:1024
	ds_read_b128 v[172:175], v176 offset:2048
	ds_read_b128 v[176:179], v176 offset:3072
	v_lshl_add_u64 v[208:209], v[142:143], 0, s[62:63]
	s_add_i32 m0, s4, 0xc000
	ds_read_b128 v[180:183], v145
	ds_read_b128 v[184:187], v145 offset:1024
	ds_read_b128 v[188:191], v145 offset:2048
	ds_read_b128 v[192:195], v145 offset:3072
	ds_read_b128 v[196:199], v145 offset:4096
	ds_read_b128 v[200:203], v145 offset:5120
	ds_read_b128 v[204:207], v145 offset:6144
	ds_read_b128 v[216:219], v145 offset:7168
	global_load_lds_dwordx4 v[208:209], off
	s_add_i32 m0, s4, 0xe000
	v_lshl_add_u64 v[208:209], v[140:141], 0, s[62:63]
	global_load_lds_dwordx4 v[208:209], off
	s_waitcnt vmcnt(8)
	s_waitcnt lgkmcnt(0)
	s_barrier
	s_waitcnt lgkmcnt(0)
	v_mfma_f32_16x16x32_bf16 v[134:137], v[146:149], v[180:183], v[134:137]
	v_mfma_f32_16x16x32_bf16 v[130:133], v[154:157], v[180:183], v[130:133]
	v_mfma_f32_16x16x32_bf16 v[110:113], v[146:149], v[188:191], v[110:113]
	v_mfma_f32_16x16x32_bf16 v[106:109], v[154:157], v[188:191], v[106:109]
	v_mfma_f32_16x16x32_bf16 v[94:97], v[146:149], v[196:199], v[94:97]
	v_mfma_f32_16x16x32_bf16 v[90:93], v[154:157], v[196:199], v[90:93]
	v_mfma_f32_16x16x32_bf16 v[78:81], v[146:149], v[204:207], v[78:81]
	v_mfma_f32_16x16x32_bf16 v[74:77], v[154:157], v[204:207], v[74:77]
	v_mfma_f32_16x16x32_bf16 v[134:137], v[150:153], v[184:187], v[134:137]
	v_mfma_f32_16x16x32_bf16 v[130:133], v[158:161], v[184:187], v[130:133]
	v_mfma_f32_16x16x32_bf16 v[110:113], v[150:153], v[192:195], v[110:113]
	v_mfma_f32_16x16x32_bf16 v[106:109], v[158:161], v[192:195], v[106:109]
	v_mfma_f32_16x16x32_bf16 v[94:97], v[150:153], v[200:203], v[94:97]
	v_mfma_f32_16x16x32_bf16 v[90:93], v[158:161], v[200:203], v[90:93]
	v_mfma_f32_16x16x32_bf16 v[78:81], v[150:153], v[216:219], v[78:81]
	v_mfma_f32_16x16x32_bf16 v[74:77], v[158:161], v[216:219], v[74:77]
	v_mfma_f32_16x16x32_bf16 v[122:125], v[162:165], v[180:183], v[122:125]
	v_mfma_f32_16x16x32_bf16 v[114:117], v[172:175], v[180:183], v[114:117]
	v_mfma_f32_16x16x32_bf16 v[102:105], v[162:165], v[188:191], v[102:105]
	v_mfma_f32_16x16x32_bf16 v[98:101], v[172:175], v[188:191], v[98:101]
	v_mfma_f32_16x16x32_bf16 v[86:89], v[162:165], v[196:199], v[86:89]
	v_mfma_f32_16x16x32_bf16 v[82:85], v[172:175], v[196:199], v[82:85]
	v_mfma_f32_16x16x32_bf16 v[70:73], v[162:165], v[204:207], v[70:73]
	v_mfma_f32_16x16x32_bf16 v[66:69], v[172:175], v[204:207], v[66:69]
	v_mfma_f32_16x16x32_bf16 v[122:125], v[168:171], v[184:187], v[122:125]
	v_mfma_f32_16x16x32_bf16 v[114:117], v[176:179], v[184:187], v[114:117]
	v_mfma_f32_16x16x32_bf16 v[102:105], v[168:171], v[192:195], v[102:105]
	v_mfma_f32_16x16x32_bf16 v[98:101], v[176:179], v[192:195], v[98:101]
	v_mfma_f32_16x16x32_bf16 v[86:89], v[168:171], v[200:203], v[86:89]
	v_mfma_f32_16x16x32_bf16 v[82:85], v[176:179], v[200:203], v[82:85]
	v_mfma_f32_16x16x32_bf16 v[70:73], v[168:171], v[216:219], v[70:73]
	v_mfma_f32_16x16x32_bf16 v[66:69], v[176:179], v[216:219], v[66:69]
	s_barrier
	s_add_i32 s18, s26, s84
	v_lshl_add_u64 v[208:209], s[70:71], 0, v[0:1]
	s_mov_b32 m0, s18
	ds_read_b128 v[180:183], v145 offset:16384
	ds_read_b128 v[184:187], v145 offset:17408
	ds_read_b128 v[188:191], v145 offset:18432
	ds_read_b128 v[192:195], v145 offset:19456
	ds_read_b128 v[196:199], v145 offset:20480
	ds_read_b128 v[200:203], v145 offset:21504
	ds_read_b128 v[204:207], v145 offset:22528
	ds_read_b128 v[216:219], v145 offset:23552
	global_load_lds_dwordx4 v[208:209], off
	s_add_i32 m0, s18, 0x2000
	s_add_u32 s18, s70, 0x40000
	v_lshl_add_u64 v[220:221], s[70:71], 0, v[118:119]
	s_addc_u32 s19, s71, 0
	s_add_i32 s26, s27, s84
	global_load_lds_dwordx4 v[220:221], off
	v_lshl_add_u64 v[222:223], s[18:19], 0, v[0:1]
	s_mov_b32 m0, s26
	v_lshl_add_u64 v[224:225], s[76:77], 0, v[120:121]
	global_load_lds_dwordx4 v[222:223], off
	s_add_i32 m0, s26, 0x2000
	v_lshl_add_u64 v[222:223], s[18:19], 0, v[118:119]
	global_load_lds_dwordx4 v[222:223], off
	s_mov_b32 m0, s4
	v_lshl_add_u64 v[222:223], s[76:77], 0, v[126:127]
	global_load_lds_dwordx4 v[222:223], off
	s_mov_b32 m0, s5
	s_nop 0
	global_load_lds_dwordx4 v[224:225], off
	s_waitcnt vmcnt(8)
	s_waitcnt lgkmcnt(0)
	s_barrier
	s_waitcnt lgkmcnt(0)
	v_mfma_f32_16x16x32_bf16 v[62:65], v[146:149], v[180:183], v[62:65]
	v_mfma_f32_16x16x32_bf16 v[58:61], v[154:157], v[180:183], v[58:61]
	v_mfma_f32_16x16x32_bf16 v[46:49], v[146:149], v[188:191], v[46:49]
	v_mfma_f32_16x16x32_bf16 v[42:45], v[154:157], v[188:191], v[42:45]
	v_mfma_f32_16x16x32_bf16 v[30:33], v[146:149], v[196:199], v[30:33]
	v_mfma_f32_16x16x32_bf16 v[26:29], v[154:157], v[196:199], v[26:29]
	v_mfma_f32_16x16x32_bf16 v[14:17], v[146:149], v[204:207], v[14:17]
	v_mfma_f32_16x16x32_bf16 v[10:13], v[154:157], v[204:207], v[10:13]
	v_mfma_f32_16x16x32_bf16 v[62:65], v[150:153], v[184:187], v[62:65]
	v_mfma_f32_16x16x32_bf16 v[58:61], v[158:161], v[184:187], v[58:61]
	v_mfma_f32_16x16x32_bf16 v[46:49], v[150:153], v[192:195], v[46:49]
	v_mfma_f32_16x16x32_bf16 v[42:45], v[158:161], v[192:195], v[42:45]
	v_mfma_f32_16x16x32_bf16 v[30:33], v[150:153], v[200:203], v[30:33]
	v_mfma_f32_16x16x32_bf16 v[26:29], v[158:161], v[200:203], v[26:29]
	v_mfma_f32_16x16x32_bf16 v[14:17], v[150:153], v[216:219], v[14:17]
	v_mfma_f32_16x16x32_bf16 v[10:13], v[158:161], v[216:219], v[10:13]
	v_mfma_f32_16x16x32_bf16 v[54:57], v[162:165], v[180:183], v[54:57]
	v_mfma_f32_16x16x32_bf16 v[50:53], v[172:175], v[180:183], v[50:53]
	v_mfma_f32_16x16x32_bf16 v[38:41], v[162:165], v[188:191], v[38:41]
	v_mfma_f32_16x16x32_bf16 v[34:37], v[172:175], v[188:191], v[34:37]
	v_mfma_f32_16x16x32_bf16 v[22:25], v[162:165], v[196:199], v[22:25]
	v_mfma_f32_16x16x32_bf16 v[18:21], v[172:175], v[196:199], v[18:21]
	v_mfma_f32_16x16x32_bf16 v[6:9], v[162:165], v[204:207], v[6:9]
	v_mfma_f32_16x16x32_bf16 v[2:5], v[172:175], v[204:207], v[2:5]
	v_mfma_f32_16x16x32_bf16 v[54:57], v[168:171], v[184:187], v[54:57]
	v_mfma_f32_16x16x32_bf16 v[50:53], v[176:179], v[184:187], v[50:53]
	v_mfma_f32_16x16x32_bf16 v[38:41], v[168:171], v[192:195], v[38:41]
	v_mfma_f32_16x16x32_bf16 v[34:37], v[176:179], v[192:195], v[34:37]
	v_mfma_f32_16x16x32_bf16 v[22:25], v[168:171], v[200:203], v[22:25]
	v_mfma_f32_16x16x32_bf16 v[18:21], v[176:179], v[200:203], v[18:21]
	v_mfma_f32_16x16x32_bf16 v[6:9], v[168:171], v[216:219], v[6:9]
	v_mfma_f32_16x16x32_bf16 v[2:5], v[176:179], v[216:219], v[2:5]
	s_barrier
	s_add_i32 s26, 0, 0x18000
	s_add_i32 s27, 0, 0x1c000
	v_add_u32_e32 v158, s26, v144
	v_add_u32_e32 v176, s27, v144
	ds_read_b128 v[146:149], v158
	ds_read_b128 v[150:153], v158 offset:1024
	ds_read_b128 v[154:157], v158 offset:2048
	ds_read_b128 v[158:161], v158 offset:3072
	ds_read_b128 v[162:165], v176
	ds_read_b128 v[168:171], v176 offset:1024
	ds_read_b128 v[172:175], v176 offset:2048
	ds_read_b128 v[176:179], v176 offset:3072
	s_add_u32 s18, s76, 0x40000
	s_addc_u32 s19, s77, 0
	s_mov_b32 m0, s33
	v_lshl_add_u64 v[242:243], s[18:19], 0, v[126:127]
	ds_read_b128 v[180:183], v145 offset:32768
	ds_read_b128 v[184:187], v145 offset:33792
	ds_read_b128 v[188:191], v145 offset:34816
	ds_read_b128 v[192:195], v145 offset:35840
	ds_read_b128 v[196:199], v145 offset:36864
	ds_read_b128 v[200:203], v145 offset:37888
	ds_read_b128 v[204:207], v145 offset:38912
	ds_read_b128 v[216:219], v145 offset:39936
	global_load_lds_dwordx4 v[242:243], off
	s_mov_b32 m0, s92
	v_lshl_add_u64 v[242:243], s[18:19], 0, v[120:121]
	global_load_lds_dwordx4 v[242:243], off
	s_waitcnt vmcnt(8)
	s_waitcnt lgkmcnt(0)
	s_barrier
	s_waitcnt lgkmcnt(0)
	v_mfma_f32_16x16x32_bf16 v[134:137], v[146:149], v[180:183], v[134:137]
	v_mfma_f32_16x16x32_bf16 v[130:133], v[154:157], v[180:183], v[130:133]
	v_mfma_f32_16x16x32_bf16 v[110:113], v[146:149], v[188:191], v[110:113]
	v_mfma_f32_16x16x32_bf16 v[106:109], v[154:157], v[188:191], v[106:109]
	v_mfma_f32_16x16x32_bf16 v[94:97], v[146:149], v[196:199], v[94:97]
	v_mfma_f32_16x16x32_bf16 v[90:93], v[154:157], v[196:199], v[90:93]
	v_mfma_f32_16x16x32_bf16 v[78:81], v[146:149], v[204:207], v[78:81]
	v_mfma_f32_16x16x32_bf16 v[74:77], v[154:157], v[204:207], v[74:77]
	v_mfma_f32_16x16x32_bf16 v[134:137], v[150:153], v[184:187], v[134:137]
	v_mfma_f32_16x16x32_bf16 v[130:133], v[158:161], v[184:187], v[130:133]
	v_mfma_f32_16x16x32_bf16 v[110:113], v[150:153], v[192:195], v[110:113]
	v_mfma_f32_16x16x32_bf16 v[106:109], v[158:161], v[192:195], v[106:109]
	v_mfma_f32_16x16x32_bf16 v[94:97], v[150:153], v[200:203], v[94:97]
	v_mfma_f32_16x16x32_bf16 v[90:93], v[158:161], v[200:203], v[90:93]
	v_mfma_f32_16x16x32_bf16 v[78:81], v[150:153], v[216:219], v[78:81]
	v_mfma_f32_16x16x32_bf16 v[74:77], v[158:161], v[216:219], v[74:77]
	v_mfma_f32_16x16x32_bf16 v[122:125], v[162:165], v[180:183], v[122:125]
	v_mfma_f32_16x16x32_bf16 v[114:117], v[172:175], v[180:183], v[114:117]
	v_mfma_f32_16x16x32_bf16 v[102:105], v[162:165], v[188:191], v[102:105]
	v_mfma_f32_16x16x32_bf16 v[98:101], v[172:175], v[188:191], v[98:101]
	v_mfma_f32_16x16x32_bf16 v[86:89], v[162:165], v[196:199], v[86:89]
	v_mfma_f32_16x16x32_bf16 v[82:85], v[172:175], v[196:199], v[82:85]
	v_mfma_f32_16x16x32_bf16 v[70:73], v[162:165], v[204:207], v[70:73]
	v_mfma_f32_16x16x32_bf16 v[66:69], v[172:175], v[204:207], v[66:69]
	v_mfma_f32_16x16x32_bf16 v[122:125], v[168:171], v[184:187], v[122:125]
	v_mfma_f32_16x16x32_bf16 v[114:117], v[176:179], v[184:187], v[114:117]
	v_mfma_f32_16x16x32_bf16 v[102:105], v[168:171], v[192:195], v[102:105]
	v_mfma_f32_16x16x32_bf16 v[98:101], v[176:179], v[192:195], v[98:101]
	v_mfma_f32_16x16x32_bf16 v[86:89], v[168:171], v[200:203], v[86:89]
	v_mfma_f32_16x16x32_bf16 v[82:85], v[176:179], v[200:203], v[82:85]
	v_mfma_f32_16x16x32_bf16 v[70:73], v[168:171], v[216:219], v[70:73]
	v_mfma_f32_16x16x32_bf16 v[66:69], v[176:179], v[216:219], v[66:69]
	s_barrier
	s_add_i32 s18, s26, s84
	v_lshl_add_u64 v[208:209], v[208:209], 0, s[56:57]
	s_mov_b32 m0, s18
	ds_read_b128 v[180:183], v145 offset:49152
	ds_read_b128 v[184:187], v145 offset:50176
	ds_read_b128 v[188:191], v145 offset:51200
	ds_read_b128 v[192:195], v145 offset:52224
	ds_read_b128 v[196:199], v145 offset:53248
	ds_read_b128 v[200:203], v145 offset:54272
	ds_read_b128 v[204:207], v145 offset:55296
	ds_read_b128 v[216:219], v145 offset:56320
	global_load_lds_dwordx4 v[208:209], off
	s_add_i32 m0, s18, 0x2000
	s_add_u32 s18, s70, 0x40080
	v_lshl_add_u64 v[208:209], v[220:221], 0, s[56:57]
	s_addc_u32 s19, s71, 0
	s_add_i32 s26, s27, s84
	global_load_lds_dwordx4 v[208:209], off
	s_mov_b32 m0, s26
	v_lshl_add_u64 v[208:209], s[18:19], 0, v[0:1]
	global_load_lds_dwordx4 v[208:209], off
	s_add_i32 m0, s26, 0x2000
	v_lshl_add_u64 v[208:209], s[18:19], 0, v[118:119]
	global_load_lds_dwordx4 v[208:209], off
	s_mov_b32 m0, s90
	v_lshl_add_u64 v[208:209], v[222:223], 0, s[56:57]
	global_load_lds_dwordx4 v[208:209], off
	s_mov_b32 m0, s96
	v_lshl_add_u64 v[208:209], v[224:225], 0, s[56:57]
	global_load_lds_dwordx4 v[208:209], off
	s_waitcnt vmcnt(8)
	s_waitcnt lgkmcnt(0)
	s_barrier
	s_waitcnt lgkmcnt(0)
	v_mfma_f32_16x16x32_bf16 v[62:65], v[146:149], v[180:183], v[62:65]
	v_mfma_f32_16x16x32_bf16 v[58:61], v[154:157], v[180:183], v[58:61]
	v_mfma_f32_16x16x32_bf16 v[46:49], v[146:149], v[188:191], v[46:49]
	v_mfma_f32_16x16x32_bf16 v[42:45], v[154:157], v[188:191], v[42:45]
	v_mfma_f32_16x16x32_bf16 v[30:33], v[146:149], v[196:199], v[30:33]
	v_mfma_f32_16x16x32_bf16 v[26:29], v[154:157], v[196:199], v[26:29]
	v_mfma_f32_16x16x32_bf16 v[14:17], v[146:149], v[204:207], v[14:17]
	v_mfma_f32_16x16x32_bf16 v[10:13], v[154:157], v[204:207], v[10:13]
	v_mfma_f32_16x16x32_bf16 v[62:65], v[150:153], v[184:187], v[62:65]
	v_mfma_f32_16x16x32_bf16 v[58:61], v[158:161], v[184:187], v[58:61]
	v_mfma_f32_16x16x32_bf16 v[46:49], v[150:153], v[192:195], v[46:49]
	v_mfma_f32_16x16x32_bf16 v[42:45], v[158:161], v[192:195], v[42:45]
	v_mfma_f32_16x16x32_bf16 v[30:33], v[150:153], v[200:203], v[30:33]
	v_mfma_f32_16x16x32_bf16 v[26:29], v[158:161], v[200:203], v[26:29]
	v_mfma_f32_16x16x32_bf16 v[14:17], v[150:153], v[216:219], v[14:17]
	v_mfma_f32_16x16x32_bf16 v[10:13], v[158:161], v[216:219], v[10:13]
	v_mfma_f32_16x16x32_bf16 v[54:57], v[162:165], v[180:183], v[54:57]
	v_mfma_f32_16x16x32_bf16 v[50:53], v[172:175], v[180:183], v[50:53]
	v_mfma_f32_16x16x32_bf16 v[38:41], v[162:165], v[188:191], v[38:41]
	v_mfma_f32_16x16x32_bf16 v[34:37], v[172:175], v[188:191], v[34:37]
	v_mfma_f32_16x16x32_bf16 v[22:25], v[162:165], v[196:199], v[22:25]
	v_mfma_f32_16x16x32_bf16 v[18:21], v[172:175], v[196:199], v[18:21]
	v_mfma_f32_16x16x32_bf16 v[6:9], v[162:165], v[204:207], v[6:9]
	v_mfma_f32_16x16x32_bf16 v[2:5], v[172:175], v[204:207], v[2:5]
	v_mfma_f32_16x16x32_bf16 v[54:57], v[168:171], v[184:187], v[54:57]
	v_mfma_f32_16x16x32_bf16 v[50:53], v[176:179], v[184:187], v[50:53]
	v_mfma_f32_16x16x32_bf16 v[38:41], v[168:171], v[192:195], v[38:41]
	v_mfma_f32_16x16x32_bf16 v[34:37], v[176:179], v[192:195], v[34:37]
	v_mfma_f32_16x16x32_bf16 v[22:25], v[168:171], v[200:203], v[22:25]
	v_mfma_f32_16x16x32_bf16 v[18:21], v[176:179], v[200:203], v[18:21]
	v_mfma_f32_16x16x32_bf16 v[6:9], v[168:171], v[216:219], v[6:9]
	v_mfma_f32_16x16x32_bf16 v[2:5], v[176:179], v[216:219], v[2:5]
	s_barrier
	s_add_i32 vcc_hi, vcc_hi, 2
	s_add_u32 s62, s62, 0x100
	s_addc_u32 s63, s63, 0
	s_cmp_gt_u32 vcc_hi, 13
	s_cbranch_scc0 .LBB0_587
	s_add_u32 s62, s8, 0xffffff00
	s_addc_u32 s63, s9, -1
	s_andn2_b64 vcc, exec, s[44:45]
	s_cbranch_vccnz .LBB0_590
	v_mov_b32_e32 v2, 0
	s_mov_b32 s20, s36
	s_mov_b32 s83, s46
	s_mov_b64 s[34:35], s[52:53]
	s_mov_b32 s68, s58
	v_mov_b32_e32 v3, v2
	v_mov_b32_e32 v4, v2
	v_mov_b32_e32 v5, v2
	v_mov_b32_e32 v6, v2
	v_mov_b32_e32 v7, v2
	v_mov_b32_e32 v8, v2
	v_mov_b32_e32 v9, v2
	v_mov_b32_e32 v18, v2
	v_mov_b32_e32 v19, v2
	v_mov_b32_e32 v20, v2
	v_mov_b32_e32 v21, v2
	v_mov_b32_e32 v22, v2
	v_mov_b32_e32 v23, v2
	v_mov_b32_e32 v24, v2
	v_mov_b32_e32 v25, v2
	v_mov_b32_e32 v34, v2
	v_mov_b32_e32 v35, v2
	v_mov_b32_e32 v36, v2
	v_mov_b32_e32 v37, v2
	v_mov_b32_e32 v38, v2
	v_mov_b32_e32 v39, v2
	v_mov_b32_e32 v40, v2
	v_mov_b32_e32 v41, v2
	v_mov_b32_e32 v50, v2
	v_mov_b32_e32 v51, v2
	v_mov_b32_e32 v52, v2
	v_mov_b32_e32 v53, v2
	v_mov_b32_e32 v54, v2
	v_mov_b32_e32 v55, v2
	v_mov_b32_e32 v56, v2
	v_mov_b32_e32 v57, v2
	v_mov_b32_e32 v10, v2
	v_mov_b32_e32 v11, v2
	v_mov_b32_e32 v12, v2
	v_mov_b32_e32 v13, v2
	v_mov_b32_e32 v14, v2
	v_mov_b32_e32 v15, v2
	v_mov_b32_e32 v16, v2
	v_mov_b32_e32 v17, v2
	v_mov_b32_e32 v26, v2
	v_mov_b32_e32 v27, v2
	v_mov_b32_e32 v28, v2
	v_mov_b32_e32 v29, v2
	v_mov_b32_e32 v30, v2
	v_mov_b32_e32 v31, v2
	v_mov_b32_e32 v32, v2
	v_mov_b32_e32 v33, v2
	v_mov_b32_e32 v42, v2
	v_mov_b32_e32 v43, v2
	v_mov_b32_e32 v44, v2
	v_mov_b32_e32 v45, v2
	v_mov_b32_e32 v46, v2
	v_mov_b32_e32 v47, v2
	v_mov_b32_e32 v48, v2
	v_mov_b32_e32 v49, v2
	v_mov_b32_e32 v58, v2
	v_mov_b32_e32 v59, v2
	v_mov_b32_e32 v60, v2
	v_mov_b32_e32 v61, v2
	v_mov_b32_e32 v62, v2
	v_mov_b32_e32 v63, v2
	v_mov_b32_e32 v64, v2
	v_mov_b32_e32 v65, v2
	v_mov_b32_e32 v66, v2
	v_mov_b32_e32 v67, v2
	v_mov_b32_e32 v68, v2
	v_mov_b32_e32 v69, v2
	v_mov_b32_e32 v70, v2
	v_mov_b32_e32 v71, v2
	v_mov_b32_e32 v72, v2
	v_mov_b32_e32 v73, v2
	v_mov_b32_e32 v82, v2
	v_mov_b32_e32 v83, v2
	v_mov_b32_e32 v84, v2
	v_mov_b32_e32 v85, v2
	v_mov_b32_e32 v86, v2
	v_mov_b32_e32 v87, v2
	v_mov_b32_e32 v88, v2
	v_mov_b32_e32 v89, v2
	v_mov_b32_e32 v98, v2
	v_mov_b32_e32 v99, v2
	v_mov_b32_e32 v100, v2
	v_mov_b32_e32 v101, v2
	v_mov_b32_e32 v102, v2
	v_mov_b32_e32 v103, v2
	v_mov_b32_e32 v104, v2
	v_mov_b32_e32 v105, v2
	v_mov_b32_e32 v114, v2
	v_mov_b32_e32 v115, v2
	v_mov_b32_e32 v116, v2
	v_mov_b32_e32 v117, v2
	v_mov_b32_e32 v122, v2
	v_mov_b32_e32 v123, v2
	v_mov_b32_e32 v124, v2
	v_mov_b32_e32 v125, v2
	v_mov_b32_e32 v74, v2
	v_mov_b32_e32 v75, v2
	v_mov_b32_e32 v76, v2
	v_mov_b32_e32 v77, v2
	v_mov_b32_e32 v78, v2
	v_mov_b32_e32 v79, v2
	v_mov_b32_e32 v80, v2
	v_mov_b32_e32 v81, v2
	v_mov_b32_e32 v90, v2
	v_mov_b32_e32 v91, v2
	v_mov_b32_e32 v92, v2
	v_mov_b32_e32 v93, v2
	v_mov_b32_e32 v94, v2
	v_mov_b32_e32 v95, v2
	v_mov_b32_e32 v96, v2
	v_mov_b32_e32 v97, v2
	v_mov_b32_e32 v106, v2
	v_mov_b32_e32 v107, v2
	v_mov_b32_e32 v108, v2
	v_mov_b32_e32 v109, v2
	v_mov_b32_e32 v110, v2
	v_mov_b32_e32 v111, v2
	v_mov_b32_e32 v112, v2
	v_mov_b32_e32 v113, v2
	v_mov_b32_e32 v130, v2
	v_mov_b32_e32 v131, v2
	v_mov_b32_e32 v132, v2
	v_mov_b32_e32 v133, v2
	v_mov_b32_e32 v134, v2
	v_mov_b32_e32 v135, v2
	v_mov_b32_e32 v136, v2
	v_mov_b32_e32 v137, v2
	s_andn2_b64 vcc, exec, s[42:43]
	s_cbranch_vccnz .LBB0_591
	s_branch .LBB0_592

.LBB0_684:
	s_add_u32 s52, s30, s48
	s_addc_u32 s53, s31, s49
	s_add_u32 s52, s52, 0x100
	s_addc_u32 s53, s53, 0
	s_add_u32 s95, s8, s48
	s_addc_u32 s96, s9, s49
	s_add_i32 vcc_lo, 0, 0x10000
	s_cmpk_eq_i32 s48, 0x700
	s_cselect_b32 s63, s37, s53
	s_cselect_b32 s62, s59, s52
	s_cselect_b32 s53, s35, s96
	s_cselect_b32 s52, s93, s95
	s_add_i32 s95, 0, 0x14000
	v_add_u32_e32 v158, vcc_lo, v144
	v_add_u32_e32 v167, s95, v144
	ds_read_b128 v[146:149], v158
	ds_read_b128 v[150:153], v158 offset:1024
	ds_read_b128 v[154:157], v158 offset:2048
	ds_read_b128 v[158:161], v158 offset:3072
	ds_read_b128 v[162:165], v167
	ds_read_b128 v[168:171], v167 offset:1024
	ds_read_b128 v[172:175], v167 offset:2048
	ds_read_b128 v[176:179], v167 offset:3072
	v_lshl_add_u64 v[208:209], v[142:143], 0, s[48:49]
	s_add_i32 m0, s4, 0xc000
	ds_read_b128 v[180:183], v145
	ds_read_b128 v[184:187], v145 offset:1024
	ds_read_b128 v[188:191], v145 offset:2048
	ds_read_b128 v[192:195], v145 offset:3072
	ds_read_b128 v[196:199], v145 offset:4096
	ds_read_b128 v[200:203], v145 offset:5120
	ds_read_b128 v[204:207], v145 offset:6144
	ds_read_b128 v[216:219], v145 offset:7168
	global_load_lds_dwordx4 v[208:209], off
	s_add_i32 m0, s4, 0xe000
	v_lshl_add_u64 v[208:209], v[140:141], 0, s[48:49]
	global_load_lds_dwordx4 v[208:209], off
	s_waitcnt vmcnt(8)
	s_waitcnt lgkmcnt(0)
	s_barrier
	s_waitcnt lgkmcnt(0)
	v_mfma_f32_16x16x32_bf16 v[134:137], v[146:149], v[180:183], v[134:137]
	v_mfma_f32_16x16x32_bf16 v[130:133], v[154:157], v[180:183], v[130:133]
	v_mfma_f32_16x16x32_bf16 v[110:113], v[146:149], v[188:191], v[110:113]
	v_mfma_f32_16x16x32_bf16 v[106:109], v[154:157], v[188:191], v[106:109]
	v_mfma_f32_16x16x32_bf16 v[94:97], v[146:149], v[196:199], v[94:97]
	v_mfma_f32_16x16x32_bf16 v[90:93], v[154:157], v[196:199], v[90:93]
	v_mfma_f32_16x16x32_bf16 v[78:81], v[146:149], v[204:207], v[78:81]
	v_mfma_f32_16x16x32_bf16 v[74:77], v[154:157], v[204:207], v[74:77]
	v_mfma_f32_16x16x32_bf16 v[134:137], v[150:153], v[184:187], v[134:137]
	v_mfma_f32_16x16x32_bf16 v[130:133], v[158:161], v[184:187], v[130:133]
	v_mfma_f32_16x16x32_bf16 v[110:113], v[150:153], v[192:195], v[110:113]
	v_mfma_f32_16x16x32_bf16 v[106:109], v[158:161], v[192:195], v[106:109]
	v_mfma_f32_16x16x32_bf16 v[94:97], v[150:153], v[200:203], v[94:97]
	v_mfma_f32_16x16x32_bf16 v[90:93], v[158:161], v[200:203], v[90:93]
	v_mfma_f32_16x16x32_bf16 v[78:81], v[150:153], v[216:219], v[78:81]
	v_mfma_f32_16x16x32_bf16 v[74:77], v[158:161], v[216:219], v[74:77]
	v_mfma_f32_16x16x32_bf16 v[122:125], v[162:165], v[180:183], v[122:125]
	v_mfma_f32_16x16x32_bf16 v[114:117], v[172:175], v[180:183], v[114:117]
	v_mfma_f32_16x16x32_bf16 v[102:105], v[162:165], v[188:191], v[102:105]
	v_mfma_f32_16x16x32_bf16 v[98:101], v[172:175], v[188:191], v[98:101]
	v_mfma_f32_16x16x32_bf16 v[86:89], v[162:165], v[196:199], v[86:89]
	v_mfma_f32_16x16x32_bf16 v[82:85], v[172:175], v[196:199], v[82:85]
	v_mfma_f32_16x16x32_bf16 v[70:73], v[162:165], v[204:207], v[70:73]
	v_mfma_f32_16x16x32_bf16 v[66:69], v[172:175], v[204:207], v[66:69]
	v_mfma_f32_16x16x32_bf16 v[122:125], v[168:171], v[184:187], v[122:125]
	v_mfma_f32_16x16x32_bf16 v[114:117], v[176:179], v[184:187], v[114:117]
	v_mfma_f32_16x16x32_bf16 v[102:105], v[168:171], v[192:195], v[102:105]
	v_mfma_f32_16x16x32_bf16 v[98:101], v[176:179], v[192:195], v[98:101]
	v_mfma_f32_16x16x32_bf16 v[86:89], v[168:171], v[200:203], v[86:89]
	v_mfma_f32_16x16x32_bf16 v[82:85], v[176:179], v[200:203], v[82:85]
	v_mfma_f32_16x16x32_bf16 v[70:73], v[168:171], v[216:219], v[70:73]
	v_mfma_f32_16x16x32_bf16 v[66:69], v[176:179], v[216:219], v[66:69]
	s_barrier
	s_add_i32 s96, vcc_lo, s77
	v_lshl_add_u64 v[208:209], s[52:53], 0, v[0:1]
	s_mov_b32 m0, s96
	ds_read_b128 v[180:183], v145 offset:16384
	ds_read_b128 v[184:187], v145 offset:17408
	ds_read_b128 v[188:191], v145 offset:18432
	ds_read_b128 v[192:195], v145 offset:19456
	ds_read_b128 v[196:199], v145 offset:20480
	ds_read_b128 v[200:203], v145 offset:21504
	ds_read_b128 v[204:207], v145 offset:22528
	ds_read_b128 v[216:219], v145 offset:23552
	global_load_lds_dwordx4 v[208:209], off
	s_add_i32 m0, s96, 0x2000
	s_add_u32 vcc_lo, s52, 0x40000
	v_lshl_add_u64 v[220:221], s[52:53], 0, v[118:119]
	s_addc_u32 vcc_hi, s53, 0
	s_add_i32 s95, s95, s77
	global_load_lds_dwordx4 v[220:221], off
	v_lshl_add_u64 v[222:223], vcc, 0, v[0:1]
	s_mov_b32 m0, s95
	v_lshl_add_u64 v[224:225], s[62:63], 0, v[120:121]
	global_load_lds_dwordx4 v[222:223], off
	s_add_i32 m0, s95, 0x2000
	v_lshl_add_u64 v[222:223], vcc, 0, v[118:119]
	global_load_lds_dwordx4 v[222:223], off
	s_mov_b32 m0, s4
	v_lshl_add_u64 v[222:223], s[62:63], 0, v[126:127]
	global_load_lds_dwordx4 v[222:223], off
	s_mov_b32 m0, s5
	s_nop 0
	global_load_lds_dwordx4 v[224:225], off
	s_waitcnt vmcnt(8)
	s_waitcnt lgkmcnt(0)
	s_barrier
	s_waitcnt lgkmcnt(0)
	v_mfma_f32_16x16x32_bf16 v[62:65], v[146:149], v[180:183], v[62:65]
	v_mfma_f32_16x16x32_bf16 v[58:61], v[154:157], v[180:183], v[58:61]
	v_mfma_f32_16x16x32_bf16 v[46:49], v[146:149], v[188:191], v[46:49]
	v_mfma_f32_16x16x32_bf16 v[42:45], v[154:157], v[188:191], v[42:45]
	v_mfma_f32_16x16x32_bf16 v[30:33], v[146:149], v[196:199], v[30:33]
	v_mfma_f32_16x16x32_bf16 v[26:29], v[154:157], v[196:199], v[26:29]
	v_mfma_f32_16x16x32_bf16 v[14:17], v[146:149], v[204:207], v[14:17]
	v_mfma_f32_16x16x32_bf16 v[10:13], v[154:157], v[204:207], v[10:13]
	v_mfma_f32_16x16x32_bf16 v[62:65], v[150:153], v[184:187], v[62:65]
	v_mfma_f32_16x16x32_bf16 v[58:61], v[158:161], v[184:187], v[58:61]
	v_mfma_f32_16x16x32_bf16 v[46:49], v[150:153], v[192:195], v[46:49]
	v_mfma_f32_16x16x32_bf16 v[42:45], v[158:161], v[192:195], v[42:45]
	v_mfma_f32_16x16x32_bf16 v[30:33], v[150:153], v[200:203], v[30:33]
	v_mfma_f32_16x16x32_bf16 v[26:29], v[158:161], v[200:203], v[26:29]
	v_mfma_f32_16x16x32_bf16 v[14:17], v[150:153], v[216:219], v[14:17]
	v_mfma_f32_16x16x32_bf16 v[10:13], v[158:161], v[216:219], v[10:13]
	v_mfma_f32_16x16x32_bf16 v[54:57], v[162:165], v[180:183], v[54:57]
	v_mfma_f32_16x16x32_bf16 v[50:53], v[172:175], v[180:183], v[50:53]
	v_mfma_f32_16x16x32_bf16 v[38:41], v[162:165], v[188:191], v[38:41]
	v_mfma_f32_16x16x32_bf16 v[34:37], v[172:175], v[188:191], v[34:37]
	v_mfma_f32_16x16x32_bf16 v[22:25], v[162:165], v[196:199], v[22:25]
	v_mfma_f32_16x16x32_bf16 v[18:21], v[172:175], v[196:199], v[18:21]
	v_mfma_f32_16x16x32_bf16 v[6:9], v[162:165], v[204:207], v[6:9]
	v_mfma_f32_16x16x32_bf16 v[2:5], v[172:175], v[204:207], v[2:5]
	v_mfma_f32_16x16x32_bf16 v[54:57], v[168:171], v[184:187], v[54:57]
	v_mfma_f32_16x16x32_bf16 v[50:53], v[176:179], v[184:187], v[50:53]
	v_mfma_f32_16x16x32_bf16 v[38:41], v[168:171], v[192:195], v[38:41]
	v_mfma_f32_16x16x32_bf16 v[34:37], v[176:179], v[192:195], v[34:37]
	v_mfma_f32_16x16x32_bf16 v[22:25], v[168:171], v[200:203], v[22:25]
	v_mfma_f32_16x16x32_bf16 v[18:21], v[176:179], v[200:203], v[18:21]
	v_mfma_f32_16x16x32_bf16 v[6:9], v[168:171], v[216:219], v[6:9]
	v_mfma_f32_16x16x32_bf16 v[2:5], v[176:179], v[216:219], v[2:5]
	s_barrier
	s_add_i32 s95, 0, 0x18000
	s_add_i32 s96, 0, 0x1c000
	v_add_u32_e32 v158, s95, v144
	v_add_u32_e32 v167, s96, v144
	ds_read_b128 v[146:149], v158
	ds_read_b128 v[150:153], v158 offset:1024
	ds_read_b128 v[154:157], v158 offset:2048
	ds_read_b128 v[158:161], v158 offset:3072
	ds_read_b128 v[162:165], v167
	ds_read_b128 v[168:171], v167 offset:1024
	ds_read_b128 v[172:175], v167 offset:2048
	ds_read_b128 v[176:179], v167 offset:3072
	s_add_u32 s62, s62, 0x40000
	s_addc_u32 s63, s63, 0
	s_mov_b32 m0, s33
	v_lshl_add_u64 v[242:243], s[62:63], 0, v[126:127]
	ds_read_b128 v[180:183], v145 offset:32768
	ds_read_b128 v[184:187], v145 offset:33792
	ds_read_b128 v[188:191], v145 offset:34816
	ds_read_b128 v[192:195], v145 offset:35840
	ds_read_b128 v[196:199], v145 offset:36864
	ds_read_b128 v[200:203], v145 offset:37888
	ds_read_b128 v[204:207], v145 offset:38912
	ds_read_b128 v[216:219], v145 offset:39936
	global_load_lds_dwordx4 v[242:243], off
	s_mov_b32 m0, s84
	v_lshl_add_u64 v[242:243], s[62:63], 0, v[120:121]
	global_load_lds_dwordx4 v[242:243], off
	s_waitcnt vmcnt(8)
	s_waitcnt lgkmcnt(0)
	s_barrier
	s_waitcnt lgkmcnt(0)
	v_mfma_f32_16x16x32_bf16 v[134:137], v[146:149], v[180:183], v[134:137]
	v_mfma_f32_16x16x32_bf16 v[130:133], v[154:157], v[180:183], v[130:133]
	v_mfma_f32_16x16x32_bf16 v[110:113], v[146:149], v[188:191], v[110:113]
	v_mfma_f32_16x16x32_bf16 v[106:109], v[154:157], v[188:191], v[106:109]
	v_mfma_f32_16x16x32_bf16 v[94:97], v[146:149], v[196:199], v[94:97]
	v_mfma_f32_16x16x32_bf16 v[90:93], v[154:157], v[196:199], v[90:93]
	v_mfma_f32_16x16x32_bf16 v[78:81], v[146:149], v[204:207], v[78:81]
	v_mfma_f32_16x16x32_bf16 v[74:77], v[154:157], v[204:207], v[74:77]
	v_mfma_f32_16x16x32_bf16 v[134:137], v[150:153], v[184:187], v[134:137]
	v_mfma_f32_16x16x32_bf16 v[130:133], v[158:161], v[184:187], v[130:133]
	v_mfma_f32_16x16x32_bf16 v[110:113], v[150:153], v[192:195], v[110:113]
	v_mfma_f32_16x16x32_bf16 v[106:109], v[158:161], v[192:195], v[106:109]
	v_mfma_f32_16x16x32_bf16 v[94:97], v[150:153], v[200:203], v[94:97]
	v_mfma_f32_16x16x32_bf16 v[90:93], v[158:161], v[200:203], v[90:93]
	v_mfma_f32_16x16x32_bf16 v[78:81], v[150:153], v[216:219], v[78:81]
	v_mfma_f32_16x16x32_bf16 v[74:77], v[158:161], v[216:219], v[74:77]
	v_mfma_f32_16x16x32_bf16 v[122:125], v[162:165], v[180:183], v[122:125]
	v_mfma_f32_16x16x32_bf16 v[114:117], v[172:175], v[180:183], v[114:117]
	v_mfma_f32_16x16x32_bf16 v[102:105], v[162:165], v[188:191], v[102:105]
	v_mfma_f32_16x16x32_bf16 v[98:101], v[172:175], v[188:191], v[98:101]
	v_mfma_f32_16x16x32_bf16 v[86:89], v[162:165], v[196:199], v[86:89]
	v_mfma_f32_16x16x32_bf16 v[82:85], v[172:175], v[196:199], v[82:85]
	v_mfma_f32_16x16x32_bf16 v[70:73], v[162:165], v[204:207], v[70:73]
	v_mfma_f32_16x16x32_bf16 v[66:69], v[172:175], v[204:207], v[66:69]
	v_mfma_f32_16x16x32_bf16 v[122:125], v[168:171], v[184:187], v[122:125]
	v_mfma_f32_16x16x32_bf16 v[114:117], v[176:179], v[184:187], v[114:117]
	v_mfma_f32_16x16x32_bf16 v[102:105], v[168:171], v[192:195], v[102:105]
	v_mfma_f32_16x16x32_bf16 v[98:101], v[176:179], v[192:195], v[98:101]
	v_mfma_f32_16x16x32_bf16 v[86:89], v[168:171], v[200:203], v[86:89]
	v_mfma_f32_16x16x32_bf16 v[82:85], v[176:179], v[200:203], v[82:85]
	v_mfma_f32_16x16x32_bf16 v[70:73], v[168:171], v[216:219], v[70:73]
	v_mfma_f32_16x16x32_bf16 v[66:69], v[176:179], v[216:219], v[66:69]
	s_barrier
	s_add_i32 s62, s95, s77
	v_lshl_add_u64 v[208:209], v[208:209], 0, s[56:57]
	s_mov_b32 m0, s62
	ds_read_b128 v[180:183], v145 offset:49152
	ds_read_b128 v[184:187], v145 offset:50176
	ds_read_b128 v[188:191], v145 offset:51200
	ds_read_b128 v[192:195], v145 offset:52224
	ds_read_b128 v[196:199], v145 offset:53248
	ds_read_b128 v[200:203], v145 offset:54272
	ds_read_b128 v[204:207], v145 offset:55296
	ds_read_b128 v[216:219], v145 offset:56320
	global_load_lds_dwordx4 v[208:209], off
	s_add_i32 m0, s62, 0x2000
	s_add_u32 s52, s52, 0x40080
	v_lshl_add_u64 v[208:209], v[220:221], 0, s[56:57]
	s_addc_u32 s53, s53, 0
	s_add_i32 s62, s96, s77
	global_load_lds_dwordx4 v[208:209], off
	s_mov_b32 m0, s62
	v_lshl_add_u64 v[208:209], s[52:53], 0, v[0:1]
	global_load_lds_dwordx4 v[208:209], off
	s_add_i32 m0, s62, 0x2000
	v_lshl_add_u64 v[208:209], s[52:53], 0, v[118:119]
	global_load_lds_dwordx4 v[208:209], off
	s_mov_b32 m0, s85
	v_lshl_add_u64 v[208:209], v[222:223], 0, s[56:57]
	global_load_lds_dwordx4 v[208:209], off
	s_mov_b32 m0, s90
	v_lshl_add_u64 v[208:209], v[224:225], 0, s[56:57]
	global_load_lds_dwordx4 v[208:209], off
	s_waitcnt vmcnt(8)
	s_waitcnt lgkmcnt(0)
	s_barrier
	s_waitcnt lgkmcnt(0)
	v_mfma_f32_16x16x32_bf16 v[62:65], v[146:149], v[180:183], v[62:65]
	v_mfma_f32_16x16x32_bf16 v[58:61], v[154:157], v[180:183], v[58:61]
	v_mfma_f32_16x16x32_bf16 v[46:49], v[146:149], v[188:191], v[46:49]
	v_mfma_f32_16x16x32_bf16 v[42:45], v[154:157], v[188:191], v[42:45]
	v_mfma_f32_16x16x32_bf16 v[30:33], v[146:149], v[196:199], v[30:33]
	v_mfma_f32_16x16x32_bf16 v[26:29], v[154:157], v[196:199], v[26:29]
	v_mfma_f32_16x16x32_bf16 v[14:17], v[146:149], v[204:207], v[14:17]
	v_mfma_f32_16x16x32_bf16 v[10:13], v[154:157], v[204:207], v[10:13]
	v_mfma_f32_16x16x32_bf16 v[62:65], v[150:153], v[184:187], v[62:65]
	v_mfma_f32_16x16x32_bf16 v[58:61], v[158:161], v[184:187], v[58:61]
	v_mfma_f32_16x16x32_bf16 v[46:49], v[150:153], v[192:195], v[46:49]
	v_mfma_f32_16x16x32_bf16 v[42:45], v[158:161], v[192:195], v[42:45]
	v_mfma_f32_16x16x32_bf16 v[30:33], v[150:153], v[200:203], v[30:33]
	v_mfma_f32_16x16x32_bf16 v[26:29], v[158:161], v[200:203], v[26:29]
	v_mfma_f32_16x16x32_bf16 v[14:17], v[150:153], v[216:219], v[14:17]
	v_mfma_f32_16x16x32_bf16 v[10:13], v[158:161], v[216:219], v[10:13]
	v_mfma_f32_16x16x32_bf16 v[54:57], v[162:165], v[180:183], v[54:57]
	v_mfma_f32_16x16x32_bf16 v[50:53], v[172:175], v[180:183], v[50:53]
	v_mfma_f32_16x16x32_bf16 v[38:41], v[162:165], v[188:191], v[38:41]
	v_mfma_f32_16x16x32_bf16 v[34:37], v[172:175], v[188:191], v[34:37]
	v_mfma_f32_16x16x32_bf16 v[22:25], v[162:165], v[196:199], v[22:25]
	v_mfma_f32_16x16x32_bf16 v[18:21], v[172:175], v[196:199], v[18:21]
	v_mfma_f32_16x16x32_bf16 v[6:9], v[162:165], v[204:207], v[6:9]
	v_mfma_f32_16x16x32_bf16 v[2:5], v[172:175], v[204:207], v[2:5]
	v_mfma_f32_16x16x32_bf16 v[54:57], v[168:171], v[184:187], v[54:57]
	v_mfma_f32_16x16x32_bf16 v[50:53], v[176:179], v[184:187], v[50:53]
	v_mfma_f32_16x16x32_bf16 v[38:41], v[168:171], v[192:195], v[38:41]
	v_mfma_f32_16x16x32_bf16 v[34:37], v[176:179], v[192:195], v[34:37]
	v_mfma_f32_16x16x32_bf16 v[22:25], v[168:171], v[200:203], v[22:25]
	v_mfma_f32_16x16x32_bf16 v[18:21], v[176:179], v[200:203], v[18:21]
	v_mfma_f32_16x16x32_bf16 v[6:9], v[168:171], v[216:219], v[6:9]
	v_mfma_f32_16x16x32_bf16 v[2:5], v[176:179], v[216:219], v[2:5]
	s_barrier
	s_add_i32 s94, s94, 2
	s_add_u32 s48, s48, 0x100
	s_addc_u32 s49, s49, 0
	s_cmp_gt_u32 s94, 13
	s_cbranch_scc0 .LBB0_684
	s_add_u32 s48, s8, 0xffffff00
	s_addc_u32 s49, s9, -1
	s_andn2_b64 vcc, exec, s[42:43]
	s_cbranch_vccnz .LBB0_687
	v_mov_b32_e32 v2, 0
	s_mov_b32 s18, s34
	s_mov_b32 s92, s36
	s_mov_b64 s[30:31], s[46:47]
	s_mov_b32 s68, s58
	v_mov_b32_e32 v3, v2
	v_mov_b32_e32 v4, v2
	v_mov_b32_e32 v5, v2
	v_mov_b32_e32 v6, v2
	v_mov_b32_e32 v7, v2
	v_mov_b32_e32 v8, v2
	v_mov_b32_e32 v9, v2
	v_mov_b32_e32 v18, v2
	v_mov_b32_e32 v19, v2
	v_mov_b32_e32 v20, v2
	v_mov_b32_e32 v21, v2
	v_mov_b32_e32 v22, v2
	v_mov_b32_e32 v23, v2
	v_mov_b32_e32 v24, v2
	v_mov_b32_e32 v25, v2
	v_mov_b32_e32 v34, v2
	v_mov_b32_e32 v35, v2
	v_mov_b32_e32 v36, v2
	v_mov_b32_e32 v37, v2
	v_mov_b32_e32 v38, v2
	v_mov_b32_e32 v39, v2
	v_mov_b32_e32 v40, v2
	v_mov_b32_e32 v41, v2
	v_mov_b32_e32 v50, v2
	v_mov_b32_e32 v51, v2
	v_mov_b32_e32 v52, v2
	v_mov_b32_e32 v53, v2
	v_mov_b32_e32 v54, v2
	v_mov_b32_e32 v55, v2
	v_mov_b32_e32 v56, v2
	v_mov_b32_e32 v57, v2
	v_mov_b32_e32 v10, v2
	v_mov_b32_e32 v11, v2
	v_mov_b32_e32 v12, v2
	v_mov_b32_e32 v13, v2
	v_mov_b32_e32 v14, v2
	v_mov_b32_e32 v15, v2
	v_mov_b32_e32 v16, v2
	v_mov_b32_e32 v17, v2
	v_mov_b32_e32 v26, v2
	v_mov_b32_e32 v27, v2
	v_mov_b32_e32 v28, v2
	v_mov_b32_e32 v29, v2
	v_mov_b32_e32 v30, v2
	v_mov_b32_e32 v31, v2
	v_mov_b32_e32 v32, v2
	v_mov_b32_e32 v33, v2
	v_mov_b32_e32 v42, v2
	v_mov_b32_e32 v43, v2
	v_mov_b32_e32 v44, v2
	v_mov_b32_e32 v45, v2
	v_mov_b32_e32 v46, v2
	v_mov_b32_e32 v47, v2
	v_mov_b32_e32 v48, v2
	v_mov_b32_e32 v49, v2
	v_mov_b32_e32 v58, v2
	v_mov_b32_e32 v59, v2
	v_mov_b32_e32 v60, v2
	v_mov_b32_e32 v61, v2
	v_mov_b32_e32 v62, v2
	v_mov_b32_e32 v63, v2
	v_mov_b32_e32 v64, v2
	v_mov_b32_e32 v65, v2
	v_mov_b32_e32 v66, v2
	v_mov_b32_e32 v67, v2
	v_mov_b32_e32 v68, v2
	v_mov_b32_e32 v69, v2
	v_mov_b32_e32 v70, v2
	v_mov_b32_e32 v71, v2
	v_mov_b32_e32 v72, v2
	v_mov_b32_e32 v73, v2
	v_mov_b32_e32 v82, v2
	v_mov_b32_e32 v83, v2
	v_mov_b32_e32 v84, v2
	v_mov_b32_e32 v85, v2
	v_mov_b32_e32 v86, v2
	v_mov_b32_e32 v87, v2
	v_mov_b32_e32 v88, v2
	v_mov_b32_e32 v89, v2
	v_mov_b32_e32 v98, v2
	v_mov_b32_e32 v99, v2
	v_mov_b32_e32 v100, v2
	v_mov_b32_e32 v101, v2
	v_mov_b32_e32 v102, v2
	v_mov_b32_e32 v103, v2
	v_mov_b32_e32 v104, v2
	v_mov_b32_e32 v105, v2
	v_mov_b32_e32 v114, v2
	v_mov_b32_e32 v115, v2
	v_mov_b32_e32 v116, v2
	v_mov_b32_e32 v117, v2
	v_mov_b32_e32 v122, v2
	v_mov_b32_e32 v123, v2
	v_mov_b32_e32 v124, v2
	v_mov_b32_e32 v125, v2
	v_mov_b32_e32 v74, v2
	v_mov_b32_e32 v75, v2
	v_mov_b32_e32 v76, v2
	v_mov_b32_e32 v77, v2
	v_mov_b32_e32 v78, v2
	v_mov_b32_e32 v79, v2
	v_mov_b32_e32 v80, v2
	v_mov_b32_e32 v81, v2
	v_mov_b32_e32 v90, v2
	v_mov_b32_e32 v91, v2
	v_mov_b32_e32 v92, v2
	v_mov_b32_e32 v93, v2
	v_mov_b32_e32 v94, v2
	v_mov_b32_e32 v95, v2
	v_mov_b32_e32 v96, v2
	v_mov_b32_e32 v97, v2
	v_mov_b32_e32 v106, v2
	v_mov_b32_e32 v107, v2
	v_mov_b32_e32 v108, v2
	v_mov_b32_e32 v109, v2
	v_mov_b32_e32 v110, v2
	v_mov_b32_e32 v111, v2
	v_mov_b32_e32 v112, v2
	v_mov_b32_e32 v113, v2
	v_mov_b32_e32 v130, v2
	v_mov_b32_e32 v131, v2
	v_mov_b32_e32 v132, v2
	v_mov_b32_e32 v133, v2
	v_mov_b32_e32 v134, v2
	v_mov_b32_e32 v135, v2
	v_mov_b32_e32 v136, v2
	v_mov_b32_e32 v137, v2
	s_branch .LBB0_688

.Lnobar_e1e:
.LBB0_836:
	s_add_u32 s28, s6, 0xfffc0080
	s_addc_u32 s29, s7, -1
	s_add_i32 s41, 0, 0x10000
	s_cmp_eq_u32 s40, 12
	s_cselect_b32 s31, s5, s29
	s_cselect_b32 s30, s8, s28
	s_cselect_b32 s29, s9, s33
	s_cselect_b32 s28, s21, s23
	s_add_i32 s53, 0, 0x14000
	v_add_u32_e32 v142, s41, v186
	v_add_u32_e32 v168, s53, v186
	ds_read_b128 v[130:133], v142
	ds_read_b128 v[134:137], v142 offset:1024
	ds_read_b128 v[138:141], v142 offset:2048
	ds_read_b128 v[142:145], v142 offset:3072
	ds_read_b128 v[146:149], v168
	ds_read_b128 v[150:153], v168 offset:1024
	ds_read_b128 v[154:157], v168 offset:2048
	ds_read_b128 v[168:171], v168 offset:3072
	v_lshl_add_u64 v[216:217], s[6:7], 0, v[166:167]
	s_add_i32 m0, s43, 0xc000
	ds_read_b128 v[172:175], v188
	ds_read_b128 v[176:179], v188 offset:1024
	ds_read_b128 v[180:183], v188 offset:2048
	ds_read_b128 v[190:193], v188 offset:3072
	ds_read_b128 v[194:197], v188 offset:4096
	ds_read_b128 v[198:201], v188 offset:5120
	ds_read_b128 v[202:205], v188 offset:6144
	ds_read_b128 v[206:209], v188 offset:7168
	global_load_lds_dwordx4 v[216:217], off
	s_add_i32 m0, s43, 0xe000
	v_lshl_add_u64 v[216:217], s[6:7], 0, v[164:165]
	global_load_lds_dwordx4 v[216:217], off
	s_waitcnt vmcnt(8)
	s_waitcnt lgkmcnt(0)
	s_barrier
	s_waitcnt lgkmcnt(0)
	v_mfma_f32_16x16x32_bf16 v[126:129], v[130:133], v[172:175], v[126:129]
	v_mfma_f32_16x16x32_bf16 v[122:125], v[138:141], v[172:175], v[122:125]
	v_mfma_f32_16x16x32_bf16 v[114:117], v[130:133], v[180:183], v[114:117]
	v_mfma_f32_16x16x32_bf16 v[106:109], v[138:141], v[180:183], v[106:109]
	v_mfma_f32_16x16x32_bf16 v[98:101], v[130:133], v[194:197], v[98:101]
	v_mfma_f32_16x16x32_bf16 v[90:93], v[138:141], v[194:197], v[90:93]
	v_mfma_f32_16x16x32_bf16 v[82:85], v[130:133], v[202:205], v[82:85]
	v_mfma_f32_16x16x32_bf16 v[74:77], v[138:141], v[202:205], v[74:77]
	v_mfma_f32_16x16x32_bf16 v[126:129], v[134:137], v[176:179], v[126:129]
	v_mfma_f32_16x16x32_bf16 v[122:125], v[142:145], v[176:179], v[122:125]
	v_mfma_f32_16x16x32_bf16 v[114:117], v[134:137], v[190:193], v[114:117]
	v_mfma_f32_16x16x32_bf16 v[106:109], v[142:145], v[190:193], v[106:109]
	v_mfma_f32_16x16x32_bf16 v[98:101], v[134:137], v[198:201], v[98:101]
	v_mfma_f32_16x16x32_bf16 v[90:93], v[142:145], v[198:201], v[90:93]
	v_mfma_f32_16x16x32_bf16 v[82:85], v[134:137], v[206:209], v[82:85]
	v_mfma_f32_16x16x32_bf16 v[74:77], v[142:145], v[206:209], v[74:77]
	v_mfma_f32_16x16x32_bf16 v[118:121], v[146:149], v[172:175], v[118:121]
	v_mfma_f32_16x16x32_bf16 v[110:113], v[154:157], v[172:175], v[110:113]
	v_mfma_f32_16x16x32_bf16 v[102:105], v[146:149], v[180:183], v[102:105]
	v_mfma_f32_16x16x32_bf16 v[94:97], v[154:157], v[180:183], v[94:97]
	v_mfma_f32_16x16x32_bf16 v[86:89], v[146:149], v[194:197], v[86:89]
	v_mfma_f32_16x16x32_bf16 v[78:81], v[154:157], v[194:197], v[78:81]
	v_mfma_f32_16x16x32_bf16 v[70:73], v[146:149], v[202:205], v[70:73]
	v_mfma_f32_16x16x32_bf16 v[66:69], v[154:157], v[202:205], v[66:69]
	v_mfma_f32_16x16x32_bf16 v[118:121], v[150:153], v[176:179], v[118:121]
	v_mfma_f32_16x16x32_bf16 v[110:113], v[168:171], v[176:179], v[110:113]
	v_mfma_f32_16x16x32_bf16 v[102:105], v[150:153], v[190:193], v[102:105]
	v_mfma_f32_16x16x32_bf16 v[94:97], v[168:171], v[190:193], v[94:97]
	v_mfma_f32_16x16x32_bf16 v[86:89], v[150:153], v[198:201], v[86:89]
	v_mfma_f32_16x16x32_bf16 v[78:81], v[168:171], v[198:201], v[78:81]
	v_mfma_f32_16x16x32_bf16 v[70:73], v[150:153], v[206:209], v[70:73]
	v_mfma_f32_16x16x32_bf16 v[66:69], v[168:171], v[206:209], v[66:69]
	s_barrier
	s_add_i32 s41, s41, s42
	v_lshl_add_u64 v[216:217], s[28:29], 0, v[0:1]
	s_mov_b32 m0, s41
	ds_read_b128 v[172:175], v188 offset:16384
	ds_read_b128 v[176:179], v188 offset:17408
	ds_read_b128 v[180:183], v188 offset:18432
	ds_read_b128 v[190:193], v188 offset:19456
	ds_read_b128 v[194:197], v188 offset:20480
	ds_read_b128 v[198:201], v188 offset:21504
	ds_read_b128 v[202:205], v188 offset:22528
	ds_read_b128 v[206:209], v188 offset:23552
	global_load_lds_dwordx4 v[216:217], off
	s_add_i32 m0, s41, 0x2000
	s_add_u32 s58, s28, 0x40000
	v_lshl_add_u64 v[218:219], s[28:29], 0, v[158:159]
	s_addc_u32 s59, s29, 0
	s_add_i32 s41, s53, s42
	global_load_lds_dwordx4 v[218:219], off
	v_lshl_add_u64 v[220:221], s[58:59], 0, v[0:1]
	s_mov_b32 m0, s41
	v_lshl_add_u64 v[222:223], s[30:31], 0, v[160:161]
	global_load_lds_dwordx4 v[220:221], off
	s_add_i32 m0, s41, 0x2000
	v_lshl_add_u64 v[220:221], s[58:59], 0, v[158:159]
	global_load_lds_dwordx4 v[220:221], off
	s_mov_b32 m0, s43
	v_lshl_add_u64 v[220:221], s[30:31], 0, v[162:163]
	global_load_lds_dwordx4 v[220:221], off
	s_mov_b32 m0, s44
	s_nop 0
	global_load_lds_dwordx4 v[222:223], off
	s_waitcnt vmcnt(8)
	s_waitcnt lgkmcnt(0)
	s_barrier
	s_waitcnt lgkmcnt(0)
	v_mfma_f32_16x16x32_bf16 v[62:65], v[130:133], v[172:175], v[62:65]
	v_mfma_f32_16x16x32_bf16 v[58:61], v[138:141], v[172:175], v[58:61]
	v_mfma_f32_16x16x32_bf16 v[50:53], v[130:133], v[180:183], v[50:53]
	v_mfma_f32_16x16x32_bf16 v[42:45], v[138:141], v[180:183], v[42:45]
	v_mfma_f32_16x16x32_bf16 v[34:37], v[130:133], v[194:197], v[34:37]
	v_mfma_f32_16x16x32_bf16 v[26:29], v[138:141], v[194:197], v[26:29]
	v_mfma_f32_16x16x32_bf16 v[18:21], v[130:133], v[202:205], v[18:21]
	v_mfma_f32_16x16x32_bf16 v[10:13], v[138:141], v[202:205], v[10:13]
	v_mfma_f32_16x16x32_bf16 v[62:65], v[134:137], v[176:179], v[62:65]
	v_mfma_f32_16x16x32_bf16 v[58:61], v[142:145], v[176:179], v[58:61]
	v_mfma_f32_16x16x32_bf16 v[50:53], v[134:137], v[190:193], v[50:53]
	v_mfma_f32_16x16x32_bf16 v[42:45], v[142:145], v[190:193], v[42:45]
	v_mfma_f32_16x16x32_bf16 v[34:37], v[134:137], v[198:201], v[34:37]
	v_mfma_f32_16x16x32_bf16 v[26:29], v[142:145], v[198:201], v[26:29]
	v_mfma_f32_16x16x32_bf16 v[18:21], v[134:137], v[206:209], v[18:21]
	v_mfma_f32_16x16x32_bf16 v[10:13], v[142:145], v[206:209], v[10:13]
	v_mfma_f32_16x16x32_bf16 v[54:57], v[146:149], v[172:175], v[54:57]
	v_mfma_f32_16x16x32_bf16 v[46:49], v[154:157], v[172:175], v[46:49]
	v_mfma_f32_16x16x32_bf16 v[38:41], v[146:149], v[180:183], v[38:41]
	v_mfma_f32_16x16x32_bf16 v[30:33], v[154:157], v[180:183], v[30:33]
	v_mfma_f32_16x16x32_bf16 v[22:25], v[146:149], v[194:197], v[22:25]
	v_mfma_f32_16x16x32_bf16 v[14:17], v[154:157], v[194:197], v[14:17]
	v_mfma_f32_16x16x32_bf16 v[6:9], v[146:149], v[202:205], v[6:9]
	v_mfma_f32_16x16x32_bf16 v[2:5], v[154:157], v[202:205], v[2:5]
	v_mfma_f32_16x16x32_bf16 v[54:57], v[150:153], v[176:179], v[54:57]
	v_mfma_f32_16x16x32_bf16 v[46:49], v[168:171], v[176:179], v[46:49]
	v_mfma_f32_16x16x32_bf16 v[38:41], v[150:153], v[190:193], v[38:41]
	v_mfma_f32_16x16x32_bf16 v[30:33], v[168:171], v[190:193], v[30:33]
	v_mfma_f32_16x16x32_bf16 v[22:25], v[150:153], v[198:201], v[22:25]
	v_mfma_f32_16x16x32_bf16 v[14:17], v[168:171], v[198:201], v[14:17]
	v_mfma_f32_16x16x32_bf16 v[6:9], v[150:153], v[206:209], v[6:9]
	v_mfma_f32_16x16x32_bf16 v[2:5], v[168:171], v[206:209], v[2:5]
	s_barrier
	s_add_i32 s41, 0, 0x18000
	s_add_i32 s53, 0, 0x1c000
	v_add_u32_e32 v142, s41, v186
	v_add_u32_e32 v168, s53, v186
	ds_read_b128 v[130:133], v142
	ds_read_b128 v[134:137], v142 offset:1024
	ds_read_b128 v[138:141], v142 offset:2048
	ds_read_b128 v[142:145], v142 offset:3072
	ds_read_b128 v[146:149], v168
	ds_read_b128 v[150:153], v168 offset:1024
	ds_read_b128 v[154:157], v168 offset:2048
	ds_read_b128 v[168:171], v168 offset:3072
	s_add_u32 s30, s30, 0x40000
	s_addc_u32 s31, s31, 0
	s_mov_b32 m0, s45
	v_lshl_add_u64 v[224:225], s[30:31], 0, v[162:163]
	ds_read_b128 v[172:175], v188 offset:32768
	ds_read_b128 v[176:179], v188 offset:33792
	ds_read_b128 v[180:183], v188 offset:34816
	ds_read_b128 v[190:193], v188 offset:35840
	ds_read_b128 v[194:197], v188 offset:36864
	ds_read_b128 v[198:201], v188 offset:37888
	ds_read_b128 v[202:205], v188 offset:38912
	ds_read_b128 v[206:209], v188 offset:39936
	global_load_lds_dwordx4 v[224:225], off
	s_mov_b32 m0, s46
	v_lshl_add_u64 v[224:225], s[30:31], 0, v[160:161]
	global_load_lds_dwordx4 v[224:225], off
	s_waitcnt vmcnt(8)
	s_waitcnt lgkmcnt(0)
	s_barrier
	s_waitcnt lgkmcnt(0)
	v_mfma_f32_16x16x32_bf16 v[126:129], v[130:133], v[172:175], v[126:129]
	v_mfma_f32_16x16x32_bf16 v[122:125], v[138:141], v[172:175], v[122:125]
	v_mfma_f32_16x16x32_bf16 v[114:117], v[130:133], v[180:183], v[114:117]
	v_mfma_f32_16x16x32_bf16 v[106:109], v[138:141], v[180:183], v[106:109]
	v_mfma_f32_16x16x32_bf16 v[98:101], v[130:133], v[194:197], v[98:101]
	v_mfma_f32_16x16x32_bf16 v[90:93], v[138:141], v[194:197], v[90:93]
	v_mfma_f32_16x16x32_bf16 v[82:85], v[130:133], v[202:205], v[82:85]
	v_mfma_f32_16x16x32_bf16 v[74:77], v[138:141], v[202:205], v[74:77]
	v_mfma_f32_16x16x32_bf16 v[126:129], v[134:137], v[176:179], v[126:129]
	v_mfma_f32_16x16x32_bf16 v[122:125], v[142:145], v[176:179], v[122:125]
	v_mfma_f32_16x16x32_bf16 v[114:117], v[134:137], v[190:193], v[114:117]
	v_mfma_f32_16x16x32_bf16 v[106:109], v[142:145], v[190:193], v[106:109]
	v_mfma_f32_16x16x32_bf16 v[98:101], v[134:137], v[198:201], v[98:101]
	v_mfma_f32_16x16x32_bf16 v[90:93], v[142:145], v[198:201], v[90:93]
	v_mfma_f32_16x16x32_bf16 v[82:85], v[134:137], v[206:209], v[82:85]
	v_mfma_f32_16x16x32_bf16 v[74:77], v[142:145], v[206:209], v[74:77]
	v_mfma_f32_16x16x32_bf16 v[118:121], v[146:149], v[172:175], v[118:121]
	v_mfma_f32_16x16x32_bf16 v[110:113], v[154:157], v[172:175], v[110:113]
	v_mfma_f32_16x16x32_bf16 v[102:105], v[146:149], v[180:183], v[102:105]
	v_mfma_f32_16x16x32_bf16 v[94:97], v[154:157], v[180:183], v[94:97]
	v_mfma_f32_16x16x32_bf16 v[86:89], v[146:149], v[194:197], v[86:89]
	v_mfma_f32_16x16x32_bf16 v[78:81], v[154:157], v[194:197], v[78:81]
	v_mfma_f32_16x16x32_bf16 v[70:73], v[146:149], v[202:205], v[70:73]
	v_mfma_f32_16x16x32_bf16 v[66:69], v[154:157], v[202:205], v[66:69]
	v_mfma_f32_16x16x32_bf16 v[118:121], v[150:153], v[176:179], v[118:121]
	v_mfma_f32_16x16x32_bf16 v[110:113], v[168:171], v[176:179], v[110:113]
	v_mfma_f32_16x16x32_bf16 v[102:105], v[150:153], v[190:193], v[102:105]
	v_mfma_f32_16x16x32_bf16 v[94:97], v[168:171], v[190:193], v[94:97]
	v_mfma_f32_16x16x32_bf16 v[86:89], v[150:153], v[198:201], v[86:89]
	v_mfma_f32_16x16x32_bf16 v[78:81], v[168:171], v[198:201], v[78:81]
	v_mfma_f32_16x16x32_bf16 v[70:73], v[150:153], v[206:209], v[70:73]
	v_mfma_f32_16x16x32_bf16 v[66:69], v[168:171], v[206:209], v[66:69]
	s_barrier
	s_add_i32 s30, s41, s42
	v_lshl_add_u64 v[216:217], v[216:217], 0, s[56:57]
	s_mov_b32 m0, s30
	ds_read_b128 v[172:175], v188 offset:49152
	ds_read_b128 v[176:179], v188 offset:50176
	ds_read_b128 v[180:183], v188 offset:51200
	ds_read_b128 v[190:193], v188 offset:52224
	ds_read_b128 v[194:197], v188 offset:53248
	ds_read_b128 v[198:201], v188 offset:54272
	ds_read_b128 v[202:205], v188 offset:55296
	ds_read_b128 v[206:209], v188 offset:56320
	global_load_lds_dwordx4 v[216:217], off
	s_add_i32 m0, s30, 0x2000
	s_add_u32 s28, s28, 0x40080
	v_lshl_add_u64 v[216:217], v[218:219], 0, s[56:57]
	s_addc_u32 s29, s29, 0
	s_add_i32 s30, s53, s42
	global_load_lds_dwordx4 v[216:217], off
	s_mov_b32 m0, s30
	v_lshl_add_u64 v[216:217], s[28:29], 0, v[0:1]
	global_load_lds_dwordx4 v[216:217], off
	s_add_i32 m0, s30, 0x2000
	v_lshl_add_u64 v[216:217], s[28:29], 0, v[158:159]
	global_load_lds_dwordx4 v[216:217], off
	s_mov_b32 m0, s47
	v_lshl_add_u64 v[216:217], v[220:221], 0, s[56:57]
	global_load_lds_dwordx4 v[216:217], off
	s_mov_b32 m0, s48
	v_lshl_add_u64 v[216:217], v[222:223], 0, s[56:57]
	global_load_lds_dwordx4 v[216:217], off
	s_waitcnt vmcnt(8)
	s_waitcnt lgkmcnt(0)
	s_barrier
	s_waitcnt lgkmcnt(0)
	v_mfma_f32_16x16x32_bf16 v[62:65], v[130:133], v[172:175], v[62:65]
	v_mfma_f32_16x16x32_bf16 v[58:61], v[138:141], v[172:175], v[58:61]
	v_mfma_f32_16x16x32_bf16 v[50:53], v[130:133], v[180:183], v[50:53]
	v_mfma_f32_16x16x32_bf16 v[42:45], v[138:141], v[180:183], v[42:45]
	v_mfma_f32_16x16x32_bf16 v[34:37], v[130:133], v[194:197], v[34:37]
	v_mfma_f32_16x16x32_bf16 v[26:29], v[138:141], v[194:197], v[26:29]
	v_mfma_f32_16x16x32_bf16 v[18:21], v[130:133], v[202:205], v[18:21]
	v_mfma_f32_16x16x32_bf16 v[10:13], v[138:141], v[202:205], v[10:13]
	v_mfma_f32_16x16x32_bf16 v[62:65], v[134:137], v[176:179], v[62:65]
	v_mfma_f32_16x16x32_bf16 v[58:61], v[142:145], v[176:179], v[58:61]
	v_mfma_f32_16x16x32_bf16 v[50:53], v[134:137], v[190:193], v[50:53]
	v_mfma_f32_16x16x32_bf16 v[42:45], v[142:145], v[190:193], v[42:45]
	v_mfma_f32_16x16x32_bf16 v[34:37], v[134:137], v[198:201], v[34:37]
	v_mfma_f32_16x16x32_bf16 v[26:29], v[142:145], v[198:201], v[26:29]
	v_mfma_f32_16x16x32_bf16 v[18:21], v[134:137], v[206:209], v[18:21]
	v_mfma_f32_16x16x32_bf16 v[10:13], v[142:145], v[206:209], v[10:13]
	v_mfma_f32_16x16x32_bf16 v[54:57], v[146:149], v[172:175], v[54:57]
	v_mfma_f32_16x16x32_bf16 v[46:49], v[154:157], v[172:175], v[46:49]
	v_mfma_f32_16x16x32_bf16 v[38:41], v[146:149], v[180:183], v[38:41]
	v_mfma_f32_16x16x32_bf16 v[30:33], v[154:157], v[180:183], v[30:33]
	v_mfma_f32_16x16x32_bf16 v[22:25], v[146:149], v[194:197], v[22:25]
	v_mfma_f32_16x16x32_bf16 v[14:17], v[154:157], v[194:197], v[14:17]
	v_mfma_f32_16x16x32_bf16 v[6:9], v[146:149], v[202:205], v[6:9]
	v_mfma_f32_16x16x32_bf16 v[2:5], v[154:157], v[202:205], v[2:5]
	v_mfma_f32_16x16x32_bf16 v[54:57], v[150:153], v[176:179], v[54:57]
	v_mfma_f32_16x16x32_bf16 v[46:49], v[168:171], v[176:179], v[46:49]
	v_mfma_f32_16x16x32_bf16 v[38:41], v[150:153], v[190:193], v[38:41]
	v_mfma_f32_16x16x32_bf16 v[30:33], v[168:171], v[190:193], v[30:33]
	v_mfma_f32_16x16x32_bf16 v[22:25], v[150:153], v[198:201], v[22:25]
	v_mfma_f32_16x16x32_bf16 v[14:17], v[168:171], v[198:201], v[14:17]
	v_mfma_f32_16x16x32_bf16 v[6:9], v[150:153], v[206:209], v[6:9]
	v_mfma_f32_16x16x32_bf16 v[2:5], v[168:171], v[206:209], v[2:5]
	s_barrier
	s_add_i32 s40, s40, 2
	s_add_u32 s23, s23, 0x100
	s_addc_u32 s33, s33, 0
	s_add_u32 s6, s6, 0x100
	s_addc_u32 s7, s7, 0
	s_cmp_gt_u32 s40, 13
	s_cbranch_scc0 .LBB0_836
	s_and_b64 vcc, exec, s[18:19]
	s_cbranch_vccz .LBB0_839
	s_barrier

.LBB0_1525:
	s_add_u32 s36, s26, s34
	s_addc_u32 s37, s27, s35
	s_add_u32 s36, s36, 0x100
	s_addc_u32 s37, s37, 0
	s_add_u32 s82, s8, s34
	s_addc_u32 s83, s9, s35
	s_add_i32 s84, 0, 0x10000
	s_cmpk_eq_i32 s34, 0xb00
	s_cselect_b32 s45, s31, s37
	s_cselect_b32 s44, s30, s36
	s_cselect_b32 s37, s29, s83
	s_cselect_b32 s36, s28, s82
	s_add_i32 s85, 0, 0x14000
	v_add_u32_e32 v158, s84, v144
	v_add_u32_e32 v176, s85, v144
	ds_read_b128 v[146:149], v158
	ds_read_b128 v[150:153], v158 offset:1024
	ds_read_b128 v[154:157], v158 offset:2048
	ds_read_b128 v[158:161], v158 offset:3072
	ds_read_b128 v[162:165], v176
	ds_read_b128 v[168:171], v176 offset:1024
	ds_read_b128 v[172:175], v176 offset:2048
	ds_read_b128 v[176:179], v176 offset:3072
	v_lshl_add_u64 v[208:209], v[142:143], 0, s[34:35]
	s_add_i32 m0, s4, 0xc000
	ds_read_b128 v[180:183], v145
	ds_read_b128 v[184:187], v145 offset:1024
	ds_read_b128 v[188:191], v145 offset:2048
	ds_read_b128 v[192:195], v145 offset:3072
	ds_read_b128 v[196:199], v145 offset:4096
	ds_read_b128 v[200:203], v145 offset:5120
	ds_read_b128 v[204:207], v145 offset:6144
	ds_read_b128 v[216:219], v145 offset:7168
	global_load_lds_dwordx4 v[208:209], off
	s_add_i32 m0, s4, 0xe000
	v_lshl_add_u64 v[208:209], v[140:141], 0, s[34:35]
	global_load_lds_dwordx4 v[208:209], off
	s_waitcnt vmcnt(8)
	s_waitcnt lgkmcnt(0)
	s_barrier
	s_waitcnt lgkmcnt(0)
	v_mfma_f32_16x16x32_bf16 v[134:137], v[146:149], v[180:183], v[134:137]
	v_mfma_f32_16x16x32_bf16 v[130:133], v[154:157], v[180:183], v[130:133]
	v_mfma_f32_16x16x32_bf16 v[110:113], v[146:149], v[188:191], v[110:113]
	v_mfma_f32_16x16x32_bf16 v[106:109], v[154:157], v[188:191], v[106:109]
	v_mfma_f32_16x16x32_bf16 v[94:97], v[146:149], v[196:199], v[94:97]
	v_mfma_f32_16x16x32_bf16 v[90:93], v[154:157], v[196:199], v[90:93]
	v_mfma_f32_16x16x32_bf16 v[78:81], v[146:149], v[204:207], v[78:81]
	v_mfma_f32_16x16x32_bf16 v[74:77], v[154:157], v[204:207], v[74:77]
	v_mfma_f32_16x16x32_bf16 v[134:137], v[150:153], v[184:187], v[134:137]
	v_mfma_f32_16x16x32_bf16 v[130:133], v[158:161], v[184:187], v[130:133]
	v_mfma_f32_16x16x32_bf16 v[110:113], v[150:153], v[192:195], v[110:113]
	v_mfma_f32_16x16x32_bf16 v[106:109], v[158:161], v[192:195], v[106:109]
	v_mfma_f32_16x16x32_bf16 v[94:97], v[150:153], v[200:203], v[94:97]
	v_mfma_f32_16x16x32_bf16 v[90:93], v[158:161], v[200:203], v[90:93]
	v_mfma_f32_16x16x32_bf16 v[78:81], v[150:153], v[216:219], v[78:81]
	v_mfma_f32_16x16x32_bf16 v[74:77], v[158:161], v[216:219], v[74:77]
	v_mfma_f32_16x16x32_bf16 v[122:125], v[162:165], v[180:183], v[122:125]
	v_mfma_f32_16x16x32_bf16 v[114:117], v[172:175], v[180:183], v[114:117]
	v_mfma_f32_16x16x32_bf16 v[102:105], v[162:165], v[188:191], v[102:105]
	v_mfma_f32_16x16x32_bf16 v[98:101], v[172:175], v[188:191], v[98:101]
	v_mfma_f32_16x16x32_bf16 v[86:89], v[162:165], v[196:199], v[86:89]
	v_mfma_f32_16x16x32_bf16 v[82:85], v[172:175], v[196:199], v[82:85]
	v_mfma_f32_16x16x32_bf16 v[70:73], v[162:165], v[204:207], v[70:73]
	v_mfma_f32_16x16x32_bf16 v[66:69], v[172:175], v[204:207], v[66:69]
	v_mfma_f32_16x16x32_bf16 v[122:125], v[168:171], v[184:187], v[122:125]
	v_mfma_f32_16x16x32_bf16 v[114:117], v[176:179], v[184:187], v[114:117]
	v_mfma_f32_16x16x32_bf16 v[102:105], v[168:171], v[192:195], v[102:105]
	v_mfma_f32_16x16x32_bf16 v[98:101], v[176:179], v[192:195], v[98:101]
	v_mfma_f32_16x16x32_bf16 v[86:89], v[168:171], v[200:203], v[86:89]
	v_mfma_f32_16x16x32_bf16 v[82:85], v[176:179], v[200:203], v[82:85]
	v_mfma_f32_16x16x32_bf16 v[70:73], v[168:171], v[216:219], v[70:73]
	v_mfma_f32_16x16x32_bf16 v[66:69], v[176:179], v[216:219], v[66:69]
	s_barrier
	s_add_i32 s82, s84, s70
	v_lshl_add_u64 v[208:209], s[36:37], 0, v[0:1]
	s_mov_b32 m0, s82
	ds_read_b128 v[180:183], v145 offset:16384
	ds_read_b128 v[184:187], v145 offset:17408
	ds_read_b128 v[188:191], v145 offset:18432
	ds_read_b128 v[192:195], v145 offset:19456
	ds_read_b128 v[196:199], v145 offset:20480
	ds_read_b128 v[200:203], v145 offset:21504
	ds_read_b128 v[204:207], v145 offset:22528
	ds_read_b128 v[216:219], v145 offset:23552
	global_load_lds_dwordx4 v[208:209], off
	s_add_i32 m0, s82, 0x2000
	s_add_u32 s82, s36, 0x60000
	v_lshl_add_u64 v[220:221], s[36:37], 0, v[118:119]
	s_addc_u32 s83, s37, 0
	s_add_i32 s84, s85, s70
	global_load_lds_dwordx4 v[220:221], off
	v_lshl_add_u64 v[222:223], s[82:83], 0, v[0:1]
	s_mov_b32 m0, s84
	v_lshl_add_u64 v[224:225], s[44:45], 0, v[120:121]
	global_load_lds_dwordx4 v[222:223], off
	s_add_i32 m0, s84, 0x2000
	v_lshl_add_u64 v[222:223], s[82:83], 0, v[118:119]
	global_load_lds_dwordx4 v[222:223], off
	s_mov_b32 m0, s4
	v_lshl_add_u64 v[222:223], s[44:45], 0, v[126:127]
	global_load_lds_dwordx4 v[222:223], off
	s_mov_b32 m0, s33
	s_nop 0
	global_load_lds_dwordx4 v[224:225], off
	s_waitcnt vmcnt(8)
	s_waitcnt lgkmcnt(0)
	s_barrier
	s_waitcnt lgkmcnt(0)
	v_mfma_f32_16x16x32_bf16 v[62:65], v[146:149], v[180:183], v[62:65]
	v_mfma_f32_16x16x32_bf16 v[58:61], v[154:157], v[180:183], v[58:61]
	v_mfma_f32_16x16x32_bf16 v[46:49], v[146:149], v[188:191], v[46:49]
	v_mfma_f32_16x16x32_bf16 v[42:45], v[154:157], v[188:191], v[42:45]
	v_mfma_f32_16x16x32_bf16 v[30:33], v[146:149], v[196:199], v[30:33]
	v_mfma_f32_16x16x32_bf16 v[26:29], v[154:157], v[196:199], v[26:29]
	v_mfma_f32_16x16x32_bf16 v[14:17], v[146:149], v[204:207], v[14:17]
	v_mfma_f32_16x16x32_bf16 v[10:13], v[154:157], v[204:207], v[10:13]
	v_mfma_f32_16x16x32_bf16 v[62:65], v[150:153], v[184:187], v[62:65]
	v_mfma_f32_16x16x32_bf16 v[58:61], v[158:161], v[184:187], v[58:61]
	v_mfma_f32_16x16x32_bf16 v[46:49], v[150:153], v[192:195], v[46:49]
	v_mfma_f32_16x16x32_bf16 v[42:45], v[158:161], v[192:195], v[42:45]
	v_mfma_f32_16x16x32_bf16 v[30:33], v[150:153], v[200:203], v[30:33]
	v_mfma_f32_16x16x32_bf16 v[26:29], v[158:161], v[200:203], v[26:29]
	v_mfma_f32_16x16x32_bf16 v[14:17], v[150:153], v[216:219], v[14:17]
	v_mfma_f32_16x16x32_bf16 v[10:13], v[158:161], v[216:219], v[10:13]
	v_mfma_f32_16x16x32_bf16 v[54:57], v[162:165], v[180:183], v[54:57]
	v_mfma_f32_16x16x32_bf16 v[50:53], v[172:175], v[180:183], v[50:53]
	v_mfma_f32_16x16x32_bf16 v[38:41], v[162:165], v[188:191], v[38:41]
	v_mfma_f32_16x16x32_bf16 v[34:37], v[172:175], v[188:191], v[34:37]
	v_mfma_f32_16x16x32_bf16 v[22:25], v[162:165], v[196:199], v[22:25]
	v_mfma_f32_16x16x32_bf16 v[18:21], v[172:175], v[196:199], v[18:21]
	v_mfma_f32_16x16x32_bf16 v[6:9], v[162:165], v[204:207], v[6:9]
	v_mfma_f32_16x16x32_bf16 v[2:5], v[172:175], v[204:207], v[2:5]
	v_mfma_f32_16x16x32_bf16 v[54:57], v[168:171], v[184:187], v[54:57]
	v_mfma_f32_16x16x32_bf16 v[50:53], v[176:179], v[184:187], v[50:53]
	v_mfma_f32_16x16x32_bf16 v[38:41], v[168:171], v[192:195], v[38:41]
	v_mfma_f32_16x16x32_bf16 v[34:37], v[176:179], v[192:195], v[34:37]
	v_mfma_f32_16x16x32_bf16 v[22:25], v[168:171], v[200:203], v[22:25]
	v_mfma_f32_16x16x32_bf16 v[18:21], v[176:179], v[200:203], v[18:21]
	v_mfma_f32_16x16x32_bf16 v[6:9], v[168:171], v[216:219], v[6:9]
	v_mfma_f32_16x16x32_bf16 v[2:5], v[176:179], v[216:219], v[2:5]
	s_barrier
	s_add_i32 s82, 0, 0x18000
	s_add_i32 s83, 0, 0x1c000
	v_add_u32_e32 v158, s82, v144
	v_add_u32_e32 v176, s83, v144
	ds_read_b128 v[146:149], v158
	ds_read_b128 v[150:153], v158 offset:1024
	ds_read_b128 v[154:157], v158 offset:2048
	ds_read_b128 v[158:161], v158 offset:3072
	ds_read_b128 v[162:165], v176
	ds_read_b128 v[168:171], v176 offset:1024
	ds_read_b128 v[172:175], v176 offset:2048
	ds_read_b128 v[176:179], v176 offset:3072
	s_add_u32 s44, s44, 0x60000
	s_addc_u32 s45, s45, 0
	s_mov_b32 m0, s71
	v_lshl_add_u64 v[242:243], s[44:45], 0, v[126:127]
	ds_read_b128 v[180:183], v145 offset:32768
	ds_read_b128 v[184:187], v145 offset:33792
	ds_read_b128 v[188:191], v145 offset:34816
	ds_read_b128 v[192:195], v145 offset:35840
	ds_read_b128 v[196:199], v145 offset:36864
	ds_read_b128 v[200:203], v145 offset:37888
	ds_read_b128 v[204:207], v145 offset:38912
	ds_read_b128 v[216:219], v145 offset:39936
	global_load_lds_dwordx4 v[242:243], off
	s_mov_b32 m0, s76
	v_lshl_add_u64 v[242:243], s[44:45], 0, v[120:121]
	global_load_lds_dwordx4 v[242:243], off
	s_waitcnt vmcnt(8)
	s_waitcnt lgkmcnt(0)
	s_barrier
	s_waitcnt lgkmcnt(0)
	v_mfma_f32_16x16x32_bf16 v[134:137], v[146:149], v[180:183], v[134:137]
	v_mfma_f32_16x16x32_bf16 v[130:133], v[154:157], v[180:183], v[130:133]
	v_mfma_f32_16x16x32_bf16 v[110:113], v[146:149], v[188:191], v[110:113]
	v_mfma_f32_16x16x32_bf16 v[106:109], v[154:157], v[188:191], v[106:109]
	v_mfma_f32_16x16x32_bf16 v[94:97], v[146:149], v[196:199], v[94:97]
	v_mfma_f32_16x16x32_bf16 v[90:93], v[154:157], v[196:199], v[90:93]
	v_mfma_f32_16x16x32_bf16 v[78:81], v[146:149], v[204:207], v[78:81]
	v_mfma_f32_16x16x32_bf16 v[74:77], v[154:157], v[204:207], v[74:77]
	v_mfma_f32_16x16x32_bf16 v[134:137], v[150:153], v[184:187], v[134:137]
	v_mfma_f32_16x16x32_bf16 v[130:133], v[158:161], v[184:187], v[130:133]
	v_mfma_f32_16x16x32_bf16 v[110:113], v[150:153], v[192:195], v[110:113]
	v_mfma_f32_16x16x32_bf16 v[106:109], v[158:161], v[192:195], v[106:109]
	v_mfma_f32_16x16x32_bf16 v[94:97], v[150:153], v[200:203], v[94:97]
	v_mfma_f32_16x16x32_bf16 v[90:93], v[158:161], v[200:203], v[90:93]
	v_mfma_f32_16x16x32_bf16 v[78:81], v[150:153], v[216:219], v[78:81]
	v_mfma_f32_16x16x32_bf16 v[74:77], v[158:161], v[216:219], v[74:77]
	v_mfma_f32_16x16x32_bf16 v[122:125], v[162:165], v[180:183], v[122:125]
	v_mfma_f32_16x16x32_bf16 v[114:117], v[172:175], v[180:183], v[114:117]
	v_mfma_f32_16x16x32_bf16 v[102:105], v[162:165], v[188:191], v[102:105]
	v_mfma_f32_16x16x32_bf16 v[98:101], v[172:175], v[188:191], v[98:101]
	v_mfma_f32_16x16x32_bf16 v[86:89], v[162:165], v[196:199], v[86:89]
	v_mfma_f32_16x16x32_bf16 v[82:85], v[172:175], v[196:199], v[82:85]
	v_mfma_f32_16x16x32_bf16 v[70:73], v[162:165], v[204:207], v[70:73]
	v_mfma_f32_16x16x32_bf16 v[66:69], v[172:175], v[204:207], v[66:69]
	v_mfma_f32_16x16x32_bf16 v[122:125], v[168:171], v[184:187], v[122:125]
	v_mfma_f32_16x16x32_bf16 v[114:117], v[176:179], v[184:187], v[114:117]
	v_mfma_f32_16x16x32_bf16 v[102:105], v[168:171], v[192:195], v[102:105]
	v_mfma_f32_16x16x32_bf16 v[98:101], v[176:179], v[192:195], v[98:101]
	v_mfma_f32_16x16x32_bf16 v[86:89], v[168:171], v[200:203], v[86:89]
	v_mfma_f32_16x16x32_bf16 v[82:85], v[176:179], v[200:203], v[82:85]
	v_mfma_f32_16x16x32_bf16 v[70:73], v[168:171], v[216:219], v[70:73]
	v_mfma_f32_16x16x32_bf16 v[66:69], v[176:179], v[216:219], v[66:69]
	s_barrier
	s_add_i32 s44, s82, s70
	v_lshl_add_u64 v[208:209], v[208:209], 0, s[56:57]
	s_mov_b32 m0, s44
	ds_read_b128 v[180:183], v145 offset:49152
	ds_read_b128 v[184:187], v145 offset:50176
	ds_read_b128 v[188:191], v145 offset:51200
	ds_read_b128 v[192:195], v145 offset:52224
	ds_read_b128 v[196:199], v145 offset:53248
	ds_read_b128 v[200:203], v145 offset:54272
	ds_read_b128 v[204:207], v145 offset:55296
	ds_read_b128 v[216:219], v145 offset:56320
	global_load_lds_dwordx4 v[208:209], off
	s_add_i32 m0, s44, 0x2000
	s_add_u32 s36, s36, 0x60080
	v_lshl_add_u64 v[208:209], v[220:221], 0, s[56:57]
	s_addc_u32 s37, s37, 0
	s_add_i32 s44, s83, s70
	global_load_lds_dwordx4 v[208:209], off
	s_mov_b32 m0, s44
	v_lshl_add_u64 v[208:209], s[36:37], 0, v[0:1]
	global_load_lds_dwordx4 v[208:209], off
	s_add_i32 m0, s44, 0x2000
	v_lshl_add_u64 v[208:209], s[36:37], 0, v[118:119]
	global_load_lds_dwordx4 v[208:209], off
	s_mov_b32 m0, s77
	v_lshl_add_u64 v[208:209], v[222:223], 0, s[56:57]
	global_load_lds_dwordx4 v[208:209], off
	s_mov_b32 m0, s79
	v_lshl_add_u64 v[208:209], v[224:225], 0, s[56:57]
	global_load_lds_dwordx4 v[208:209], off
	s_waitcnt vmcnt(8)
	s_waitcnt lgkmcnt(0)
	s_barrier
	s_waitcnt lgkmcnt(0)
	v_mfma_f32_16x16x32_bf16 v[62:65], v[146:149], v[180:183], v[62:65]
	v_mfma_f32_16x16x32_bf16 v[58:61], v[154:157], v[180:183], v[58:61]
	v_mfma_f32_16x16x32_bf16 v[46:49], v[146:149], v[188:191], v[46:49]
	v_mfma_f32_16x16x32_bf16 v[42:45], v[154:157], v[188:191], v[42:45]
	v_mfma_f32_16x16x32_bf16 v[30:33], v[146:149], v[196:199], v[30:33]
	v_mfma_f32_16x16x32_bf16 v[26:29], v[154:157], v[196:199], v[26:29]
	v_mfma_f32_16x16x32_bf16 v[14:17], v[146:149], v[204:207], v[14:17]
	v_mfma_f32_16x16x32_bf16 v[10:13], v[154:157], v[204:207], v[10:13]
	v_mfma_f32_16x16x32_bf16 v[62:65], v[150:153], v[184:187], v[62:65]
	v_mfma_f32_16x16x32_bf16 v[58:61], v[158:161], v[184:187], v[58:61]
	v_mfma_f32_16x16x32_bf16 v[46:49], v[150:153], v[192:195], v[46:49]
	v_mfma_f32_16x16x32_bf16 v[42:45], v[158:161], v[192:195], v[42:45]
	v_mfma_f32_16x16x32_bf16 v[30:33], v[150:153], v[200:203], v[30:33]
	v_mfma_f32_16x16x32_bf16 v[26:29], v[158:161], v[200:203], v[26:29]
	v_mfma_f32_16x16x32_bf16 v[14:17], v[150:153], v[216:219], v[14:17]
	v_mfma_f32_16x16x32_bf16 v[10:13], v[158:161], v[216:219], v[10:13]
	v_mfma_f32_16x16x32_bf16 v[54:57], v[162:165], v[180:183], v[54:57]
	v_mfma_f32_16x16x32_bf16 v[50:53], v[172:175], v[180:183], v[50:53]
	v_mfma_f32_16x16x32_bf16 v[38:41], v[162:165], v[188:191], v[38:41]
	v_mfma_f32_16x16x32_bf16 v[34:37], v[172:175], v[188:191], v[34:37]
	v_mfma_f32_16x16x32_bf16 v[22:25], v[162:165], v[196:199], v[22:25]
	v_mfma_f32_16x16x32_bf16 v[18:21], v[172:175], v[196:199], v[18:21]
	v_mfma_f32_16x16x32_bf16 v[6:9], v[162:165], v[204:207], v[6:9]
	v_mfma_f32_16x16x32_bf16 v[2:5], v[172:175], v[204:207], v[2:5]
	v_mfma_f32_16x16x32_bf16 v[54:57], v[168:171], v[184:187], v[54:57]
	v_mfma_f32_16x16x32_bf16 v[50:53], v[176:179], v[184:187], v[50:53]
	v_mfma_f32_16x16x32_bf16 v[38:41], v[168:171], v[192:195], v[38:41]
	v_mfma_f32_16x16x32_bf16 v[34:37], v[176:179], v[192:195], v[34:37]
	v_mfma_f32_16x16x32_bf16 v[22:25], v[168:171], v[200:203], v[22:25]
	v_mfma_f32_16x16x32_bf16 v[18:21], v[176:179], v[200:203], v[18:21]
	v_mfma_f32_16x16x32_bf16 v[6:9], v[168:171], v[216:219], v[6:9]
	v_mfma_f32_16x16x32_bf16 v[2:5], v[176:179], v[216:219], v[2:5]
	s_barrier
	s_add_i32 s59, s59, 2
	s_add_u32 s34, s34, 0x100
	s_addc_u32 s35, s35, 0
	s_cmp_gt_u32 s59, 21
	s_cbranch_scc0 .LBB0_1525
	s_add_u32 s34, s8, 0xffffff00
	s_addc_u32 s35, s9, -1
	s_and_b64 vcc, exec, s[42:43]
	s_cbranch_vccnz .LBB0_1528
	v_mov_b32_e32 v2, 0
	s_mov_b32 s16, s80
	s_mov_b32 s47, s81
	s_mov_b64 s[26:27], s[30:31]
	s_mov_b32 s68, s58
	v_mov_b32_e32 v3, v2
	v_mov_b32_e32 v4, v2
	v_mov_b32_e32 v5, v2
	v_mov_b32_e32 v6, v2
	v_mov_b32_e32 v7, v2
	v_mov_b32_e32 v8, v2
	v_mov_b32_e32 v9, v2
	v_mov_b32_e32 v18, v2
	v_mov_b32_e32 v19, v2
	v_mov_b32_e32 v20, v2
	v_mov_b32_e32 v21, v2
	v_mov_b32_e32 v22, v2
	v_mov_b32_e32 v23, v2
	v_mov_b32_e32 v24, v2
	v_mov_b32_e32 v25, v2
	v_mov_b32_e32 v34, v2
	v_mov_b32_e32 v35, v2
	v_mov_b32_e32 v36, v2
	v_mov_b32_e32 v37, v2
	v_mov_b32_e32 v38, v2
	v_mov_b32_e32 v39, v2
	v_mov_b32_e32 v40, v2
	v_mov_b32_e32 v41, v2
	v_mov_b32_e32 v50, v2
	v_mov_b32_e32 v51, v2
	v_mov_b32_e32 v52, v2
	v_mov_b32_e32 v53, v2
	v_mov_b32_e32 v54, v2
	v_mov_b32_e32 v55, v2
	v_mov_b32_e32 v56, v2
	v_mov_b32_e32 v57, v2
	v_mov_b32_e32 v10, v2
	v_mov_b32_e32 v11, v2
	v_mov_b32_e32 v12, v2
	v_mov_b32_e32 v13, v2
	v_mov_b32_e32 v14, v2
	v_mov_b32_e32 v15, v2
	v_mov_b32_e32 v16, v2
	v_mov_b32_e32 v17, v2
	v_mov_b32_e32 v26, v2
	v_mov_b32_e32 v27, v2
	v_mov_b32_e32 v28, v2
	v_mov_b32_e32 v29, v2
	v_mov_b32_e32 v30, v2
	v_mov_b32_e32 v31, v2
	v_mov_b32_e32 v32, v2
	v_mov_b32_e32 v33, v2
	v_mov_b32_e32 v42, v2
	v_mov_b32_e32 v43, v2
	v_mov_b32_e32 v44, v2
	v_mov_b32_e32 v45, v2
	v_mov_b32_e32 v46, v2
	v_mov_b32_e32 v47, v2
	v_mov_b32_e32 v48, v2
	v_mov_b32_e32 v49, v2
	v_mov_b32_e32 v58, v2
	v_mov_b32_e32 v59, v2
	v_mov_b32_e32 v60, v2
	v_mov_b32_e32 v61, v2
	v_mov_b32_e32 v62, v2
	v_mov_b32_e32 v63, v2
	v_mov_b32_e32 v64, v2
	v_mov_b32_e32 v65, v2
	v_mov_b32_e32 v66, v2
	v_mov_b32_e32 v67, v2
	v_mov_b32_e32 v68, v2
	v_mov_b32_e32 v69, v2
	v_mov_b32_e32 v70, v2
	v_mov_b32_e32 v71, v2
	v_mov_b32_e32 v72, v2
	v_mov_b32_e32 v73, v2
	v_mov_b32_e32 v82, v2
	v_mov_b32_e32 v83, v2
	v_mov_b32_e32 v84, v2
	v_mov_b32_e32 v85, v2
	v_mov_b32_e32 v86, v2
	v_mov_b32_e32 v87, v2
	v_mov_b32_e32 v88, v2
	v_mov_b32_e32 v89, v2
	v_mov_b32_e32 v98, v2
	v_mov_b32_e32 v99, v2
	v_mov_b32_e32 v100, v2
	v_mov_b32_e32 v101, v2
	v_mov_b32_e32 v102, v2
	v_mov_b32_e32 v103, v2
	v_mov_b32_e32 v104, v2
	v_mov_b32_e32 v105, v2
	v_mov_b32_e32 v114, v2
	v_mov_b32_e32 v115, v2
	v_mov_b32_e32 v116, v2
	v_mov_b32_e32 v117, v2
	v_mov_b32_e32 v122, v2
	v_mov_b32_e32 v123, v2
	v_mov_b32_e32 v124, v2
	v_mov_b32_e32 v125, v2
	v_mov_b32_e32 v74, v2
	v_mov_b32_e32 v75, v2
	v_mov_b32_e32 v76, v2
	v_mov_b32_e32 v77, v2
	v_mov_b32_e32 v78, v2
	v_mov_b32_e32 v79, v2
	v_mov_b32_e32 v80, v2
	v_mov_b32_e32 v81, v2
	v_mov_b32_e32 v90, v2
	v_mov_b32_e32 v91, v2
	v_mov_b32_e32 v92, v2
	v_mov_b32_e32 v93, v2
	v_mov_b32_e32 v94, v2
	v_mov_b32_e32 v95, v2
	v_mov_b32_e32 v96, v2
	v_mov_b32_e32 v97, v2
	v_mov_b32_e32 v106, v2
	v_mov_b32_e32 v107, v2
	v_mov_b32_e32 v108, v2
	v_mov_b32_e32 v109, v2
	v_mov_b32_e32 v110, v2
	v_mov_b32_e32 v111, v2
	v_mov_b32_e32 v112, v2
	v_mov_b32_e32 v113, v2
	v_mov_b32_e32 v130, v2
	v_mov_b32_e32 v131, v2
	v_mov_b32_e32 v132, v2
	v_mov_b32_e32 v133, v2
	v_mov_b32_e32 v134, v2
	v_mov_b32_e32 v135, v2
	v_mov_b32_e32 v136, v2
	v_mov_b32_e32 v137, v2
	s_andn2_b64 vcc, exec, s[40:41]
	s_cbranch_vccnz .LBB0_1529
	s_branch .LBB0_1531

.LBB0_1623:
	s_add_u32 s36, s26, s34
	s_addc_u32 s37, s27, s35
	s_add_u32 s36, s36, 0x100
	s_addc_u32 s37, s37, 0
	s_add_u32 s80, s8, s34
	s_addc_u32 s81, s9, s35
	s_add_i32 s82, 0, 0x10000
	s_cmpk_eq_i32 s34, 0xb00
	s_cselect_b32 s43, s31, s37
	s_cselect_b32 s42, s30, s36
	s_cselect_b32 s37, s29, s81
	s_cselect_b32 s36, s28, s80
	s_add_i32 s83, 0, 0x14000
	v_add_u32_e32 v158, s82, v144
	v_add_u32_e32 v167, s83, v144
	ds_read_b128 v[146:149], v158
	ds_read_b128 v[150:153], v158 offset:1024
	ds_read_b128 v[154:157], v158 offset:2048
	ds_read_b128 v[158:161], v158 offset:3072
	ds_read_b128 v[162:165], v167
	ds_read_b128 v[168:171], v167 offset:1024
	ds_read_b128 v[172:175], v167 offset:2048
	ds_read_b128 v[176:179], v167 offset:3072
	v_lshl_add_u64 v[208:209], v[142:143], 0, s[34:35]
	s_add_i32 m0, s4, 0xc000
	ds_read_b128 v[180:183], v145
	ds_read_b128 v[184:187], v145 offset:1024
	ds_read_b128 v[188:191], v145 offset:2048
	ds_read_b128 v[192:195], v145 offset:3072
	ds_read_b128 v[196:199], v145 offset:4096
	ds_read_b128 v[200:203], v145 offset:5120
	ds_read_b128 v[204:207], v145 offset:6144
	ds_read_b128 v[216:219], v145 offset:7168
	global_load_lds_dwordx4 v[208:209], off
	s_add_i32 m0, s4, 0xe000
	v_lshl_add_u64 v[208:209], v[140:141], 0, s[34:35]
	global_load_lds_dwordx4 v[208:209], off
	s_waitcnt vmcnt(8)
	s_waitcnt lgkmcnt(0)
	s_barrier
	s_waitcnt lgkmcnt(0)
	v_mfma_f32_16x16x32_bf16 v[134:137], v[146:149], v[180:183], v[134:137]
	v_mfma_f32_16x16x32_bf16 v[130:133], v[154:157], v[180:183], v[130:133]
	v_mfma_f32_16x16x32_bf16 v[110:113], v[146:149], v[188:191], v[110:113]
	v_mfma_f32_16x16x32_bf16 v[106:109], v[154:157], v[188:191], v[106:109]
	v_mfma_f32_16x16x32_bf16 v[94:97], v[146:149], v[196:199], v[94:97]
	v_mfma_f32_16x16x32_bf16 v[90:93], v[154:157], v[196:199], v[90:93]
	v_mfma_f32_16x16x32_bf16 v[78:81], v[146:149], v[204:207], v[78:81]
	v_mfma_f32_16x16x32_bf16 v[74:77], v[154:157], v[204:207], v[74:77]
	v_mfma_f32_16x16x32_bf16 v[134:137], v[150:153], v[184:187], v[134:137]
	v_mfma_f32_16x16x32_bf16 v[130:133], v[158:161], v[184:187], v[130:133]
	v_mfma_f32_16x16x32_bf16 v[110:113], v[150:153], v[192:195], v[110:113]
	v_mfma_f32_16x16x32_bf16 v[106:109], v[158:161], v[192:195], v[106:109]
	v_mfma_f32_16x16x32_bf16 v[94:97], v[150:153], v[200:203], v[94:97]
	v_mfma_f32_16x16x32_bf16 v[90:93], v[158:161], v[200:203], v[90:93]
	v_mfma_f32_16x16x32_bf16 v[78:81], v[150:153], v[216:219], v[78:81]
	v_mfma_f32_16x16x32_bf16 v[74:77], v[158:161], v[216:219], v[74:77]
	v_mfma_f32_16x16x32_bf16 v[122:125], v[162:165], v[180:183], v[122:125]
	v_mfma_f32_16x16x32_bf16 v[114:117], v[172:175], v[180:183], v[114:117]
	v_mfma_f32_16x16x32_bf16 v[102:105], v[162:165], v[188:191], v[102:105]
	v_mfma_f32_16x16x32_bf16 v[98:101], v[172:175], v[188:191], v[98:101]
	v_mfma_f32_16x16x32_bf16 v[86:89], v[162:165], v[196:199], v[86:89]
	v_mfma_f32_16x16x32_bf16 v[82:85], v[172:175], v[196:199], v[82:85]
	v_mfma_f32_16x16x32_bf16 v[70:73], v[162:165], v[204:207], v[70:73]
	v_mfma_f32_16x16x32_bf16 v[66:69], v[172:175], v[204:207], v[66:69]
	v_mfma_f32_16x16x32_bf16 v[122:125], v[168:171], v[184:187], v[122:125]
	v_mfma_f32_16x16x32_bf16 v[114:117], v[176:179], v[184:187], v[114:117]
	v_mfma_f32_16x16x32_bf16 v[102:105], v[168:171], v[192:195], v[102:105]
	v_mfma_f32_16x16x32_bf16 v[98:101], v[176:179], v[192:195], v[98:101]
	v_mfma_f32_16x16x32_bf16 v[86:89], v[168:171], v[200:203], v[86:89]
	v_mfma_f32_16x16x32_bf16 v[82:85], v[176:179], v[200:203], v[82:85]
	v_mfma_f32_16x16x32_bf16 v[70:73], v[168:171], v[216:219], v[70:73]
	v_mfma_f32_16x16x32_bf16 v[66:69], v[176:179], v[216:219], v[66:69]
	s_barrier
	s_add_i32 s80, s82, s53
	v_lshl_add_u64 v[208:209], s[36:37], 0, v[0:1]
	s_mov_b32 m0, s80
	ds_read_b128 v[180:183], v145 offset:16384
	ds_read_b128 v[184:187], v145 offset:17408
	ds_read_b128 v[188:191], v145 offset:18432
	ds_read_b128 v[192:195], v145 offset:19456
	ds_read_b128 v[196:199], v145 offset:20480
	ds_read_b128 v[200:203], v145 offset:21504
	ds_read_b128 v[204:207], v145 offset:22528
	ds_read_b128 v[216:219], v145 offset:23552
	global_load_lds_dwordx4 v[208:209], off
	s_add_i32 m0, s80, 0x2000
	s_add_u32 s80, s36, 0x60000
	v_lshl_add_u64 v[220:221], s[36:37], 0, v[118:119]
	s_addc_u32 s81, s37, 0
	s_add_i32 s82, s83, s53
	global_load_lds_dwordx4 v[220:221], off
	v_lshl_add_u64 v[222:223], s[80:81], 0, v[0:1]
	s_mov_b32 m0, s82
	v_lshl_add_u64 v[224:225], s[42:43], 0, v[120:121]
	global_load_lds_dwordx4 v[222:223], off
	s_add_i32 m0, s82, 0x2000
	v_lshl_add_u64 v[222:223], s[80:81], 0, v[118:119]
	global_load_lds_dwordx4 v[222:223], off
	s_mov_b32 m0, s4
	v_lshl_add_u64 v[222:223], s[42:43], 0, v[126:127]
	global_load_lds_dwordx4 v[222:223], off
	s_mov_b32 m0, s33
	s_nop 0
	global_load_lds_dwordx4 v[224:225], off
	s_waitcnt vmcnt(8)
	s_waitcnt lgkmcnt(0)
	s_barrier
	s_waitcnt lgkmcnt(0)
	v_mfma_f32_16x16x32_bf16 v[62:65], v[146:149], v[180:183], v[62:65]
	v_mfma_f32_16x16x32_bf16 v[58:61], v[154:157], v[180:183], v[58:61]
	v_mfma_f32_16x16x32_bf16 v[46:49], v[146:149], v[188:191], v[46:49]
	v_mfma_f32_16x16x32_bf16 v[42:45], v[154:157], v[188:191], v[42:45]
	v_mfma_f32_16x16x32_bf16 v[30:33], v[146:149], v[196:199], v[30:33]
	v_mfma_f32_16x16x32_bf16 v[26:29], v[154:157], v[196:199], v[26:29]
	v_mfma_f32_16x16x32_bf16 v[14:17], v[146:149], v[204:207], v[14:17]
	v_mfma_f32_16x16x32_bf16 v[10:13], v[154:157], v[204:207], v[10:13]
	v_mfma_f32_16x16x32_bf16 v[62:65], v[150:153], v[184:187], v[62:65]
	v_mfma_f32_16x16x32_bf16 v[58:61], v[158:161], v[184:187], v[58:61]
	v_mfma_f32_16x16x32_bf16 v[46:49], v[150:153], v[192:195], v[46:49]
	v_mfma_f32_16x16x32_bf16 v[42:45], v[158:161], v[192:195], v[42:45]
	v_mfma_f32_16x16x32_bf16 v[30:33], v[150:153], v[200:203], v[30:33]
	v_mfma_f32_16x16x32_bf16 v[26:29], v[158:161], v[200:203], v[26:29]
	v_mfma_f32_16x16x32_bf16 v[14:17], v[150:153], v[216:219], v[14:17]
	v_mfma_f32_16x16x32_bf16 v[10:13], v[158:161], v[216:219], v[10:13]
	v_mfma_f32_16x16x32_bf16 v[54:57], v[162:165], v[180:183], v[54:57]
	v_mfma_f32_16x16x32_bf16 v[50:53], v[172:175], v[180:183], v[50:53]
	v_mfma_f32_16x16x32_bf16 v[38:41], v[162:165], v[188:191], v[38:41]
	v_mfma_f32_16x16x32_bf16 v[34:37], v[172:175], v[188:191], v[34:37]
	v_mfma_f32_16x16x32_bf16 v[22:25], v[162:165], v[196:199], v[22:25]
	v_mfma_f32_16x16x32_bf16 v[18:21], v[172:175], v[196:199], v[18:21]
	v_mfma_f32_16x16x32_bf16 v[6:9], v[162:165], v[204:207], v[6:9]
	v_mfma_f32_16x16x32_bf16 v[2:5], v[172:175], v[204:207], v[2:5]
	v_mfma_f32_16x16x32_bf16 v[54:57], v[168:171], v[184:187], v[54:57]
	v_mfma_f32_16x16x32_bf16 v[50:53], v[176:179], v[184:187], v[50:53]
	v_mfma_f32_16x16x32_bf16 v[38:41], v[168:171], v[192:195], v[38:41]
	v_mfma_f32_16x16x32_bf16 v[34:37], v[176:179], v[192:195], v[34:37]
	v_mfma_f32_16x16x32_bf16 v[22:25], v[168:171], v[200:203], v[22:25]
	v_mfma_f32_16x16x32_bf16 v[18:21], v[176:179], v[200:203], v[18:21]
	v_mfma_f32_16x16x32_bf16 v[6:9], v[168:171], v[216:219], v[6:9]
	v_mfma_f32_16x16x32_bf16 v[2:5], v[176:179], v[216:219], v[2:5]
	s_barrier
	s_add_i32 s80, 0, 0x18000
	s_add_i32 s81, 0, 0x1c000
	v_add_u32_e32 v158, s80, v144
	v_add_u32_e32 v167, s81, v144
	ds_read_b128 v[146:149], v158
	ds_read_b128 v[150:153], v158 offset:1024
	ds_read_b128 v[154:157], v158 offset:2048
	ds_read_b128 v[158:161], v158 offset:3072
	ds_read_b128 v[162:165], v167
	ds_read_b128 v[168:171], v167 offset:1024
	ds_read_b128 v[172:175], v167 offset:2048
	ds_read_b128 v[176:179], v167 offset:3072
	s_add_u32 s42, s42, 0x60000
	s_addc_u32 s43, s43, 0
	s_mov_b32 m0, s62
	v_lshl_add_u64 v[242:243], s[42:43], 0, v[126:127]
	ds_read_b128 v[180:183], v145 offset:32768
	ds_read_b128 v[184:187], v145 offset:33792
	ds_read_b128 v[188:191], v145 offset:34816
	ds_read_b128 v[192:195], v145 offset:35840
	ds_read_b128 v[196:199], v145 offset:36864
	ds_read_b128 v[200:203], v145 offset:37888
	ds_read_b128 v[204:207], v145 offset:38912
	ds_read_b128 v[216:219], v145 offset:39936
	global_load_lds_dwordx4 v[242:243], off
	s_mov_b32 m0, s63
	v_lshl_add_u64 v[242:243], s[42:43], 0, v[120:121]
	global_load_lds_dwordx4 v[242:243], off
	s_waitcnt vmcnt(8)
	s_waitcnt lgkmcnt(0)
	s_barrier
	s_waitcnt lgkmcnt(0)
	v_mfma_f32_16x16x32_bf16 v[134:137], v[146:149], v[180:183], v[134:137]
	v_mfma_f32_16x16x32_bf16 v[130:133], v[154:157], v[180:183], v[130:133]
	v_mfma_f32_16x16x32_bf16 v[110:113], v[146:149], v[188:191], v[110:113]
	v_mfma_f32_16x16x32_bf16 v[106:109], v[154:157], v[188:191], v[106:109]
	v_mfma_f32_16x16x32_bf16 v[94:97], v[146:149], v[196:199], v[94:97]
	v_mfma_f32_16x16x32_bf16 v[90:93], v[154:157], v[196:199], v[90:93]
	v_mfma_f32_16x16x32_bf16 v[78:81], v[146:149], v[204:207], v[78:81]
	v_mfma_f32_16x16x32_bf16 v[74:77], v[154:157], v[204:207], v[74:77]
	v_mfma_f32_16x16x32_bf16 v[134:137], v[150:153], v[184:187], v[134:137]
	v_mfma_f32_16x16x32_bf16 v[130:133], v[158:161], v[184:187], v[130:133]
	v_mfma_f32_16x16x32_bf16 v[110:113], v[150:153], v[192:195], v[110:113]
	v_mfma_f32_16x16x32_bf16 v[106:109], v[158:161], v[192:195], v[106:109]
	v_mfma_f32_16x16x32_bf16 v[94:97], v[150:153], v[200:203], v[94:97]
	v_mfma_f32_16x16x32_bf16 v[90:93], v[158:161], v[200:203], v[90:93]
	v_mfma_f32_16x16x32_bf16 v[78:81], v[150:153], v[216:219], v[78:81]
	v_mfma_f32_16x16x32_bf16 v[74:77], v[158:161], v[216:219], v[74:77]
	v_mfma_f32_16x16x32_bf16 v[122:125], v[162:165], v[180:183], v[122:125]
	v_mfma_f32_16x16x32_bf16 v[114:117], v[172:175], v[180:183], v[114:117]
	v_mfma_f32_16x16x32_bf16 v[102:105], v[162:165], v[188:191], v[102:105]
	v_mfma_f32_16x16x32_bf16 v[98:101], v[172:175], v[188:191], v[98:101]
	v_mfma_f32_16x16x32_bf16 v[86:89], v[162:165], v[196:199], v[86:89]
	v_mfma_f32_16x16x32_bf16 v[82:85], v[172:175], v[196:199], v[82:85]
	v_mfma_f32_16x16x32_bf16 v[70:73], v[162:165], v[204:207], v[70:73]
	v_mfma_f32_16x16x32_bf16 v[66:69], v[172:175], v[204:207], v[66:69]
	v_mfma_f32_16x16x32_bf16 v[122:125], v[168:171], v[184:187], v[122:125]
	v_mfma_f32_16x16x32_bf16 v[114:117], v[176:179], v[184:187], v[114:117]
	v_mfma_f32_16x16x32_bf16 v[102:105], v[168:171], v[192:195], v[102:105]
	v_mfma_f32_16x16x32_bf16 v[98:101], v[176:179], v[192:195], v[98:101]
	v_mfma_f32_16x16x32_bf16 v[86:89], v[168:171], v[200:203], v[86:89]
	v_mfma_f32_16x16x32_bf16 v[82:85], v[176:179], v[200:203], v[82:85]
	v_mfma_f32_16x16x32_bf16 v[70:73], v[168:171], v[216:219], v[70:73]
	v_mfma_f32_16x16x32_bf16 v[66:69], v[176:179], v[216:219], v[66:69]
	s_barrier
	s_add_i32 s42, s80, s53
	v_lshl_add_u64 v[208:209], v[208:209], 0, s[56:57]
	s_mov_b32 m0, s42
	ds_read_b128 v[180:183], v145 offset:49152
	ds_read_b128 v[184:187], v145 offset:50176
	ds_read_b128 v[188:191], v145 offset:51200
	ds_read_b128 v[192:195], v145 offset:52224
	ds_read_b128 v[196:199], v145 offset:53248
	ds_read_b128 v[200:203], v145 offset:54272
	ds_read_b128 v[204:207], v145 offset:55296
	ds_read_b128 v[216:219], v145 offset:56320
	global_load_lds_dwordx4 v[208:209], off
	s_add_i32 m0, s42, 0x2000
	s_add_u32 s36, s36, 0x60080
	v_lshl_add_u64 v[208:209], v[220:221], 0, s[56:57]
	s_addc_u32 s37, s37, 0
	s_add_i32 s42, s81, s53
	global_load_lds_dwordx4 v[208:209], off
	s_mov_b32 m0, s42
	v_lshl_add_u64 v[208:209], s[36:37], 0, v[0:1]
	global_load_lds_dwordx4 v[208:209], off
	s_add_i32 m0, s42, 0x2000
	v_lshl_add_u64 v[208:209], s[36:37], 0, v[118:119]
	global_load_lds_dwordx4 v[208:209], off
	s_mov_b32 m0, s70
	v_lshl_add_u64 v[208:209], v[222:223], 0, s[56:57]
	global_load_lds_dwordx4 v[208:209], off
	s_mov_b32 m0, s71
	v_lshl_add_u64 v[208:209], v[224:225], 0, s[56:57]
	global_load_lds_dwordx4 v[208:209], off
	s_waitcnt vmcnt(8)
	s_waitcnt lgkmcnt(0)
	s_barrier
	s_waitcnt lgkmcnt(0)
	v_mfma_f32_16x16x32_bf16 v[62:65], v[146:149], v[180:183], v[62:65]
	v_mfma_f32_16x16x32_bf16 v[58:61], v[154:157], v[180:183], v[58:61]
	v_mfma_f32_16x16x32_bf16 v[46:49], v[146:149], v[188:191], v[46:49]
	v_mfma_f32_16x16x32_bf16 v[42:45], v[154:157], v[188:191], v[42:45]
	v_mfma_f32_16x16x32_bf16 v[30:33], v[146:149], v[196:199], v[30:33]
	v_mfma_f32_16x16x32_bf16 v[26:29], v[154:157], v[196:199], v[26:29]
	v_mfma_f32_16x16x32_bf16 v[14:17], v[146:149], v[204:207], v[14:17]
	v_mfma_f32_16x16x32_bf16 v[10:13], v[154:157], v[204:207], v[10:13]
	v_mfma_f32_16x16x32_bf16 v[62:65], v[150:153], v[184:187], v[62:65]
	v_mfma_f32_16x16x32_bf16 v[58:61], v[158:161], v[184:187], v[58:61]
	v_mfma_f32_16x16x32_bf16 v[46:49], v[150:153], v[192:195], v[46:49]
	v_mfma_f32_16x16x32_bf16 v[42:45], v[158:161], v[192:195], v[42:45]
	v_mfma_f32_16x16x32_bf16 v[30:33], v[150:153], v[200:203], v[30:33]
	v_mfma_f32_16x16x32_bf16 v[26:29], v[158:161], v[200:203], v[26:29]
	v_mfma_f32_16x16x32_bf16 v[14:17], v[150:153], v[216:219], v[14:17]
	v_mfma_f32_16x16x32_bf16 v[10:13], v[158:161], v[216:219], v[10:13]
	v_mfma_f32_16x16x32_bf16 v[54:57], v[162:165], v[180:183], v[54:57]
	v_mfma_f32_16x16x32_bf16 v[50:53], v[172:175], v[180:183], v[50:53]
	v_mfma_f32_16x16x32_bf16 v[38:41], v[162:165], v[188:191], v[38:41]
	v_mfma_f32_16x16x32_bf16 v[34:37], v[172:175], v[188:191], v[34:37]
	v_mfma_f32_16x16x32_bf16 v[22:25], v[162:165], v[196:199], v[22:25]
	v_mfma_f32_16x16x32_bf16 v[18:21], v[172:175], v[196:199], v[18:21]
	v_mfma_f32_16x16x32_bf16 v[6:9], v[162:165], v[204:207], v[6:9]
	v_mfma_f32_16x16x32_bf16 v[2:5], v[172:175], v[204:207], v[2:5]
	v_mfma_f32_16x16x32_bf16 v[54:57], v[168:171], v[184:187], v[54:57]
	v_mfma_f32_16x16x32_bf16 v[50:53], v[176:179], v[184:187], v[50:53]
	v_mfma_f32_16x16x32_bf16 v[38:41], v[168:171], v[192:195], v[38:41]
	v_mfma_f32_16x16x32_bf16 v[34:37], v[176:179], v[192:195], v[34:37]
	v_mfma_f32_16x16x32_bf16 v[22:25], v[168:171], v[200:203], v[22:25]
	v_mfma_f32_16x16x32_bf16 v[18:21], v[176:179], v[200:203], v[18:21]
	v_mfma_f32_16x16x32_bf16 v[6:9], v[168:171], v[216:219], v[6:9]
	v_mfma_f32_16x16x32_bf16 v[2:5], v[176:179], v[216:219], v[2:5]
	s_barrier
	s_add_i32 s59, s59, 2
	s_add_u32 s34, s34, 0x100
	s_addc_u32 s35, s35, 0
	s_cmp_gt_u32 s59, 21
	s_cbranch_scc0 .LBB0_1623
	s_add_u32 s34, s8, 0xffffff00
	s_addc_u32 s35, s9, -1
	s_and_b64 vcc, exec, s[40:41]
	s_cbranch_vccnz .LBB0_1626
	v_mov_b32_e32 v2, 0
	s_mov_b32 s16, s77
	s_mov_b32 s76, s79
	s_mov_b64 s[26:27], s[30:31]
	s_mov_b32 s68, s58
	v_mov_b32_e32 v3, v2
	v_mov_b32_e32 v4, v2
	v_mov_b32_e32 v5, v2
	v_mov_b32_e32 v6, v2
	v_mov_b32_e32 v7, v2
	v_mov_b32_e32 v8, v2
	v_mov_b32_e32 v9, v2
	v_mov_b32_e32 v18, v2
	v_mov_b32_e32 v19, v2
	v_mov_b32_e32 v20, v2
	v_mov_b32_e32 v21, v2
	v_mov_b32_e32 v22, v2
	v_mov_b32_e32 v23, v2
	v_mov_b32_e32 v24, v2
	v_mov_b32_e32 v25, v2
	v_mov_b32_e32 v34, v2
	v_mov_b32_e32 v35, v2
	v_mov_b32_e32 v36, v2
	v_mov_b32_e32 v37, v2
	v_mov_b32_e32 v38, v2
	v_mov_b32_e32 v39, v2
	v_mov_b32_e32 v40, v2
	v_mov_b32_e32 v41, v2
	v_mov_b32_e32 v50, v2
	v_mov_b32_e32 v51, v2
	v_mov_b32_e32 v52, v2
	v_mov_b32_e32 v53, v2
	v_mov_b32_e32 v54, v2
	v_mov_b32_e32 v55, v2
	v_mov_b32_e32 v56, v2
	v_mov_b32_e32 v57, v2
	v_mov_b32_e32 v10, v2
	v_mov_b32_e32 v11, v2
	v_mov_b32_e32 v12, v2
	v_mov_b32_e32 v13, v2
	v_mov_b32_e32 v14, v2
	v_mov_b32_e32 v15, v2
	v_mov_b32_e32 v16, v2
	v_mov_b32_e32 v17, v2
	v_mov_b32_e32 v26, v2
	v_mov_b32_e32 v27, v2
	v_mov_b32_e32 v28, v2
	v_mov_b32_e32 v29, v2
	v_mov_b32_e32 v30, v2
	v_mov_b32_e32 v31, v2
	v_mov_b32_e32 v32, v2
	v_mov_b32_e32 v33, v2
	v_mov_b32_e32 v42, v2
	v_mov_b32_e32 v43, v2
	v_mov_b32_e32 v44, v2
	v_mov_b32_e32 v45, v2
	v_mov_b32_e32 v46, v2
	v_mov_b32_e32 v47, v2
	v_mov_b32_e32 v48, v2
	v_mov_b32_e32 v49, v2
	v_mov_b32_e32 v58, v2
	v_mov_b32_e32 v59, v2
	v_mov_b32_e32 v60, v2
	v_mov_b32_e32 v61, v2
	v_mov_b32_e32 v62, v2
	v_mov_b32_e32 v63, v2
	v_mov_b32_e32 v64, v2
	v_mov_b32_e32 v65, v2
	v_mov_b32_e32 v66, v2
	v_mov_b32_e32 v67, v2
	v_mov_b32_e32 v68, v2
	v_mov_b32_e32 v69, v2
	v_mov_b32_e32 v70, v2
	v_mov_b32_e32 v71, v2
	v_mov_b32_e32 v72, v2
	v_mov_b32_e32 v73, v2
	v_mov_b32_e32 v82, v2
	v_mov_b32_e32 v83, v2
	v_mov_b32_e32 v84, v2
	v_mov_b32_e32 v85, v2
	v_mov_b32_e32 v86, v2
	v_mov_b32_e32 v87, v2
	v_mov_b32_e32 v88, v2
	v_mov_b32_e32 v89, v2
	v_mov_b32_e32 v98, v2
	v_mov_b32_e32 v99, v2
	v_mov_b32_e32 v100, v2
	v_mov_b32_e32 v101, v2
	v_mov_b32_e32 v102, v2
	v_mov_b32_e32 v103, v2
	v_mov_b32_e32 v104, v2
	v_mov_b32_e32 v105, v2
	v_mov_b32_e32 v114, v2
	v_mov_b32_e32 v115, v2
	v_mov_b32_e32 v116, v2
	v_mov_b32_e32 v117, v2
	v_mov_b32_e32 v122, v2
	v_mov_b32_e32 v123, v2
	v_mov_b32_e32 v124, v2
	v_mov_b32_e32 v125, v2
	v_mov_b32_e32 v74, v2
	v_mov_b32_e32 v75, v2
	v_mov_b32_e32 v76, v2
	v_mov_b32_e32 v77, v2
	v_mov_b32_e32 v78, v2
	v_mov_b32_e32 v79, v2
	v_mov_b32_e32 v80, v2
	v_mov_b32_e32 v81, v2
	v_mov_b32_e32 v90, v2
	v_mov_b32_e32 v91, v2
	v_mov_b32_e32 v92, v2
	v_mov_b32_e32 v93, v2
	v_mov_b32_e32 v94, v2
	v_mov_b32_e32 v95, v2
	v_mov_b32_e32 v96, v2
	v_mov_b32_e32 v97, v2
	v_mov_b32_e32 v106, v2
	v_mov_b32_e32 v107, v2
	v_mov_b32_e32 v108, v2
	v_mov_b32_e32 v109, v2
	v_mov_b32_e32 v110, v2
	v_mov_b32_e32 v111, v2
	v_mov_b32_e32 v112, v2
	v_mov_b32_e32 v113, v2
	v_mov_b32_e32 v130, v2
	v_mov_b32_e32 v131, v2
	v_mov_b32_e32 v132, v2
	v_mov_b32_e32 v133, v2
	v_mov_b32_e32 v134, v2
	v_mov_b32_e32 v135, v2
	v_mov_b32_e32 v136, v2
	v_mov_b32_e32 v137, v2
	s_andn2_b64 vcc, exec, s[38:39]
	s_cbranch_vccnz .LBB0_1627
	s_branch .LBB0_1628

.LBB0_1783:
	s_add_u32 s28, s6, 0xfffc0080
	s_addc_u32 s29, s7, -1
	s_add_i32 s53, 0, 0x10000
	s_cmp_eq_u32 s41, 12
	s_cselect_b32 s31, s8, s29
	s_cselect_b32 s30, s9, s28
	s_cselect_b32 s29, s21, s40
	s_cselect_b32 s28, s23, s33
	s_add_i32 s62, 0, 0x14000
	v_add_u32_e32 v142, s53, v181
	v_add_u32_e32 v168, s62, v181
	ds_read_b128 v[130:133], v142
	ds_read_b128 v[134:137], v142 offset:1024
	ds_read_b128 v[138:141], v142 offset:2048
	ds_read_b128 v[142:145], v142 offset:3072
	ds_read_b128 v[146:149], v168
	ds_read_b128 v[150:153], v168 offset:1024
	ds_read_b128 v[154:157], v168 offset:2048
	ds_read_b128 v[168:171], v168 offset:3072
	v_lshl_add_u64 v[176:177], s[6:7], 0, v[166:167]
	s_add_i32 m0, s37, 0xc000
	ds_read_b128 v[172:175], v183
	ds_read_b128 v[184:187], v183 offset:1024
	ds_read_b128 v[188:191], v183 offset:2048
	ds_read_b128 v[192:195], v183 offset:3072
	ds_read_b128 v[196:199], v183 offset:4096
	ds_read_b128 v[200:203], v183 offset:5120
	ds_read_b128 v[204:207], v183 offset:6144
	ds_read_b128 v[216:219], v183 offset:7168
	global_load_lds_dwordx4 v[176:177], off
	s_add_i32 m0, s37, 0xe000
	v_lshl_add_u64 v[176:177], s[6:7], 0, v[164:165]
	global_load_lds_dwordx4 v[176:177], off
	s_waitcnt vmcnt(8)
	s_waitcnt lgkmcnt(0)
	s_barrier
	s_waitcnt lgkmcnt(0)
	v_mfma_f32_16x16x32_bf16 v[126:129], v[130:133], v[172:175], v[126:129]
	v_mfma_f32_16x16x32_bf16 v[122:125], v[138:141], v[172:175], v[122:125]
	v_mfma_f32_16x16x32_bf16 v[114:117], v[130:133], v[188:191], v[114:117]
	v_mfma_f32_16x16x32_bf16 v[106:109], v[138:141], v[188:191], v[106:109]
	v_mfma_f32_16x16x32_bf16 v[98:101], v[130:133], v[196:199], v[98:101]
	v_mfma_f32_16x16x32_bf16 v[90:93], v[138:141], v[196:199], v[90:93]
	v_mfma_f32_16x16x32_bf16 v[82:85], v[130:133], v[204:207], v[82:85]
	v_mfma_f32_16x16x32_bf16 v[74:77], v[138:141], v[204:207], v[74:77]
	v_mfma_f32_16x16x32_bf16 v[126:129], v[134:137], v[184:187], v[126:129]
	v_mfma_f32_16x16x32_bf16 v[122:125], v[142:145], v[184:187], v[122:125]
	v_mfma_f32_16x16x32_bf16 v[114:117], v[134:137], v[192:195], v[114:117]
	v_mfma_f32_16x16x32_bf16 v[106:109], v[142:145], v[192:195], v[106:109]
	v_mfma_f32_16x16x32_bf16 v[98:101], v[134:137], v[200:203], v[98:101]
	v_mfma_f32_16x16x32_bf16 v[90:93], v[142:145], v[200:203], v[90:93]
	v_mfma_f32_16x16x32_bf16 v[82:85], v[134:137], v[216:219], v[82:85]
	v_mfma_f32_16x16x32_bf16 v[74:77], v[142:145], v[216:219], v[74:77]
	v_mfma_f32_16x16x32_bf16 v[118:121], v[146:149], v[172:175], v[118:121]
	v_mfma_f32_16x16x32_bf16 v[110:113], v[154:157], v[172:175], v[110:113]
	v_mfma_f32_16x16x32_bf16 v[102:105], v[146:149], v[188:191], v[102:105]
	v_mfma_f32_16x16x32_bf16 v[94:97], v[154:157], v[188:191], v[94:97]
	v_mfma_f32_16x16x32_bf16 v[86:89], v[146:149], v[196:199], v[86:89]
	v_mfma_f32_16x16x32_bf16 v[78:81], v[154:157], v[196:199], v[78:81]
	v_mfma_f32_16x16x32_bf16 v[70:73], v[146:149], v[204:207], v[70:73]
	v_mfma_f32_16x16x32_bf16 v[66:69], v[154:157], v[204:207], v[66:69]
	v_mfma_f32_16x16x32_bf16 v[118:121], v[150:153], v[184:187], v[118:121]
	v_mfma_f32_16x16x32_bf16 v[110:113], v[168:171], v[184:187], v[110:113]
	v_mfma_f32_16x16x32_bf16 v[102:105], v[150:153], v[192:195], v[102:105]
	v_mfma_f32_16x16x32_bf16 v[94:97], v[168:171], v[192:195], v[94:97]
	v_mfma_f32_16x16x32_bf16 v[86:89], v[150:153], v[200:203], v[86:89]
	v_mfma_f32_16x16x32_bf16 v[78:81], v[168:171], v[200:203], v[78:81]
	v_mfma_f32_16x16x32_bf16 v[70:73], v[150:153], v[216:219], v[70:73]
	v_mfma_f32_16x16x32_bf16 v[66:69], v[168:171], v[216:219], v[66:69]
	s_barrier
	s_add_i32 s53, s53, s36
	v_lshl_add_u64 v[176:177], s[28:29], 0, v[162:163]
	s_mov_b32 m0, s53
	ds_read_b128 v[172:175], v183 offset:16384
	ds_read_b128 v[184:187], v183 offset:17408
	ds_read_b128 v[188:191], v183 offset:18432
	ds_read_b128 v[192:195], v183 offset:19456
	ds_read_b128 v[196:199], v183 offset:20480
	ds_read_b128 v[200:203], v183 offset:21504
	ds_read_b128 v[204:207], v183 offset:22528
	ds_read_b128 v[216:219], v183 offset:23552
	global_load_lds_dwordx4 v[176:177], off
	s_add_i32 m0, s53, 0x2000
	s_add_u32 s58, s28, 0x40000
	v_lshl_add_u64 v[208:209], s[28:29], 0, v[158:159]
	s_addc_u32 s59, s29, 0
	s_add_i32 s53, s62, s36
	global_load_lds_dwordx4 v[208:209], off
	v_lshl_add_u64 v[220:221], s[58:59], 0, v[162:163]
	s_mov_b32 m0, s53
	v_lshl_add_u64 v[222:223], s[30:31], 0, v[160:161]
	global_load_lds_dwordx4 v[220:221], off
	s_add_i32 m0, s53, 0x2000
	v_lshl_add_u64 v[220:221], s[58:59], 0, v[158:159]
	global_load_lds_dwordx4 v[220:221], off
	s_mov_b32 m0, s37
	v_lshl_add_u64 v[220:221], s[30:31], 0, v[0:1]
	global_load_lds_dwordx4 v[220:221], off
	s_mov_b32 m0, s44
	s_nop 0
	global_load_lds_dwordx4 v[222:223], off
	s_waitcnt vmcnt(8)
	s_waitcnt lgkmcnt(0)
	s_barrier
	s_waitcnt lgkmcnt(0)
	v_mfma_f32_16x16x32_bf16 v[62:65], v[130:133], v[172:175], v[62:65]
	v_mfma_f32_16x16x32_bf16 v[58:61], v[138:141], v[172:175], v[58:61]
	v_mfma_f32_16x16x32_bf16 v[50:53], v[130:133], v[188:191], v[50:53]
	v_mfma_f32_16x16x32_bf16 v[42:45], v[138:141], v[188:191], v[42:45]
	v_mfma_f32_16x16x32_bf16 v[34:37], v[130:133], v[196:199], v[34:37]
	v_mfma_f32_16x16x32_bf16 v[26:29], v[138:141], v[196:199], v[26:29]
	v_mfma_f32_16x16x32_bf16 v[18:21], v[130:133], v[204:207], v[18:21]
	v_mfma_f32_16x16x32_bf16 v[10:13], v[138:141], v[204:207], v[10:13]
	v_mfma_f32_16x16x32_bf16 v[62:65], v[134:137], v[184:187], v[62:65]
	v_mfma_f32_16x16x32_bf16 v[58:61], v[142:145], v[184:187], v[58:61]
	v_mfma_f32_16x16x32_bf16 v[50:53], v[134:137], v[192:195], v[50:53]
	v_mfma_f32_16x16x32_bf16 v[42:45], v[142:145], v[192:195], v[42:45]
	v_mfma_f32_16x16x32_bf16 v[34:37], v[134:137], v[200:203], v[34:37]
	v_mfma_f32_16x16x32_bf16 v[26:29], v[142:145], v[200:203], v[26:29]
	v_mfma_f32_16x16x32_bf16 v[18:21], v[134:137], v[216:219], v[18:21]
	v_mfma_f32_16x16x32_bf16 v[10:13], v[142:145], v[216:219], v[10:13]
	v_mfma_f32_16x16x32_bf16 v[54:57], v[146:149], v[172:175], v[54:57]
	v_mfma_f32_16x16x32_bf16 v[46:49], v[154:157], v[172:175], v[46:49]
	v_mfma_f32_16x16x32_bf16 v[38:41], v[146:149], v[188:191], v[38:41]
	v_mfma_f32_16x16x32_bf16 v[30:33], v[154:157], v[188:191], v[30:33]
	v_mfma_f32_16x16x32_bf16 v[22:25], v[146:149], v[196:199], v[22:25]
	v_mfma_f32_16x16x32_bf16 v[14:17], v[154:157], v[196:199], v[14:17]
	v_mfma_f32_16x16x32_bf16 v[6:9], v[146:149], v[204:207], v[6:9]
	v_mfma_f32_16x16x32_bf16 v[2:5], v[154:157], v[204:207], v[2:5]
	v_mfma_f32_16x16x32_bf16 v[54:57], v[150:153], v[184:187], v[54:57]
	v_mfma_f32_16x16x32_bf16 v[46:49], v[168:171], v[184:187], v[46:49]
	v_mfma_f32_16x16x32_bf16 v[38:41], v[150:153], v[192:195], v[38:41]
	v_mfma_f32_16x16x32_bf16 v[30:33], v[168:171], v[192:195], v[30:33]
	v_mfma_f32_16x16x32_bf16 v[22:25], v[150:153], v[200:203], v[22:25]
	v_mfma_f32_16x16x32_bf16 v[14:17], v[168:171], v[200:203], v[14:17]
	v_mfma_f32_16x16x32_bf16 v[6:9], v[150:153], v[216:219], v[6:9]
	v_mfma_f32_16x16x32_bf16 v[2:5], v[168:171], v[216:219], v[2:5]
	s_barrier
	s_add_i32 s53, 0, 0x18000
	s_add_i32 s58, 0, 0x1c000
	v_add_u32_e32 v142, s53, v181
	v_add_u32_e32 v168, s58, v181
	ds_read_b128 v[130:133], v142
	ds_read_b128 v[134:137], v142 offset:1024
	ds_read_b128 v[138:141], v142 offset:2048
	ds_read_b128 v[142:145], v142 offset:3072
	ds_read_b128 v[146:149], v168
	ds_read_b128 v[150:153], v168 offset:1024
	ds_read_b128 v[154:157], v168 offset:2048
	ds_read_b128 v[168:171], v168 offset:3072
	s_add_u32 s30, s30, 0x40000
	s_addc_u32 s31, s31, 0
	s_mov_b32 m0, s45
	v_lshl_add_u64 v[224:225], s[30:31], 0, v[0:1]
	ds_read_b128 v[172:175], v183 offset:32768
	ds_read_b128 v[184:187], v183 offset:33792
	ds_read_b128 v[188:191], v183 offset:34816
	ds_read_b128 v[192:195], v183 offset:35840
	ds_read_b128 v[196:199], v183 offset:36864
	ds_read_b128 v[200:203], v183 offset:37888
	ds_read_b128 v[204:207], v183 offset:38912
	ds_read_b128 v[216:219], v183 offset:39936
	global_load_lds_dwordx4 v[224:225], off
	s_mov_b32 m0, s46
	v_lshl_add_u64 v[224:225], s[30:31], 0, v[160:161]
	global_load_lds_dwordx4 v[224:225], off
	s_waitcnt vmcnt(8)
	s_waitcnt lgkmcnt(0)
	s_barrier
	s_waitcnt lgkmcnt(0)
	v_mfma_f32_16x16x32_bf16 v[126:129], v[130:133], v[172:175], v[126:129]
	v_mfma_f32_16x16x32_bf16 v[122:125], v[138:141], v[172:175], v[122:125]
	v_mfma_f32_16x16x32_bf16 v[114:117], v[130:133], v[188:191], v[114:117]
	v_mfma_f32_16x16x32_bf16 v[106:109], v[138:141], v[188:191], v[106:109]
	v_mfma_f32_16x16x32_bf16 v[98:101], v[130:133], v[196:199], v[98:101]
	v_mfma_f32_16x16x32_bf16 v[90:93], v[138:141], v[196:199], v[90:93]
	v_mfma_f32_16x16x32_bf16 v[82:85], v[130:133], v[204:207], v[82:85]
	v_mfma_f32_16x16x32_bf16 v[74:77], v[138:141], v[204:207], v[74:77]
	v_mfma_f32_16x16x32_bf16 v[126:129], v[134:137], v[184:187], v[126:129]
	v_mfma_f32_16x16x32_bf16 v[122:125], v[142:145], v[184:187], v[122:125]
	v_mfma_f32_16x16x32_bf16 v[114:117], v[134:137], v[192:195], v[114:117]
	v_mfma_f32_16x16x32_bf16 v[106:109], v[142:145], v[192:195], v[106:109]
	v_mfma_f32_16x16x32_bf16 v[98:101], v[134:137], v[200:203], v[98:101]
	v_mfma_f32_16x16x32_bf16 v[90:93], v[142:145], v[200:203], v[90:93]
	v_mfma_f32_16x16x32_bf16 v[82:85], v[134:137], v[216:219], v[82:85]
	v_mfma_f32_16x16x32_bf16 v[74:77], v[142:145], v[216:219], v[74:77]
	v_mfma_f32_16x16x32_bf16 v[118:121], v[146:149], v[172:175], v[118:121]
	v_mfma_f32_16x16x32_bf16 v[110:113], v[154:157], v[172:175], v[110:113]
	v_mfma_f32_16x16x32_bf16 v[102:105], v[146:149], v[188:191], v[102:105]
	v_mfma_f32_16x16x32_bf16 v[94:97], v[154:157], v[188:191], v[94:97]
	v_mfma_f32_16x16x32_bf16 v[86:89], v[146:149], v[196:199], v[86:89]
	v_mfma_f32_16x16x32_bf16 v[78:81], v[154:157], v[196:199], v[78:81]
	v_mfma_f32_16x16x32_bf16 v[70:73], v[146:149], v[204:207], v[70:73]
	v_mfma_f32_16x16x32_bf16 v[66:69], v[154:157], v[204:207], v[66:69]
	v_mfma_f32_16x16x32_bf16 v[118:121], v[150:153], v[184:187], v[118:121]
	v_mfma_f32_16x16x32_bf16 v[110:113], v[168:171], v[184:187], v[110:113]
	v_mfma_f32_16x16x32_bf16 v[102:105], v[150:153], v[192:195], v[102:105]
	v_mfma_f32_16x16x32_bf16 v[94:97], v[168:171], v[192:195], v[94:97]
	v_mfma_f32_16x16x32_bf16 v[86:89], v[150:153], v[200:203], v[86:89]
	v_mfma_f32_16x16x32_bf16 v[78:81], v[168:171], v[200:203], v[78:81]
	v_mfma_f32_16x16x32_bf16 v[70:73], v[150:153], v[216:219], v[70:73]
	v_mfma_f32_16x16x32_bf16 v[66:69], v[168:171], v[216:219], v[66:69]
	s_barrier
	s_add_i32 s30, s53, s36
	v_lshl_add_u64 v[176:177], v[176:177], 0, s[56:57]
	s_mov_b32 m0, s30
	ds_read_b128 v[172:175], v183 offset:49152
	ds_read_b128 v[184:187], v183 offset:50176
	ds_read_b128 v[188:191], v183 offset:51200
	ds_read_b128 v[192:195], v183 offset:52224
	ds_read_b128 v[196:199], v183 offset:53248
	ds_read_b128 v[200:203], v183 offset:54272
	ds_read_b128 v[204:207], v183 offset:55296
	ds_read_b128 v[216:219], v183 offset:56320
	global_load_lds_dwordx4 v[176:177], off
	s_add_i32 m0, s30, 0x2000
	s_add_u32 s28, s28, 0x40080
	v_lshl_add_u64 v[176:177], v[208:209], 0, s[56:57]
	s_addc_u32 s29, s29, 0
	s_add_i32 s30, s58, s36
	global_load_lds_dwordx4 v[176:177], off
	s_mov_b32 m0, s30
	v_lshl_add_u64 v[176:177], s[28:29], 0, v[162:163]
	global_load_lds_dwordx4 v[176:177], off
	s_add_i32 m0, s30, 0x2000
	v_lshl_add_u64 v[176:177], s[28:29], 0, v[158:159]
	global_load_lds_dwordx4 v[176:177], off
	s_mov_b32 m0, s47
	v_lshl_add_u64 v[176:177], v[220:221], 0, s[56:57]
	global_load_lds_dwordx4 v[176:177], off
	s_mov_b32 m0, s48
	v_lshl_add_u64 v[176:177], v[222:223], 0, s[56:57]
	global_load_lds_dwordx4 v[176:177], off
	s_waitcnt vmcnt(8)
	s_waitcnt lgkmcnt(0)
	s_barrier
	s_waitcnt lgkmcnt(0)
	v_mfma_f32_16x16x32_bf16 v[62:65], v[130:133], v[172:175], v[62:65]
	v_mfma_f32_16x16x32_bf16 v[58:61], v[138:141], v[172:175], v[58:61]
	v_mfma_f32_16x16x32_bf16 v[50:53], v[130:133], v[188:191], v[50:53]
	v_mfma_f32_16x16x32_bf16 v[42:45], v[138:141], v[188:191], v[42:45]
	v_mfma_f32_16x16x32_bf16 v[34:37], v[130:133], v[196:199], v[34:37]
	v_mfma_f32_16x16x32_bf16 v[26:29], v[138:141], v[196:199], v[26:29]
	v_mfma_f32_16x16x32_bf16 v[18:21], v[130:133], v[204:207], v[18:21]
	v_mfma_f32_16x16x32_bf16 v[10:13], v[138:141], v[204:207], v[10:13]
	v_mfma_f32_16x16x32_bf16 v[62:65], v[134:137], v[184:187], v[62:65]
	v_mfma_f32_16x16x32_bf16 v[58:61], v[142:145], v[184:187], v[58:61]
	v_mfma_f32_16x16x32_bf16 v[50:53], v[134:137], v[192:195], v[50:53]
	v_mfma_f32_16x16x32_bf16 v[42:45], v[142:145], v[192:195], v[42:45]
	v_mfma_f32_16x16x32_bf16 v[34:37], v[134:137], v[200:203], v[34:37]
	v_mfma_f32_16x16x32_bf16 v[26:29], v[142:145], v[200:203], v[26:29]
	v_mfma_f32_16x16x32_bf16 v[18:21], v[134:137], v[216:219], v[18:21]
	v_mfma_f32_16x16x32_bf16 v[10:13], v[142:145], v[216:219], v[10:13]
	v_mfma_f32_16x16x32_bf16 v[54:57], v[146:149], v[172:175], v[54:57]
	v_mfma_f32_16x16x32_bf16 v[46:49], v[154:157], v[172:175], v[46:49]
	v_mfma_f32_16x16x32_bf16 v[38:41], v[146:149], v[188:191], v[38:41]
	v_mfma_f32_16x16x32_bf16 v[30:33], v[154:157], v[188:191], v[30:33]
	v_mfma_f32_16x16x32_bf16 v[22:25], v[146:149], v[196:199], v[22:25]
	v_mfma_f32_16x16x32_bf16 v[14:17], v[154:157], v[196:199], v[14:17]
	v_mfma_f32_16x16x32_bf16 v[6:9], v[146:149], v[204:207], v[6:9]
	v_mfma_f32_16x16x32_bf16 v[2:5], v[154:157], v[204:207], v[2:5]
	v_mfma_f32_16x16x32_bf16 v[54:57], v[150:153], v[184:187], v[54:57]
	v_mfma_f32_16x16x32_bf16 v[46:49], v[168:171], v[184:187], v[46:49]
	v_mfma_f32_16x16x32_bf16 v[38:41], v[150:153], v[192:195], v[38:41]
	v_mfma_f32_16x16x32_bf16 v[30:33], v[168:171], v[192:195], v[30:33]
	v_mfma_f32_16x16x32_bf16 v[22:25], v[150:153], v[200:203], v[22:25]
	v_mfma_f32_16x16x32_bf16 v[14:17], v[168:171], v[200:203], v[14:17]
	v_mfma_f32_16x16x32_bf16 v[6:9], v[150:153], v[216:219], v[6:9]
	v_mfma_f32_16x16x32_bf16 v[2:5], v[168:171], v[216:219], v[2:5]
	s_barrier
	s_add_i32 s41, s41, 2
	s_add_u32 s33, s33, 0x100
	s_addc_u32 s40, s40, 0
	s_add_u32 s6, s6, 0x100
	s_addc_u32 s7, s7, 0
	s_cmp_gt_u32 s41, 13
	s_cbranch_scc0 .LBB0_1783
	s_and_b64 vcc, exec, s[18:19]
	s_cbranch_vccz .LBB0_1786
	s_barrier

.LBB0_1799:
	s_add_u32 s26, s24, 0xfffc0080
	s_addc_u32 s27, s25, -1
	s_add_i32 s48, 0, 0x10000
	s_cmp_eq_u32 s47, 12
	s_cselect_b32 s29, s8, s27
	s_cselect_b32 s28, s9, s26
	v_add_u32_e32 v142, s48, v144
	s_cselect_b32 s27, s15, s46
	s_cselect_b32 s26, s17, s45
	s_add_i32 s52, 0, 0x14000
	ds_read_b128 v[148:151], v142
	ds_read_b128 v[152:155], v142 offset:1024
	ds_read_b128 v[156:159], v142 offset:2048
	ds_read_b128 v[160:163], v142 offset:3072
	v_add_u32_e32 v142, s52, v144
	ds_read_b128 v[164:167], v142
	ds_read_b128 v[168:171], v142 offset:1024
	ds_read_b128 v[172:175], v142 offset:2048
	ds_read_b128 v[180:183], v142 offset:3072
	v_lshl_add_u64 v[142:143], s[24:25], 0, v[140:141]
	s_add_i32 m0, s36, 0xc000
	ds_read_b128 v[184:187], v146
	ds_read_b128 v[188:191], v146 offset:1024
	ds_read_b128 v[192:195], v146 offset:2048
	ds_read_b128 v[196:199], v146 offset:3072
	ds_read_b128 v[200:203], v146 offset:4096
	ds_read_b128 v[204:207], v146 offset:5120
	ds_read_b128 v[216:219], v146 offset:6144
	ds_read_b128 v[220:223], v146 offset:7168
	global_load_lds_dwordx4 v[142:143], off
	s_add_i32 m0, s36, 0xe000
	v_lshl_add_u64 v[142:143], s[24:25], 0, v[138:139]
	global_load_lds_dwordx4 v[142:143], off
	s_waitcnt vmcnt(8)
	s_waitcnt lgkmcnt(0)
	s_barrier
	s_waitcnt lgkmcnt(0)
	v_mfma_f32_16x16x32_bf16 v[126:129], v[148:151], v[184:187], v[126:129]
	v_mfma_f32_16x16x32_bf16 v[122:125], v[156:159], v[184:187], v[122:125]
	v_mfma_f32_16x16x32_bf16 v[118:121], v[148:151], v[192:195], v[118:121]
	v_mfma_f32_16x16x32_bf16 v[110:113], v[156:159], v[192:195], v[110:113]
	v_mfma_f32_16x16x32_bf16 v[102:105], v[148:151], v[200:203], v[102:105]
	v_mfma_f32_16x16x32_bf16 v[94:97], v[156:159], v[200:203], v[94:97]
	v_mfma_f32_16x16x32_bf16 v[86:89], v[148:151], v[216:219], v[86:89]
	v_mfma_f32_16x16x32_bf16 v[78:81], v[156:159], v[216:219], v[78:81]
	v_mfma_f32_16x16x32_bf16 v[126:129], v[152:155], v[188:191], v[126:129]
	v_mfma_f32_16x16x32_bf16 v[122:125], v[160:163], v[188:191], v[122:125]
	v_mfma_f32_16x16x32_bf16 v[118:121], v[152:155], v[196:199], v[118:121]
	v_mfma_f32_16x16x32_bf16 v[110:113], v[160:163], v[196:199], v[110:113]
	v_mfma_f32_16x16x32_bf16 v[102:105], v[152:155], v[204:207], v[102:105]
	v_mfma_f32_16x16x32_bf16 v[94:97], v[160:163], v[204:207], v[94:97]
	v_mfma_f32_16x16x32_bf16 v[86:89], v[152:155], v[220:223], v[86:89]
	v_mfma_f32_16x16x32_bf16 v[78:81], v[160:163], v[220:223], v[78:81]
	v_mfma_f32_16x16x32_bf16 v[114:117], v[164:167], v[184:187], v[114:117]
	v_mfma_f32_16x16x32_bf16 v[106:109], v[172:175], v[184:187], v[106:109]
	v_mfma_f32_16x16x32_bf16 v[98:101], v[164:167], v[192:195], v[98:101]
	v_mfma_f32_16x16x32_bf16 v[90:93], v[172:175], v[192:195], v[90:93]
	v_mfma_f32_16x16x32_bf16 v[82:85], v[164:167], v[200:203], v[82:85]
	v_mfma_f32_16x16x32_bf16 v[74:77], v[172:175], v[200:203], v[74:77]
	v_mfma_f32_16x16x32_bf16 v[70:73], v[164:167], v[216:219], v[70:73]
	v_mfma_f32_16x16x32_bf16 v[66:69], v[172:175], v[216:219], v[66:69]
	v_mfma_f32_16x16x32_bf16 v[114:117], v[168:171], v[188:191], v[114:117]
	v_mfma_f32_16x16x32_bf16 v[106:109], v[180:183], v[188:191], v[106:109]
	v_mfma_f32_16x16x32_bf16 v[98:101], v[168:171], v[196:199], v[98:101]
	v_mfma_f32_16x16x32_bf16 v[90:93], v[180:183], v[196:199], v[90:93]
	v_mfma_f32_16x16x32_bf16 v[82:85], v[168:171], v[204:207], v[82:85]
	v_mfma_f32_16x16x32_bf16 v[74:77], v[180:183], v[204:207], v[74:77]
	v_mfma_f32_16x16x32_bf16 v[70:73], v[168:171], v[220:223], v[70:73]
	v_mfma_f32_16x16x32_bf16 v[66:69], v[180:183], v[220:223], v[66:69]
	s_barrier
	s_add_i32 s48, s48, s35
	v_lshl_add_u64 v[142:143], s[26:27], 0, v[134:135]
	s_mov_b32 m0, s48
	ds_read_b128 v[184:187], v146 offset:16384
	ds_read_b128 v[188:191], v146 offset:17408
	ds_read_b128 v[192:195], v146 offset:18432
	ds_read_b128 v[196:199], v146 offset:19456
	ds_read_b128 v[200:203], v146 offset:20480
	ds_read_b128 v[204:207], v146 offset:21504
	ds_read_b128 v[216:219], v146 offset:22528
	ds_read_b128 v[220:223], v146 offset:23552
	global_load_lds_dwordx4 v[142:143], off
	s_add_i32 m0, s48, 0x2000
	s_add_u32 s48, s26, 0x40000
	v_lshl_add_u64 v[176:177], s[26:27], 0, v[130:131]
	s_addc_u32 s49, s27, 0
	s_add_i32 s52, s52, s35
	global_load_lds_dwordx4 v[176:177], off
	v_lshl_add_u64 v[208:209], s[48:49], 0, v[134:135]
	s_mov_b32 m0, s52
	v_lshl_add_u64 v[224:225], s[28:29], 0, v[132:133]
	global_load_lds_dwordx4 v[208:209], off
	s_add_i32 m0, s52, 0x2000
	v_lshl_add_u64 v[208:209], s[48:49], 0, v[130:131]
	global_load_lds_dwordx4 v[208:209], off
	s_mov_b32 m0, s36
	v_lshl_add_u64 v[208:209], s[28:29], 0, v[136:137]
	global_load_lds_dwordx4 v[208:209], off
	s_mov_b32 m0, s37
	s_nop 0
	global_load_lds_dwordx4 v[224:225], off
	s_waitcnt vmcnt(8)
	s_waitcnt lgkmcnt(0)
	s_barrier
	s_waitcnt lgkmcnt(0)
	v_mfma_f32_16x16x32_bf16 v[62:65], v[148:151], v[184:187], v[62:65]
	v_mfma_f32_16x16x32_bf16 v[58:61], v[156:159], v[184:187], v[58:61]
	v_mfma_f32_16x16x32_bf16 v[54:57], v[148:151], v[192:195], v[54:57]
	v_mfma_f32_16x16x32_bf16 v[46:49], v[156:159], v[192:195], v[46:49]
	v_mfma_f32_16x16x32_bf16 v[38:41], v[148:151], v[200:203], v[38:41]
	v_mfma_f32_16x16x32_bf16 v[30:33], v[156:159], v[200:203], v[30:33]
	v_mfma_f32_16x16x32_bf16 v[22:25], v[148:151], v[216:219], v[22:25]
	v_mfma_f32_16x16x32_bf16 v[14:17], v[156:159], v[216:219], v[14:17]
	v_mfma_f32_16x16x32_bf16 v[62:65], v[152:155], v[188:191], v[62:65]
	v_mfma_f32_16x16x32_bf16 v[58:61], v[160:163], v[188:191], v[58:61]
	v_mfma_f32_16x16x32_bf16 v[54:57], v[152:155], v[196:199], v[54:57]
	v_mfma_f32_16x16x32_bf16 v[46:49], v[160:163], v[196:199], v[46:49]
	v_mfma_f32_16x16x32_bf16 v[38:41], v[152:155], v[204:207], v[38:41]
	v_mfma_f32_16x16x32_bf16 v[30:33], v[160:163], v[204:207], v[30:33]
	v_mfma_f32_16x16x32_bf16 v[22:25], v[152:155], v[220:223], v[22:25]
	v_mfma_f32_16x16x32_bf16 v[14:17], v[160:163], v[220:223], v[14:17]
	v_mfma_f32_16x16x32_bf16 v[50:53], v[164:167], v[184:187], v[50:53]
	v_mfma_f32_16x16x32_bf16 v[42:45], v[172:175], v[184:187], v[42:45]
	v_mfma_f32_16x16x32_bf16 v[34:37], v[164:167], v[192:195], v[34:37]
	v_mfma_f32_16x16x32_bf16 v[26:29], v[172:175], v[192:195], v[26:29]
	v_mfma_f32_16x16x32_bf16 v[18:21], v[164:167], v[200:203], v[18:21]
	v_mfma_f32_16x16x32_bf16 v[10:13], v[172:175], v[200:203], v[10:13]
	v_mfma_f32_16x16x32_bf16 v[6:9], v[164:167], v[216:219], v[6:9]
	v_mfma_f32_16x16x32_bf16 v[2:5], v[172:175], v[216:219], v[2:5]
	v_mfma_f32_16x16x32_bf16 v[50:53], v[168:171], v[188:191], v[50:53]
	v_mfma_f32_16x16x32_bf16 v[42:45], v[180:183], v[188:191], v[42:45]
	v_mfma_f32_16x16x32_bf16 v[34:37], v[168:171], v[196:199], v[34:37]
	v_mfma_f32_16x16x32_bf16 v[26:29], v[180:183], v[196:199], v[26:29]
	v_mfma_f32_16x16x32_bf16 v[18:21], v[168:171], v[204:207], v[18:21]
	v_mfma_f32_16x16x32_bf16 v[10:13], v[180:183], v[204:207], v[10:13]
	v_mfma_f32_16x16x32_bf16 v[6:9], v[168:171], v[220:223], v[6:9]
	v_mfma_f32_16x16x32_bf16 v[2:5], v[180:183], v[220:223], v[2:5]
	s_barrier
	s_add_i32 s48, 0, 0x18000
	v_add_u32_e32 v147, s48, v144
	s_add_i32 s49, 0, 0x1c000
	ds_read_b128 v[148:151], v147
	ds_read_b128 v[152:155], v147 offset:1024
	ds_read_b128 v[156:159], v147 offset:2048
	ds_read_b128 v[160:163], v147 offset:3072
	v_add_u32_e32 v147, s49, v144
	ds_read_b128 v[164:167], v147
	ds_read_b128 v[168:171], v147 offset:1024
	ds_read_b128 v[172:175], v147 offset:2048
	ds_read_b128 v[180:183], v147 offset:3072
	s_add_u32 s28, s28, 0x40000
	s_addc_u32 s29, s29, 0
	s_mov_b32 m0, s4
	v_lshl_add_u64 v[240:241], s[28:29], 0, v[136:137]
	ds_read_b128 v[184:187], v146 offset:32768
	ds_read_b128 v[188:191], v146 offset:33792
	ds_read_b128 v[192:195], v146 offset:34816
	ds_read_b128 v[196:199], v146 offset:35840
	ds_read_b128 v[200:203], v146 offset:36864
	ds_read_b128 v[204:207], v146 offset:37888
	ds_read_b128 v[216:219], v146 offset:38912
	ds_read_b128 v[220:223], v146 offset:39936
	global_load_lds_dwordx4 v[240:241], off
	s_mov_b32 m0, s33
	v_lshl_add_u64 v[240:241], s[28:29], 0, v[132:133]
	global_load_lds_dwordx4 v[240:241], off
	s_waitcnt vmcnt(8)
	s_waitcnt lgkmcnt(0)
	s_barrier
	s_waitcnt lgkmcnt(0)
	v_mfma_f32_16x16x32_bf16 v[126:129], v[148:151], v[184:187], v[126:129]
	v_mfma_f32_16x16x32_bf16 v[122:125], v[156:159], v[184:187], v[122:125]
	v_mfma_f32_16x16x32_bf16 v[118:121], v[148:151], v[192:195], v[118:121]
	v_mfma_f32_16x16x32_bf16 v[110:113], v[156:159], v[192:195], v[110:113]
	v_mfma_f32_16x16x32_bf16 v[102:105], v[148:151], v[200:203], v[102:105]
	v_mfma_f32_16x16x32_bf16 v[94:97], v[156:159], v[200:203], v[94:97]
	v_mfma_f32_16x16x32_bf16 v[86:89], v[148:151], v[216:219], v[86:89]
	v_mfma_f32_16x16x32_bf16 v[78:81], v[156:159], v[216:219], v[78:81]
	v_mfma_f32_16x16x32_bf16 v[126:129], v[152:155], v[188:191], v[126:129]
	v_mfma_f32_16x16x32_bf16 v[122:125], v[160:163], v[188:191], v[122:125]
	v_mfma_f32_16x16x32_bf16 v[118:121], v[152:155], v[196:199], v[118:121]
	v_mfma_f32_16x16x32_bf16 v[110:113], v[160:163], v[196:199], v[110:113]
	v_mfma_f32_16x16x32_bf16 v[102:105], v[152:155], v[204:207], v[102:105]
	v_mfma_f32_16x16x32_bf16 v[94:97], v[160:163], v[204:207], v[94:97]
	v_mfma_f32_16x16x32_bf16 v[86:89], v[152:155], v[220:223], v[86:89]
	v_mfma_f32_16x16x32_bf16 v[78:81], v[160:163], v[220:223], v[78:81]
	v_mfma_f32_16x16x32_bf16 v[114:117], v[164:167], v[184:187], v[114:117]
	v_mfma_f32_16x16x32_bf16 v[106:109], v[172:175], v[184:187], v[106:109]
	v_mfma_f32_16x16x32_bf16 v[98:101], v[164:167], v[192:195], v[98:101]
	v_mfma_f32_16x16x32_bf16 v[90:93], v[172:175], v[192:195], v[90:93]
	v_mfma_f32_16x16x32_bf16 v[82:85], v[164:167], v[200:203], v[82:85]
	v_mfma_f32_16x16x32_bf16 v[74:77], v[172:175], v[200:203], v[74:77]
	v_mfma_f32_16x16x32_bf16 v[70:73], v[164:167], v[216:219], v[70:73]
	v_mfma_f32_16x16x32_bf16 v[66:69], v[172:175], v[216:219], v[66:69]
	v_mfma_f32_16x16x32_bf16 v[114:117], v[168:171], v[188:191], v[114:117]
	v_mfma_f32_16x16x32_bf16 v[106:109], v[180:183], v[188:191], v[106:109]
	v_mfma_f32_16x16x32_bf16 v[98:101], v[168:171], v[196:199], v[98:101]
	v_mfma_f32_16x16x32_bf16 v[90:93], v[180:183], v[196:199], v[90:93]
	v_mfma_f32_16x16x32_bf16 v[82:85], v[168:171], v[204:207], v[82:85]
	v_mfma_f32_16x16x32_bf16 v[74:77], v[180:183], v[204:207], v[74:77]
	v_mfma_f32_16x16x32_bf16 v[70:73], v[168:171], v[220:223], v[70:73]
	v_mfma_f32_16x16x32_bf16 v[66:69], v[180:183], v[220:223], v[66:69]
	s_barrier
	s_add_i32 s28, s48, s35
	v_lshl_add_u64 v[142:143], v[142:143], 0, s[56:57]
	s_mov_b32 m0, s28
	ds_read_b128 v[184:187], v146 offset:49152
	ds_read_b128 v[188:191], v146 offset:50176
	ds_read_b128 v[192:195], v146 offset:51200
	ds_read_b128 v[196:199], v146 offset:52224
	ds_read_b128 v[200:203], v146 offset:53248
	ds_read_b128 v[204:207], v146 offset:54272
	ds_read_b128 v[216:219], v146 offset:55296
	ds_read_b128 v[220:223], v146 offset:56320
	global_load_lds_dwordx4 v[142:143], off
	s_add_i32 m0, s28, 0x2000
	s_add_u32 s26, s26, 0x40080
	v_lshl_add_u64 v[142:143], v[176:177], 0, s[56:57]
	s_addc_u32 s27, s27, 0
	s_add_i32 s28, s49, s35
	global_load_lds_dwordx4 v[142:143], off
	s_mov_b32 m0, s28
	v_lshl_add_u64 v[142:143], s[26:27], 0, v[134:135]
	global_load_lds_dwordx4 v[142:143], off
	s_add_i32 m0, s28, 0x2000
	v_lshl_add_u64 v[142:143], s[26:27], 0, v[130:131]
	global_load_lds_dwordx4 v[142:143], off
	s_mov_b32 m0, s38
	v_lshl_add_u64 v[142:143], v[208:209], 0, s[56:57]
	global_load_lds_dwordx4 v[142:143], off
	s_mov_b32 m0, s39
	v_lshl_add_u64 v[142:143], v[224:225], 0, s[56:57]
	global_load_lds_dwordx4 v[142:143], off
	s_waitcnt vmcnt(8)
	s_waitcnt lgkmcnt(0)
	s_barrier
	s_waitcnt lgkmcnt(0)
	v_mfma_f32_16x16x32_bf16 v[62:65], v[148:151], v[184:187], v[62:65]
	v_mfma_f32_16x16x32_bf16 v[58:61], v[156:159], v[184:187], v[58:61]
	v_mfma_f32_16x16x32_bf16 v[54:57], v[148:151], v[192:195], v[54:57]
	v_mfma_f32_16x16x32_bf16 v[46:49], v[156:159], v[192:195], v[46:49]
	v_mfma_f32_16x16x32_bf16 v[38:41], v[148:151], v[200:203], v[38:41]
	v_mfma_f32_16x16x32_bf16 v[30:33], v[156:159], v[200:203], v[30:33]
	v_mfma_f32_16x16x32_bf16 v[22:25], v[148:151], v[216:219], v[22:25]
	v_mfma_f32_16x16x32_bf16 v[14:17], v[156:159], v[216:219], v[14:17]
	v_mfma_f32_16x16x32_bf16 v[62:65], v[152:155], v[188:191], v[62:65]
	v_mfma_f32_16x16x32_bf16 v[58:61], v[160:163], v[188:191], v[58:61]
	v_mfma_f32_16x16x32_bf16 v[54:57], v[152:155], v[196:199], v[54:57]
	v_mfma_f32_16x16x32_bf16 v[46:49], v[160:163], v[196:199], v[46:49]
	v_mfma_f32_16x16x32_bf16 v[38:41], v[152:155], v[204:207], v[38:41]
	v_mfma_f32_16x16x32_bf16 v[30:33], v[160:163], v[204:207], v[30:33]
	v_mfma_f32_16x16x32_bf16 v[22:25], v[152:155], v[220:223], v[22:25]
	v_mfma_f32_16x16x32_bf16 v[14:17], v[160:163], v[220:223], v[14:17]
	v_mfma_f32_16x16x32_bf16 v[50:53], v[164:167], v[184:187], v[50:53]
	v_mfma_f32_16x16x32_bf16 v[42:45], v[172:175], v[184:187], v[42:45]
	v_mfma_f32_16x16x32_bf16 v[34:37], v[164:167], v[192:195], v[34:37]
	v_mfma_f32_16x16x32_bf16 v[26:29], v[172:175], v[192:195], v[26:29]
	v_mfma_f32_16x16x32_bf16 v[18:21], v[164:167], v[200:203], v[18:21]
	v_mfma_f32_16x16x32_bf16 v[10:13], v[172:175], v[200:203], v[10:13]
	v_mfma_f32_16x16x32_bf16 v[6:9], v[164:167], v[216:219], v[6:9]
	v_mfma_f32_16x16x32_bf16 v[2:5], v[172:175], v[216:219], v[2:5]
	v_mfma_f32_16x16x32_bf16 v[50:53], v[168:171], v[188:191], v[50:53]
	v_mfma_f32_16x16x32_bf16 v[42:45], v[180:183], v[188:191], v[42:45]
	v_mfma_f32_16x16x32_bf16 v[34:37], v[168:171], v[196:199], v[34:37]
	v_mfma_f32_16x16x32_bf16 v[26:29], v[180:183], v[196:199], v[26:29]
	v_mfma_f32_16x16x32_bf16 v[18:21], v[168:171], v[204:207], v[18:21]
	v_mfma_f32_16x16x32_bf16 v[10:13], v[180:183], v[204:207], v[10:13]
	v_mfma_f32_16x16x32_bf16 v[6:9], v[168:171], v[220:223], v[6:9]
	v_mfma_f32_16x16x32_bf16 v[2:5], v[180:183], v[220:223], v[2:5]
	s_barrier
	s_add_i32 s47, s47, 2
	s_add_u32 s45, s45, 0x100
	s_addc_u32 s46, s46, 0
	s_add_u32 s24, s24, 0x100
	s_addc_u32 s25, s25, 0
	s_cmp_gt_u32 s47, 13
	s_cbranch_scc0 .LBB0_1799
	s_and_b64 vcc, exec, s[12:13]
	s_cbranch_vccz .LBB0_1802
	s_barrier

.LBB0_2367:
	s_add_u32 s10, s34, s38
	s_addc_u32 s11, s35, 0
	s_add_u32 s39, s10, 0x100
	s_addc_u32 s76, s11, 0
	s_and_b64 s[70:71], s[62:63], exec
	s_cselect_b32 s77, s45, s76
	s_cselect_b32 s76, s59, s39
	s_add_u32 s38, s30, s38
	s_addc_u32 s39, s31, 0
	s_add_u32 s70, s38, 0x100
	s_addc_u32 s71, s39, 0
	s_add_i32 s91, 0, 0x10000
	s_and_b64 s[38:39], s[62:63], exec
	s_cselect_b32 s79, s37, s71
	s_cselect_b32 s78, s82, s70
	s_add_i32 s38, 0, 0x14000
	s_add_u32 s10, s10, 0x10080
	s_addc_u32 s11, s11, 0
	s_add_i32 s8, s91, s95
	s_add_i32 m0, s65, 0xc000
	s_add_i32 s14, s65, 0xe000
	s_add_i32 s9, s8, 0x2000
	s_add_u32 s80, s78, 0x10000
	s_addc_u32 s81, s79, 0
	s_add_i32 s50, s38, s95
	v_add_u32_e32 v152, s91, v138
	v_add_u32_e32 v164, s38, v138
	s_add_i32 s74, s50, 0x2000
	s_add_i32 vcc_hi, 0, 0x18000
	s_add_i32 s39, 0, 0x1c000
	ds_read_b128 v[140:143], v152
	ds_read_b128 v[144:147], v152 offset:1024
	ds_read_b128 v[148:151], v152 offset:2048
	ds_read_b128 v[152:155], v152 offset:3072
	ds_read_b128 v[156:159], v164
	ds_read_b128 v[160:163], v164 offset:1024
	ds_read_b128 v[168:171], v164 offset:2048
	ds_read_b128 v[172:175], v164 offset:3072
	s_add_u32 s70, s76, 0x10000
	s_addc_u32 s71, s77, 0
	s_add_i32 vcc_lo, vcc_hi, s95
	s_add_i32 s64, vcc_lo, 0x2000
	s_add_u32 s62, s78, 0x10080
	s_addc_u32 s63, s79, 0
	s_add_i32 s91, s39, s95
	s_add_i32 s38, s91, 0x2000
	v_lshl_add_u64 v[164:165], s[10:11], 0, v[128:129]
	ds_read_b128 v[176:179], v139
	ds_read_b128 v[180:183], v139 offset:1024
	ds_read_b128 v[184:187], v139 offset:2048
	ds_read_b128 v[188:191], v139 offset:3072
	ds_read_b128 v[192:195], v139 offset:4096
	ds_read_b128 v[196:199], v139 offset:5120
	ds_read_b128 v[200:203], v139 offset:6144
	ds_read_b128 v[204:207], v139 offset:7168
	global_load_lds_dwordx4 v[164:165], off
	s_mov_b32 m0, s14
	v_lshl_add_u64 v[164:165], s[10:11], 0, v[124:125]
	global_load_lds_dwordx4 v[164:165], off
	s_waitcnt vmcnt(8)
	s_waitcnt lgkmcnt(0)
	s_barrier
	s_waitcnt lgkmcnt(0)
	v_mfma_f32_16x16x32_bf16 v[134:137], v[140:143], v[176:179], v[134:137]
	v_mfma_f32_16x16x32_bf16 v[130:133], v[148:151], v[176:179], v[130:133]
	v_mfma_f32_16x16x32_bf16 v[110:113], v[140:143], v[184:187], v[110:113]
	v_mfma_f32_16x16x32_bf16 v[106:109], v[148:151], v[184:187], v[106:109]
	v_mfma_f32_16x16x32_bf16 v[94:97], v[140:143], v[192:195], v[94:97]
	v_mfma_f32_16x16x32_bf16 v[90:93], v[148:151], v[192:195], v[90:93]
	v_mfma_f32_16x16x32_bf16 v[78:81], v[140:143], v[200:203], v[78:81]
	v_mfma_f32_16x16x32_bf16 v[74:77], v[148:151], v[200:203], v[74:77]
	v_mfma_f32_16x16x32_bf16 v[134:137], v[144:147], v[180:183], v[134:137]
	v_mfma_f32_16x16x32_bf16 v[130:133], v[152:155], v[180:183], v[130:133]
	v_mfma_f32_16x16x32_bf16 v[110:113], v[144:147], v[188:191], v[110:113]
	v_mfma_f32_16x16x32_bf16 v[106:109], v[152:155], v[188:191], v[106:109]
	v_mfma_f32_16x16x32_bf16 v[94:97], v[144:147], v[196:199], v[94:97]
	v_mfma_f32_16x16x32_bf16 v[90:93], v[152:155], v[196:199], v[90:93]
	v_mfma_f32_16x16x32_bf16 v[78:81], v[144:147], v[204:207], v[78:81]
	v_mfma_f32_16x16x32_bf16 v[74:77], v[152:155], v[204:207], v[74:77]
	v_mfma_f32_16x16x32_bf16 v[118:121], v[156:159], v[176:179], v[118:121]
	v_mfma_f32_16x16x32_bf16 v[114:117], v[168:171], v[176:179], v[114:117]
	v_mfma_f32_16x16x32_bf16 v[102:105], v[156:159], v[184:187], v[102:105]
	v_mfma_f32_16x16x32_bf16 v[98:101], v[168:171], v[184:187], v[98:101]
	v_mfma_f32_16x16x32_bf16 v[86:89], v[156:159], v[192:195], v[86:89]
	v_mfma_f32_16x16x32_bf16 v[82:85], v[168:171], v[192:195], v[82:85]
	v_mfma_f32_16x16x32_bf16 v[70:73], v[156:159], v[200:203], v[70:73]
	v_mfma_f32_16x16x32_bf16 v[66:69], v[168:171], v[200:203], v[66:69]
	v_mfma_f32_16x16x32_bf16 v[118:121], v[160:163], v[180:183], v[118:121]
	v_mfma_f32_16x16x32_bf16 v[114:117], v[172:175], v[180:183], v[114:117]
	v_mfma_f32_16x16x32_bf16 v[102:105], v[160:163], v[188:191], v[102:105]
	v_mfma_f32_16x16x32_bf16 v[98:101], v[172:175], v[188:191], v[98:101]
	v_mfma_f32_16x16x32_bf16 v[86:89], v[160:163], v[196:199], v[86:89]
	v_mfma_f32_16x16x32_bf16 v[82:85], v[172:175], v[196:199], v[82:85]
	v_mfma_f32_16x16x32_bf16 v[70:73], v[160:163], v[204:207], v[70:73]
	v_mfma_f32_16x16x32_bf16 v[66:69], v[172:175], v[204:207], v[66:69]
	s_barrier
	s_mov_b32 m0, s8
	v_lshl_add_u64 v[164:165], s[78:79], 0, v[126:127]
	ds_read_b128 v[176:179], v139 offset:16384
	ds_read_b128 v[180:183], v139 offset:17408
	ds_read_b128 v[184:187], v139 offset:18432
	ds_read_b128 v[188:191], v139 offset:19456
	ds_read_b128 v[192:195], v139 offset:20480
	ds_read_b128 v[196:199], v139 offset:21504
	ds_read_b128 v[200:203], v139 offset:22528
	ds_read_b128 v[204:207], v139 offset:23552
	global_load_lds_dwordx4 v[164:165], off
	v_lshl_add_u64 v[208:209], s[78:79], 0, v[122:123]
	s_mov_b32 m0, s9
	v_lshl_add_u64 v[216:217], s[80:81], 0, v[126:127]
	global_load_lds_dwordx4 v[208:209], off
	s_mov_b32 m0, s50
	v_lshl_add_u64 v[218:219], s[76:77], 0, v[124:125]
	global_load_lds_dwordx4 v[216:217], off
	s_mov_b32 m0, s74
	v_lshl_add_u64 v[216:217], s[80:81], 0, v[122:123]
	global_load_lds_dwordx4 v[216:217], off
	s_mov_b32 m0, s65
	v_lshl_add_u64 v[216:217], s[76:77], 0, v[128:129]
	global_load_lds_dwordx4 v[216:217], off
	s_mov_b32 m0, s15
	s_nop 0
	global_load_lds_dwordx4 v[218:219], off
	s_waitcnt vmcnt(8)
	s_waitcnt lgkmcnt(0)
	s_barrier
	s_waitcnt lgkmcnt(0)
	v_mfma_f32_16x16x32_bf16 v[62:65], v[140:143], v[176:179], v[62:65]
	v_mfma_f32_16x16x32_bf16 v[58:61], v[148:151], v[176:179], v[58:61]
	v_mfma_f32_16x16x32_bf16 v[46:49], v[140:143], v[184:187], v[46:49]
	v_mfma_f32_16x16x32_bf16 v[42:45], v[148:151], v[184:187], v[42:45]
	v_mfma_f32_16x16x32_bf16 v[30:33], v[140:143], v[192:195], v[30:33]
	v_mfma_f32_16x16x32_bf16 v[26:29], v[148:151], v[192:195], v[26:29]
	v_mfma_f32_16x16x32_bf16 v[14:17], v[140:143], v[200:203], v[14:17]
	v_mfma_f32_16x16x32_bf16 v[10:13], v[148:151], v[200:203], v[10:13]
	v_mfma_f32_16x16x32_bf16 v[62:65], v[144:147], v[180:183], v[62:65]
	v_mfma_f32_16x16x32_bf16 v[58:61], v[152:155], v[180:183], v[58:61]
	v_mfma_f32_16x16x32_bf16 v[46:49], v[144:147], v[188:191], v[46:49]
	v_mfma_f32_16x16x32_bf16 v[42:45], v[152:155], v[188:191], v[42:45]
	v_mfma_f32_16x16x32_bf16 v[30:33], v[144:147], v[196:199], v[30:33]
	v_mfma_f32_16x16x32_bf16 v[26:29], v[152:155], v[196:199], v[26:29]
	v_mfma_f32_16x16x32_bf16 v[14:17], v[144:147], v[204:207], v[14:17]
	v_mfma_f32_16x16x32_bf16 v[10:13], v[152:155], v[204:207], v[10:13]
	v_mfma_f32_16x16x32_bf16 v[54:57], v[156:159], v[176:179], v[54:57]
	v_mfma_f32_16x16x32_bf16 v[50:53], v[168:171], v[176:179], v[50:53]
	v_mfma_f32_16x16x32_bf16 v[38:41], v[156:159], v[184:187], v[38:41]
	v_mfma_f32_16x16x32_bf16 v[34:37], v[168:171], v[184:187], v[34:37]
	v_mfma_f32_16x16x32_bf16 v[22:25], v[156:159], v[192:195], v[22:25]
	v_mfma_f32_16x16x32_bf16 v[18:21], v[168:171], v[192:195], v[18:21]
	v_mfma_f32_16x16x32_bf16 v[6:9], v[156:159], v[200:203], v[6:9]
	v_mfma_f32_16x16x32_bf16 v[2:5], v[168:171], v[200:203], v[2:5]
	v_mfma_f32_16x16x32_bf16 v[54:57], v[160:163], v[180:183], v[54:57]
	v_mfma_f32_16x16x32_bf16 v[50:53], v[172:175], v[180:183], v[50:53]
	v_mfma_f32_16x16x32_bf16 v[38:41], v[160:163], v[188:191], v[38:41]
	v_mfma_f32_16x16x32_bf16 v[34:37], v[172:175], v[188:191], v[34:37]
	v_mfma_f32_16x16x32_bf16 v[22:25], v[160:163], v[196:199], v[22:25]
	v_mfma_f32_16x16x32_bf16 v[18:21], v[172:175], v[196:199], v[18:21]
	v_mfma_f32_16x16x32_bf16 v[6:9], v[160:163], v[204:207], v[6:9]
	v_mfma_f32_16x16x32_bf16 v[2:5], v[172:175], v[204:207], v[2:5]
	s_barrier
	v_add_u32_e32 v152, vcc_hi, v138
	v_add_u32_e32 v167, s39, v138
	ds_read_b128 v[140:143], v152
	ds_read_b128 v[144:147], v152 offset:1024
	ds_read_b128 v[148:151], v152 offset:2048
	ds_read_b128 v[152:155], v152 offset:3072
	ds_read_b128 v[156:159], v167
	ds_read_b128 v[160:163], v167 offset:1024
	ds_read_b128 v[168:171], v167 offset:2048
	ds_read_b128 v[172:175], v167 offset:3072
	s_mov_b32 m0, s84
	v_lshl_add_u64 v[220:221], s[70:71], 0, v[128:129]
	ds_read_b128 v[176:179], v139 offset:32768
	ds_read_b128 v[180:183], v139 offset:33792
	ds_read_b128 v[184:187], v139 offset:34816
	ds_read_b128 v[188:191], v139 offset:35840
	ds_read_b128 v[192:195], v139 offset:36864
	ds_read_b128 v[196:199], v139 offset:37888
	ds_read_b128 v[200:203], v139 offset:38912
	ds_read_b128 v[204:207], v139 offset:39936
	global_load_lds_dwordx4 v[220:221], off
	s_mov_b32 m0, s90
	v_lshl_add_u64 v[220:221], s[70:71], 0, v[124:125]
	global_load_lds_dwordx4 v[220:221], off
	s_waitcnt vmcnt(8)
	s_waitcnt lgkmcnt(0)
	s_barrier
	s_waitcnt lgkmcnt(0)
	v_mfma_f32_16x16x32_bf16 v[134:137], v[140:143], v[176:179], v[134:137]
	v_mfma_f32_16x16x32_bf16 v[130:133], v[148:151], v[176:179], v[130:133]
	v_mfma_f32_16x16x32_bf16 v[110:113], v[140:143], v[184:187], v[110:113]
	v_mfma_f32_16x16x32_bf16 v[106:109], v[148:151], v[184:187], v[106:109]
	v_mfma_f32_16x16x32_bf16 v[94:97], v[140:143], v[192:195], v[94:97]
	v_mfma_f32_16x16x32_bf16 v[90:93], v[148:151], v[192:195], v[90:93]
	v_mfma_f32_16x16x32_bf16 v[78:81], v[140:143], v[200:203], v[78:81]
	v_mfma_f32_16x16x32_bf16 v[74:77], v[148:151], v[200:203], v[74:77]
	v_mfma_f32_16x16x32_bf16 v[134:137], v[144:147], v[180:183], v[134:137]
	v_mfma_f32_16x16x32_bf16 v[130:133], v[152:155], v[180:183], v[130:133]
	v_mfma_f32_16x16x32_bf16 v[110:113], v[144:147], v[188:191], v[110:113]
	v_mfma_f32_16x16x32_bf16 v[106:109], v[152:155], v[188:191], v[106:109]
	v_mfma_f32_16x16x32_bf16 v[94:97], v[144:147], v[196:199], v[94:97]
	v_mfma_f32_16x16x32_bf16 v[90:93], v[152:155], v[196:199], v[90:93]
	v_mfma_f32_16x16x32_bf16 v[78:81], v[144:147], v[204:207], v[78:81]
	v_mfma_f32_16x16x32_bf16 v[74:77], v[152:155], v[204:207], v[74:77]
	v_mfma_f32_16x16x32_bf16 v[118:121], v[156:159], v[176:179], v[118:121]
	v_mfma_f32_16x16x32_bf16 v[114:117], v[168:171], v[176:179], v[114:117]
	v_mfma_f32_16x16x32_bf16 v[102:105], v[156:159], v[184:187], v[102:105]
	v_mfma_f32_16x16x32_bf16 v[98:101], v[168:171], v[184:187], v[98:101]
	v_mfma_f32_16x16x32_bf16 v[86:89], v[156:159], v[192:195], v[86:89]
	v_mfma_f32_16x16x32_bf16 v[82:85], v[168:171], v[192:195], v[82:85]
	v_mfma_f32_16x16x32_bf16 v[70:73], v[156:159], v[200:203], v[70:73]
	v_mfma_f32_16x16x32_bf16 v[66:69], v[168:171], v[200:203], v[66:69]
	v_mfma_f32_16x16x32_bf16 v[118:121], v[160:163], v[180:183], v[118:121]
	v_mfma_f32_16x16x32_bf16 v[114:117], v[172:175], v[180:183], v[114:117]
	v_mfma_f32_16x16x32_bf16 v[102:105], v[160:163], v[188:191], v[102:105]
	v_mfma_f32_16x16x32_bf16 v[98:101], v[172:175], v[188:191], v[98:101]
	v_mfma_f32_16x16x32_bf16 v[86:89], v[160:163], v[196:199], v[86:89]
	v_mfma_f32_16x16x32_bf16 v[82:85], v[172:175], v[196:199], v[82:85]
	v_mfma_f32_16x16x32_bf16 v[70:73], v[160:163], v[204:207], v[70:73]
	v_mfma_f32_16x16x32_bf16 v[66:69], v[172:175], v[204:207], v[66:69]
	s_barrier
	s_mov_b32 m0, vcc_lo
	v_lshl_add_u64 v[164:165], v[164:165], 0, s[56:57]
	ds_read_b128 v[176:179], v139 offset:49152
	ds_read_b128 v[180:183], v139 offset:50176
	ds_read_b128 v[184:187], v139 offset:51200
	ds_read_b128 v[188:191], v139 offset:52224
	ds_read_b128 v[192:195], v139 offset:53248
	ds_read_b128 v[196:199], v139 offset:54272
	ds_read_b128 v[200:203], v139 offset:55296
	ds_read_b128 v[204:207], v139 offset:56320
	global_load_lds_dwordx4 v[164:165], off
	s_mov_b32 m0, s64
	v_lshl_add_u64 v[164:165], v[208:209], 0, s[56:57]
	global_load_lds_dwordx4 v[164:165], off
	s_mov_b32 m0, s91
	v_lshl_add_u64 v[164:165], s[62:63], 0, v[126:127]
	global_load_lds_dwordx4 v[164:165], off
	s_mov_b32 m0, s38
	v_lshl_add_u64 v[164:165], s[62:63], 0, v[122:123]
	global_load_lds_dwordx4 v[164:165], off
	s_mov_b32 m0, s68
	v_lshl_add_u64 v[164:165], v[216:217], 0, s[56:57]
	global_load_lds_dwordx4 v[164:165], off
	s_mov_b32 m0, s22
	v_lshl_add_u64 v[164:165], v[218:219], 0, s[56:57]
	global_load_lds_dwordx4 v[164:165], off
	s_waitcnt vmcnt(8)
	s_waitcnt lgkmcnt(0)
	s_barrier
	s_waitcnt lgkmcnt(0)
	v_mfma_f32_16x16x32_bf16 v[62:65], v[140:143], v[176:179], v[62:65]
	v_mfma_f32_16x16x32_bf16 v[58:61], v[148:151], v[176:179], v[58:61]
	v_mfma_f32_16x16x32_bf16 v[46:49], v[140:143], v[184:187], v[46:49]
	v_mfma_f32_16x16x32_bf16 v[42:45], v[148:151], v[184:187], v[42:45]
	v_mfma_f32_16x16x32_bf16 v[30:33], v[140:143], v[192:195], v[30:33]
	v_mfma_f32_16x16x32_bf16 v[26:29], v[148:151], v[192:195], v[26:29]
	v_mfma_f32_16x16x32_bf16 v[14:17], v[140:143], v[200:203], v[14:17]
	v_mfma_f32_16x16x32_bf16 v[10:13], v[148:151], v[200:203], v[10:13]
	v_mfma_f32_16x16x32_bf16 v[62:65], v[144:147], v[180:183], v[62:65]
	v_mfma_f32_16x16x32_bf16 v[58:61], v[152:155], v[180:183], v[58:61]
	v_mfma_f32_16x16x32_bf16 v[46:49], v[144:147], v[188:191], v[46:49]
	v_mfma_f32_16x16x32_bf16 v[42:45], v[152:155], v[188:191], v[42:45]
	v_mfma_f32_16x16x32_bf16 v[30:33], v[144:147], v[196:199], v[30:33]
	v_mfma_f32_16x16x32_bf16 v[26:29], v[152:155], v[196:199], v[26:29]
	v_mfma_f32_16x16x32_bf16 v[14:17], v[144:147], v[204:207], v[14:17]
	v_mfma_f32_16x16x32_bf16 v[10:13], v[152:155], v[204:207], v[10:13]
	v_mfma_f32_16x16x32_bf16 v[54:57], v[156:159], v[176:179], v[54:57]
	v_mfma_f32_16x16x32_bf16 v[50:53], v[168:171], v[176:179], v[50:53]
	v_mfma_f32_16x16x32_bf16 v[38:41], v[156:159], v[184:187], v[38:41]
	v_mfma_f32_16x16x32_bf16 v[34:37], v[168:171], v[184:187], v[34:37]
	v_mfma_f32_16x16x32_bf16 v[22:25], v[156:159], v[192:195], v[22:25]
	v_mfma_f32_16x16x32_bf16 v[18:21], v[168:171], v[192:195], v[18:21]
	v_mfma_f32_16x16x32_bf16 v[6:9], v[156:159], v[200:203], v[6:9]
	v_mfma_f32_16x16x32_bf16 v[2:5], v[168:171], v[200:203], v[2:5]
	v_mfma_f32_16x16x32_bf16 v[54:57], v[160:163], v[180:183], v[54:57]
	v_mfma_f32_16x16x32_bf16 v[50:53], v[172:175], v[180:183], v[50:53]
	v_mfma_f32_16x16x32_bf16 v[38:41], v[160:163], v[188:191], v[38:41]
	v_mfma_f32_16x16x32_bf16 v[34:37], v[172:175], v[188:191], v[34:37]
	v_mfma_f32_16x16x32_bf16 v[22:25], v[160:163], v[196:199], v[22:25]
	v_mfma_f32_16x16x32_bf16 v[18:21], v[172:175], v[196:199], v[18:21]
	v_mfma_f32_16x16x32_bf16 v[6:9], v[160:163], v[204:207], v[6:9]
	v_mfma_f32_16x16x32_bf16 v[2:5], v[172:175], v[204:207], v[2:5]
	s_barrier
	s_movk_i32 s38, 0x100
	s_andn2_b64 vcc, exec, s[52:53]
	s_mov_b64 s[62:63], -1
	s_mov_b64 s[52:53], 0
	s_cbranch_vccz .LBB0_2367
	s_andn2_b64 vcc, exec, s[42:43]
	s_cbranch_vccnz .LBB0_2359
	v_mov_b32_e32 v2, 0
	s_mov_b32 s16, s36
	s_mov_b32 s94, s44
	s_mov_b64 s[30:31], s[48:49]
	s_mov_b64 s[34:35], s[46:47]
	s_mov_b32 s58, s23
	v_mov_b32_e32 v3, v2
	v_mov_b32_e32 v4, v2
	v_mov_b32_e32 v5, v2
	v_mov_b32_e32 v6, v2
	v_mov_b32_e32 v7, v2
	v_mov_b32_e32 v8, v2
	v_mov_b32_e32 v9, v2
	v_mov_b32_e32 v18, v2
	v_mov_b32_e32 v19, v2
	v_mov_b32_e32 v20, v2
	v_mov_b32_e32 v21, v2
	v_mov_b32_e32 v22, v2
	v_mov_b32_e32 v23, v2
	v_mov_b32_e32 v24, v2
	v_mov_b32_e32 v25, v2
	v_mov_b32_e32 v34, v2
	v_mov_b32_e32 v35, v2
	v_mov_b32_e32 v36, v2
	v_mov_b32_e32 v37, v2
	v_mov_b32_e32 v38, v2
	v_mov_b32_e32 v39, v2
	v_mov_b32_e32 v40, v2
	v_mov_b32_e32 v41, v2
	v_mov_b32_e32 v50, v2
	v_mov_b32_e32 v51, v2
	v_mov_b32_e32 v52, v2
	v_mov_b32_e32 v53, v2
	v_mov_b32_e32 v54, v2
	v_mov_b32_e32 v55, v2
	v_mov_b32_e32 v56, v2
	v_mov_b32_e32 v57, v2
	v_mov_b32_e32 v10, v2
	v_mov_b32_e32 v11, v2
	v_mov_b32_e32 v12, v2
	v_mov_b32_e32 v13, v2
	v_mov_b32_e32 v14, v2
	v_mov_b32_e32 v15, v2
	v_mov_b32_e32 v16, v2
	v_mov_b32_e32 v17, v2
	v_mov_b32_e32 v26, v2
	v_mov_b32_e32 v27, v2
	v_mov_b32_e32 v28, v2
	v_mov_b32_e32 v29, v2
	v_mov_b32_e32 v30, v2
	v_mov_b32_e32 v31, v2
	v_mov_b32_e32 v32, v2
	v_mov_b32_e32 v33, v2
	v_mov_b32_e32 v42, v2
	v_mov_b32_e32 v43, v2
	v_mov_b32_e32 v44, v2
	v_mov_b32_e32 v45, v2
	v_mov_b32_e32 v46, v2
	v_mov_b32_e32 v47, v2
	v_mov_b32_e32 v48, v2
	v_mov_b32_e32 v49, v2
	v_mov_b32_e32 v58, v2
	v_mov_b32_e32 v59, v2
	v_mov_b32_e32 v60, v2
	v_mov_b32_e32 v61, v2
	v_mov_b32_e32 v62, v2
	v_mov_b32_e32 v63, v2
	v_mov_b32_e32 v64, v2
	v_mov_b32_e32 v65, v2
	v_mov_b32_e32 v66, v2
	v_mov_b32_e32 v67, v2
	v_mov_b32_e32 v68, v2
	v_mov_b32_e32 v69, v2
	v_mov_b32_e32 v70, v2
	v_mov_b32_e32 v71, v2
	v_mov_b32_e32 v72, v2
	v_mov_b32_e32 v73, v2
	v_mov_b32_e32 v82, v2
	v_mov_b32_e32 v83, v2
	v_mov_b32_e32 v84, v2
	v_mov_b32_e32 v85, v2
	v_mov_b32_e32 v86, v2
	v_mov_b32_e32 v87, v2
	v_mov_b32_e32 v88, v2
	v_mov_b32_e32 v89, v2
	v_mov_b32_e32 v98, v2
	v_mov_b32_e32 v99, v2
	v_mov_b32_e32 v100, v2
	v_mov_b32_e32 v101, v2
	v_mov_b32_e32 v102, v2
	v_mov_b32_e32 v103, v2
	v_mov_b32_e32 v104, v2
	v_mov_b32_e32 v105, v2
	v_mov_b32_e32 v114, v2
	v_mov_b32_e32 v115, v2
	v_mov_b32_e32 v116, v2
	v_mov_b32_e32 v117, v2
	v_mov_b32_e32 v118, v2
	v_mov_b32_e32 v119, v2
	v_mov_b32_e32 v120, v2
	v_mov_b32_e32 v121, v2
	v_mov_b32_e32 v74, v2
	v_mov_b32_e32 v75, v2
	v_mov_b32_e32 v76, v2
	v_mov_b32_e32 v77, v2
	v_mov_b32_e32 v78, v2
	v_mov_b32_e32 v79, v2
	v_mov_b32_e32 v80, v2
	v_mov_b32_e32 v81, v2
	v_mov_b32_e32 v90, v2
	v_mov_b32_e32 v91, v2
	v_mov_b32_e32 v92, v2
	v_mov_b32_e32 v93, v2
	v_mov_b32_e32 v94, v2
	v_mov_b32_e32 v95, v2
	v_mov_b32_e32 v96, v2
	v_mov_b32_e32 v97, v2
	v_mov_b32_e32 v106, v2
	v_mov_b32_e32 v107, v2
	v_mov_b32_e32 v108, v2
	v_mov_b32_e32 v109, v2
	v_mov_b32_e32 v110, v2
	v_mov_b32_e32 v111, v2
	v_mov_b32_e32 v112, v2
	v_mov_b32_e32 v113, v2
	v_mov_b32_e32 v130, v2
	v_mov_b32_e32 v131, v2
	v_mov_b32_e32 v132, v2
	v_mov_b32_e32 v133, v2
	v_mov_b32_e32 v134, v2
	v_mov_b32_e32 v135, v2
	v_mov_b32_e32 v136, v2
	v_mov_b32_e32 v137, v2
	s_branch .LBB0_2359

.LBB0_2467:
	s_add_u32 s8, s30, s12
	s_addc_u32 s9, s31, 0
	s_add_u32 s13, s8, 0x100
	s_addc_u32 s50, s9, 0
	s_and_b64 s[10:11], s[48:49], exec
	s_cselect_b32 s63, s37, s50
	s_cselect_b32 s62, s59, s13
	s_add_u32 s10, s28, s12
	s_addc_u32 s11, s29, 0
	s_add_u32 s12, s10, 0x100
	s_addc_u32 s13, s11, 0
	s_add_i32 s50, 0, 0x10000
	s_and_b64 s[10:11], s[48:49], exec
	s_cselect_b32 s71, s35, s13
	s_cselect_b32 s70, s96, s12
	s_add_i32 s12, 0, 0x14000
	s_add_u32 s10, s8, 0x10080
	s_addc_u32 s11, s9, 0
	s_add_i32 s9, s50, s81
	s_add_i32 m0, s82, 0xc000
	s_add_i32 s8, s82, 0xe000
	s_add_i32 s64, s9, 0x2000
	s_add_u32 s76, s70, 0x10000
	s_addc_u32 s77, s71, 0
	s_add_i32 s65, s12, s81
	v_add_u32_e32 v152, s50, v138
	v_add_u32_e32 v168, s12, v138
	s_add_i32 s74, s65, 0x2000
	s_add_i32 s91, 0, 0x18000
	s_add_i32 s13, 0, 0x1c000
	ds_read_b128 v[140:143], v152
	ds_read_b128 v[144:147], v152 offset:1024
	ds_read_b128 v[148:151], v152 offset:2048
	ds_read_b128 v[152:155], v152 offset:3072
	ds_read_b128 v[156:159], v168
	ds_read_b128 v[160:163], v168 offset:1024
	ds_read_b128 v[164:167], v168 offset:2048
	ds_read_b128 v[168:171], v168 offset:3072
	s_add_u32 s52, s62, 0x10000
	s_addc_u32 s53, s63, 0
	s_add_i32 vcc_hi, s91, s81
	s_add_i32 vcc_lo, vcc_hi, 0x2000
	s_add_u32 s48, s70, 0x10080
	s_addc_u32 s49, s71, 0
	s_add_i32 s50, s13, s81
	s_add_i32 s12, s50, 0x2000
	v_lshl_add_u64 v[204:205], s[10:11], 0, v[128:129]
	ds_read_b128 v[172:175], v139
	ds_read_b128 v[176:179], v139 offset:1024
	ds_read_b128 v[180:183], v139 offset:2048
	ds_read_b128 v[184:187], v139 offset:3072
	ds_read_b128 v[188:191], v139 offset:4096
	ds_read_b128 v[192:195], v139 offset:5120
	ds_read_b128 v[196:199], v139 offset:6144
	ds_read_b128 v[200:203], v139 offset:7168
	global_load_lds_dwordx4 v[204:205], off
	s_mov_b32 m0, s8
	v_lshl_add_u64 v[204:205], s[10:11], 0, v[124:125]
	global_load_lds_dwordx4 v[204:205], off
	s_waitcnt vmcnt(8)
	s_waitcnt lgkmcnt(0)
	s_barrier
	s_waitcnt lgkmcnt(0)
	v_mfma_f32_16x16x32_bf16 v[134:137], v[140:143], v[172:175], v[134:137]
	v_mfma_f32_16x16x32_bf16 v[130:133], v[148:151], v[172:175], v[130:133]
	v_mfma_f32_16x16x32_bf16 v[110:113], v[140:143], v[180:183], v[110:113]
	v_mfma_f32_16x16x32_bf16 v[106:109], v[148:151], v[180:183], v[106:109]
	v_mfma_f32_16x16x32_bf16 v[94:97], v[140:143], v[188:191], v[94:97]
	v_mfma_f32_16x16x32_bf16 v[90:93], v[148:151], v[188:191], v[90:93]
	v_mfma_f32_16x16x32_bf16 v[78:81], v[140:143], v[196:199], v[78:81]
	v_mfma_f32_16x16x32_bf16 v[74:77], v[148:151], v[196:199], v[74:77]
	v_mfma_f32_16x16x32_bf16 v[134:137], v[144:147], v[176:179], v[134:137]
	v_mfma_f32_16x16x32_bf16 v[130:133], v[152:155], v[176:179], v[130:133]
	v_mfma_f32_16x16x32_bf16 v[110:113], v[144:147], v[184:187], v[110:113]
	v_mfma_f32_16x16x32_bf16 v[106:109], v[152:155], v[184:187], v[106:109]
	v_mfma_f32_16x16x32_bf16 v[94:97], v[144:147], v[192:195], v[94:97]
	v_mfma_f32_16x16x32_bf16 v[90:93], v[152:155], v[192:195], v[90:93]
	v_mfma_f32_16x16x32_bf16 v[78:81], v[144:147], v[200:203], v[78:81]
	v_mfma_f32_16x16x32_bf16 v[74:77], v[152:155], v[200:203], v[74:77]
	v_mfma_f32_16x16x32_bf16 v[118:121], v[156:159], v[172:175], v[118:121]
	v_mfma_f32_16x16x32_bf16 v[114:117], v[164:167], v[172:175], v[114:117]
	v_mfma_f32_16x16x32_bf16 v[102:105], v[156:159], v[180:183], v[102:105]
	v_mfma_f32_16x16x32_bf16 v[98:101], v[164:167], v[180:183], v[98:101]
	v_mfma_f32_16x16x32_bf16 v[86:89], v[156:159], v[188:191], v[86:89]
	v_mfma_f32_16x16x32_bf16 v[82:85], v[164:167], v[188:191], v[82:85]
	v_mfma_f32_16x16x32_bf16 v[70:73], v[156:159], v[196:199], v[70:73]
	v_mfma_f32_16x16x32_bf16 v[66:69], v[164:167], v[196:199], v[66:69]
	v_mfma_f32_16x16x32_bf16 v[118:121], v[160:163], v[176:179], v[118:121]
	v_mfma_f32_16x16x32_bf16 v[114:117], v[168:171], v[176:179], v[114:117]
	v_mfma_f32_16x16x32_bf16 v[102:105], v[160:163], v[184:187], v[102:105]
	v_mfma_f32_16x16x32_bf16 v[98:101], v[168:171], v[184:187], v[98:101]
	v_mfma_f32_16x16x32_bf16 v[86:89], v[160:163], v[192:195], v[86:89]
	v_mfma_f32_16x16x32_bf16 v[82:85], v[168:171], v[192:195], v[82:85]
	v_mfma_f32_16x16x32_bf16 v[70:73], v[160:163], v[200:203], v[70:73]
	v_mfma_f32_16x16x32_bf16 v[66:69], v[168:171], v[200:203], v[66:69]
	s_barrier
	s_mov_b32 m0, s9
	v_lshl_add_u64 v[204:205], s[70:71], 0, v[126:127]
	ds_read_b128 v[172:175], v139 offset:16384
	ds_read_b128 v[176:179], v139 offset:17408
	ds_read_b128 v[180:183], v139 offset:18432
	ds_read_b128 v[184:187], v139 offset:19456
	ds_read_b128 v[188:191], v139 offset:20480
	ds_read_b128 v[192:195], v139 offset:21504
	ds_read_b128 v[196:199], v139 offset:22528
	ds_read_b128 v[200:203], v139 offset:23552
	global_load_lds_dwordx4 v[204:205], off
	v_lshl_add_u64 v[206:207], s[70:71], 0, v[122:123]
	s_mov_b32 m0, s64
	v_lshl_add_u64 v[208:209], s[76:77], 0, v[126:127]
	global_load_lds_dwordx4 v[206:207], off
	s_mov_b32 m0, s65
	v_lshl_add_u64 v[216:217], s[62:63], 0, v[124:125]
	global_load_lds_dwordx4 v[208:209], off
	s_mov_b32 m0, s74
	v_lshl_add_u64 v[208:209], s[76:77], 0, v[122:123]
	global_load_lds_dwordx4 v[208:209], off
	s_mov_b32 m0, s82
	v_lshl_add_u64 v[208:209], s[62:63], 0, v[128:129]
	global_load_lds_dwordx4 v[208:209], off
	s_mov_b32 m0, s92
	s_nop 0
	global_load_lds_dwordx4 v[216:217], off
	s_waitcnt vmcnt(8)
	s_waitcnt lgkmcnt(0)
	s_barrier
	s_waitcnt lgkmcnt(0)
	v_mfma_f32_16x16x32_bf16 v[62:65], v[140:143], v[172:175], v[62:65]
	v_mfma_f32_16x16x32_bf16 v[58:61], v[148:151], v[172:175], v[58:61]
	v_mfma_f32_16x16x32_bf16 v[46:49], v[140:143], v[180:183], v[46:49]
	v_mfma_f32_16x16x32_bf16 v[42:45], v[148:151], v[180:183], v[42:45]
	v_mfma_f32_16x16x32_bf16 v[30:33], v[140:143], v[188:191], v[30:33]
	v_mfma_f32_16x16x32_bf16 v[26:29], v[148:151], v[188:191], v[26:29]
	v_mfma_f32_16x16x32_bf16 v[14:17], v[140:143], v[196:199], v[14:17]
	v_mfma_f32_16x16x32_bf16 v[10:13], v[148:151], v[196:199], v[10:13]
	v_mfma_f32_16x16x32_bf16 v[62:65], v[144:147], v[176:179], v[62:65]
	v_mfma_f32_16x16x32_bf16 v[58:61], v[152:155], v[176:179], v[58:61]
	v_mfma_f32_16x16x32_bf16 v[46:49], v[144:147], v[184:187], v[46:49]
	v_mfma_f32_16x16x32_bf16 v[42:45], v[152:155], v[184:187], v[42:45]
	v_mfma_f32_16x16x32_bf16 v[30:33], v[144:147], v[192:195], v[30:33]
	v_mfma_f32_16x16x32_bf16 v[26:29], v[152:155], v[192:195], v[26:29]
	v_mfma_f32_16x16x32_bf16 v[14:17], v[144:147], v[200:203], v[14:17]
	v_mfma_f32_16x16x32_bf16 v[10:13], v[152:155], v[200:203], v[10:13]
	v_mfma_f32_16x16x32_bf16 v[54:57], v[156:159], v[172:175], v[54:57]
	v_mfma_f32_16x16x32_bf16 v[50:53], v[164:167], v[172:175], v[50:53]
	v_mfma_f32_16x16x32_bf16 v[38:41], v[156:159], v[180:183], v[38:41]
	v_mfma_f32_16x16x32_bf16 v[34:37], v[164:167], v[180:183], v[34:37]
	v_mfma_f32_16x16x32_bf16 v[22:25], v[156:159], v[188:191], v[22:25]
	v_mfma_f32_16x16x32_bf16 v[18:21], v[164:167], v[188:191], v[18:21]
	v_mfma_f32_16x16x32_bf16 v[6:9], v[156:159], v[196:199], v[6:9]
	v_mfma_f32_16x16x32_bf16 v[2:5], v[164:167], v[196:199], v[2:5]
	v_mfma_f32_16x16x32_bf16 v[54:57], v[160:163], v[176:179], v[54:57]
	v_mfma_f32_16x16x32_bf16 v[50:53], v[168:171], v[176:179], v[50:53]
	v_mfma_f32_16x16x32_bf16 v[38:41], v[160:163], v[184:187], v[38:41]
	v_mfma_f32_16x16x32_bf16 v[34:37], v[168:171], v[184:187], v[34:37]
	v_mfma_f32_16x16x32_bf16 v[22:25], v[160:163], v[192:195], v[22:25]
	v_mfma_f32_16x16x32_bf16 v[18:21], v[168:171], v[192:195], v[18:21]
	v_mfma_f32_16x16x32_bf16 v[6:9], v[160:163], v[200:203], v[6:9]
	v_mfma_f32_16x16x32_bf16 v[2:5], v[168:171], v[200:203], v[2:5]
	s_barrier
	v_add_u32_e32 v152, s91, v138
	v_add_u32_e32 v168, s13, v138
	ds_read_b128 v[140:143], v152
	ds_read_b128 v[144:147], v152 offset:1024
	ds_read_b128 v[148:151], v152 offset:2048
	ds_read_b128 v[152:155], v152 offset:3072
	ds_read_b128 v[156:159], v168
	ds_read_b128 v[160:163], v168 offset:1024
	ds_read_b128 v[164:167], v168 offset:2048
	ds_read_b128 v[168:171], v168 offset:3072
	s_mov_b32 m0, s84
	v_lshl_add_u64 v[218:219], s[52:53], 0, v[128:129]
	ds_read_b128 v[172:175], v139 offset:32768
	ds_read_b128 v[176:179], v139 offset:33792
	ds_read_b128 v[180:183], v139 offset:34816
	ds_read_b128 v[184:187], v139 offset:35840
	ds_read_b128 v[188:191], v139 offset:36864
	ds_read_b128 v[192:195], v139 offset:37888
	ds_read_b128 v[196:199], v139 offset:38912
	ds_read_b128 v[200:203], v139 offset:39936
	global_load_lds_dwordx4 v[218:219], off
	s_mov_b32 m0, s90
	v_lshl_add_u64 v[218:219], s[52:53], 0, v[124:125]
	global_load_lds_dwordx4 v[218:219], off
	s_waitcnt vmcnt(8)
	s_waitcnt lgkmcnt(0)
	s_barrier
	s_waitcnt lgkmcnt(0)
	v_mfma_f32_16x16x32_bf16 v[134:137], v[140:143], v[172:175], v[134:137]
	v_mfma_f32_16x16x32_bf16 v[130:133], v[148:151], v[172:175], v[130:133]
	v_mfma_f32_16x16x32_bf16 v[110:113], v[140:143], v[180:183], v[110:113]
	v_mfma_f32_16x16x32_bf16 v[106:109], v[148:151], v[180:183], v[106:109]
	v_mfma_f32_16x16x32_bf16 v[94:97], v[140:143], v[188:191], v[94:97]
	v_mfma_f32_16x16x32_bf16 v[90:93], v[148:151], v[188:191], v[90:93]
	v_mfma_f32_16x16x32_bf16 v[78:81], v[140:143], v[196:199], v[78:81]
	v_mfma_f32_16x16x32_bf16 v[74:77], v[148:151], v[196:199], v[74:77]
	v_mfma_f32_16x16x32_bf16 v[134:137], v[144:147], v[176:179], v[134:137]
	v_mfma_f32_16x16x32_bf16 v[130:133], v[152:155], v[176:179], v[130:133]
	v_mfma_f32_16x16x32_bf16 v[110:113], v[144:147], v[184:187], v[110:113]
	v_mfma_f32_16x16x32_bf16 v[106:109], v[152:155], v[184:187], v[106:109]
	v_mfma_f32_16x16x32_bf16 v[94:97], v[144:147], v[192:195], v[94:97]
	v_mfma_f32_16x16x32_bf16 v[90:93], v[152:155], v[192:195], v[90:93]
	v_mfma_f32_16x16x32_bf16 v[78:81], v[144:147], v[200:203], v[78:81]
	v_mfma_f32_16x16x32_bf16 v[74:77], v[152:155], v[200:203], v[74:77]
	v_mfma_f32_16x16x32_bf16 v[118:121], v[156:159], v[172:175], v[118:121]
	v_mfma_f32_16x16x32_bf16 v[114:117], v[164:167], v[172:175], v[114:117]
	v_mfma_f32_16x16x32_bf16 v[102:105], v[156:159], v[180:183], v[102:105]
	v_mfma_f32_16x16x32_bf16 v[98:101], v[164:167], v[180:183], v[98:101]
	v_mfma_f32_16x16x32_bf16 v[86:89], v[156:159], v[188:191], v[86:89]
	v_mfma_f32_16x16x32_bf16 v[82:85], v[164:167], v[188:191], v[82:85]
	v_mfma_f32_16x16x32_bf16 v[70:73], v[156:159], v[196:199], v[70:73]
	v_mfma_f32_16x16x32_bf16 v[66:69], v[164:167], v[196:199], v[66:69]
	v_mfma_f32_16x16x32_bf16 v[118:121], v[160:163], v[176:179], v[118:121]
	v_mfma_f32_16x16x32_bf16 v[114:117], v[168:171], v[176:179], v[114:117]
	v_mfma_f32_16x16x32_bf16 v[102:105], v[160:163], v[184:187], v[102:105]
	v_mfma_f32_16x16x32_bf16 v[98:101], v[168:171], v[184:187], v[98:101]
	v_mfma_f32_16x16x32_bf16 v[86:89], v[160:163], v[192:195], v[86:89]
	v_mfma_f32_16x16x32_bf16 v[82:85], v[168:171], v[192:195], v[82:85]
	v_mfma_f32_16x16x32_bf16 v[70:73], v[160:163], v[200:203], v[70:73]
	v_mfma_f32_16x16x32_bf16 v[66:69], v[168:171], v[200:203], v[66:69]
	s_barrier
	s_mov_b32 m0, vcc_hi
	v_lshl_add_u64 v[204:205], v[204:205], 0, s[56:57]
	ds_read_b128 v[172:175], v139 offset:49152
	ds_read_b128 v[176:179], v139 offset:50176
	ds_read_b128 v[180:183], v139 offset:51200
	ds_read_b128 v[184:187], v139 offset:52224
	ds_read_b128 v[188:191], v139 offset:53248
	ds_read_b128 v[192:195], v139 offset:54272
	ds_read_b128 v[196:199], v139 offset:55296
	ds_read_b128 v[200:203], v139 offset:56320
	global_load_lds_dwordx4 v[204:205], off
	s_mov_b32 m0, vcc_lo
	v_lshl_add_u64 v[204:205], v[206:207], 0, s[56:57]
	global_load_lds_dwordx4 v[204:205], off
	s_mov_b32 m0, s50
	v_lshl_add_u64 v[204:205], s[48:49], 0, v[126:127]
	global_load_lds_dwordx4 v[204:205], off
	s_mov_b32 m0, s12
	v_lshl_add_u64 v[204:205], s[48:49], 0, v[122:123]
	global_load_lds_dwordx4 v[204:205], off
	s_mov_b32 m0, s68
	v_lshl_add_u64 v[204:205], v[208:209], 0, s[56:57]
	global_load_lds_dwordx4 v[204:205], off
	s_mov_b32 m0, s93
	v_lshl_add_u64 v[204:205], v[216:217], 0, s[56:57]
	global_load_lds_dwordx4 v[204:205], off
	s_waitcnt vmcnt(8)
	s_waitcnt lgkmcnt(0)
	s_barrier
	s_waitcnt lgkmcnt(0)
	v_mfma_f32_16x16x32_bf16 v[62:65], v[140:143], v[172:175], v[62:65]
	v_mfma_f32_16x16x32_bf16 v[58:61], v[148:151], v[172:175], v[58:61]
	v_mfma_f32_16x16x32_bf16 v[46:49], v[140:143], v[180:183], v[46:49]
	v_mfma_f32_16x16x32_bf16 v[42:45], v[148:151], v[180:183], v[42:45]
	v_mfma_f32_16x16x32_bf16 v[30:33], v[140:143], v[188:191], v[30:33]
	v_mfma_f32_16x16x32_bf16 v[26:29], v[148:151], v[188:191], v[26:29]
	v_mfma_f32_16x16x32_bf16 v[14:17], v[140:143], v[196:199], v[14:17]
	v_mfma_f32_16x16x32_bf16 v[10:13], v[148:151], v[196:199], v[10:13]
	v_mfma_f32_16x16x32_bf16 v[62:65], v[144:147], v[176:179], v[62:65]
	v_mfma_f32_16x16x32_bf16 v[58:61], v[152:155], v[176:179], v[58:61]
	v_mfma_f32_16x16x32_bf16 v[46:49], v[144:147], v[184:187], v[46:49]
	v_mfma_f32_16x16x32_bf16 v[42:45], v[152:155], v[184:187], v[42:45]
	v_mfma_f32_16x16x32_bf16 v[30:33], v[144:147], v[192:195], v[30:33]
	v_mfma_f32_16x16x32_bf16 v[26:29], v[152:155], v[192:195], v[26:29]
	v_mfma_f32_16x16x32_bf16 v[14:17], v[144:147], v[200:203], v[14:17]
	v_mfma_f32_16x16x32_bf16 v[10:13], v[152:155], v[200:203], v[10:13]
	v_mfma_f32_16x16x32_bf16 v[54:57], v[156:159], v[172:175], v[54:57]
	v_mfma_f32_16x16x32_bf16 v[50:53], v[164:167], v[172:175], v[50:53]
	v_mfma_f32_16x16x32_bf16 v[38:41], v[156:159], v[180:183], v[38:41]
	v_mfma_f32_16x16x32_bf16 v[34:37], v[164:167], v[180:183], v[34:37]
	v_mfma_f32_16x16x32_bf16 v[22:25], v[156:159], v[188:191], v[22:25]
	v_mfma_f32_16x16x32_bf16 v[18:21], v[164:167], v[188:191], v[18:21]
	v_mfma_f32_16x16x32_bf16 v[6:9], v[156:159], v[196:199], v[6:9]
	v_mfma_f32_16x16x32_bf16 v[2:5], v[164:167], v[196:199], v[2:5]
	v_mfma_f32_16x16x32_bf16 v[54:57], v[160:163], v[176:179], v[54:57]
	v_mfma_f32_16x16x32_bf16 v[50:53], v[168:171], v[176:179], v[50:53]
	v_mfma_f32_16x16x32_bf16 v[38:41], v[160:163], v[184:187], v[38:41]
	v_mfma_f32_16x16x32_bf16 v[34:37], v[168:171], v[184:187], v[34:37]
	v_mfma_f32_16x16x32_bf16 v[22:25], v[160:163], v[192:195], v[22:25]
	v_mfma_f32_16x16x32_bf16 v[18:21], v[168:171], v[192:195], v[18:21]
	v_mfma_f32_16x16x32_bf16 v[6:9], v[160:163], v[200:203], v[6:9]
	v_mfma_f32_16x16x32_bf16 v[2:5], v[168:171], v[200:203], v[2:5]
	s_barrier
	s_movk_i32 s12, 0x100
	s_andn2_b64 vcc, exec, s[46:47]
	s_mov_b64 s[48:49], -1
	s_mov_b64 s[46:47], 0
	s_cbranch_vccz .LBB0_2467
	s_andn2_b64 vcc, exec, s[40:41]
	s_cbranch_vccnz .LBB0_2459
	v_mov_b32_e32 v2, 0
	s_mov_b32 s14, s34
	s_mov_b32 s95, s36
	s_mov_b64 s[28:29], s[44:45]
	s_mov_b64 s[30:31], s[42:43]
	s_mov_b32 s94, s58
	v_mov_b32_e32 v3, v2
	v_mov_b32_e32 v4, v2
	v_mov_b32_e32 v5, v2
	v_mov_b32_e32 v6, v2
	v_mov_b32_e32 v7, v2
	v_mov_b32_e32 v8, v2
	v_mov_b32_e32 v9, v2
	v_mov_b32_e32 v18, v2
	v_mov_b32_e32 v19, v2
	v_mov_b32_e32 v20, v2
	v_mov_b32_e32 v21, v2
	v_mov_b32_e32 v22, v2
	v_mov_b32_e32 v23, v2
	v_mov_b32_e32 v24, v2
	v_mov_b32_e32 v25, v2
	v_mov_b32_e32 v34, v2
	v_mov_b32_e32 v35, v2
	v_mov_b32_e32 v36, v2
	v_mov_b32_e32 v37, v2
	v_mov_b32_e32 v38, v2
	v_mov_b32_e32 v39, v2
	v_mov_b32_e32 v40, v2
	v_mov_b32_e32 v41, v2
	v_mov_b32_e32 v50, v2
	v_mov_b32_e32 v51, v2
	v_mov_b32_e32 v52, v2
	v_mov_b32_e32 v53, v2
	v_mov_b32_e32 v54, v2
	v_mov_b32_e32 v55, v2
	v_mov_b32_e32 v56, v2
	v_mov_b32_e32 v57, v2
	v_mov_b32_e32 v10, v2
	v_mov_b32_e32 v11, v2
	v_mov_b32_e32 v12, v2
	v_mov_b32_e32 v13, v2
	v_mov_b32_e32 v14, v2
	v_mov_b32_e32 v15, v2
	v_mov_b32_e32 v16, v2
	v_mov_b32_e32 v17, v2
	v_mov_b32_e32 v26, v2
	v_mov_b32_e32 v27, v2
	v_mov_b32_e32 v28, v2
	v_mov_b32_e32 v29, v2
	v_mov_b32_e32 v30, v2
	v_mov_b32_e32 v31, v2
	v_mov_b32_e32 v32, v2
	v_mov_b32_e32 v33, v2
	v_mov_b32_e32 v42, v2
	v_mov_b32_e32 v43, v2
	v_mov_b32_e32 v44, v2
	v_mov_b32_e32 v45, v2
	v_mov_b32_e32 v46, v2
	v_mov_b32_e32 v47, v2
	v_mov_b32_e32 v48, v2
	v_mov_b32_e32 v49, v2
	v_mov_b32_e32 v58, v2
	v_mov_b32_e32 v59, v2
	v_mov_b32_e32 v60, v2
	v_mov_b32_e32 v61, v2
	v_mov_b32_e32 v62, v2
	v_mov_b32_e32 v63, v2
	v_mov_b32_e32 v64, v2
	v_mov_b32_e32 v65, v2
	v_mov_b32_e32 v66, v2
	v_mov_b32_e32 v67, v2
	v_mov_b32_e32 v68, v2
	v_mov_b32_e32 v69, v2
	v_mov_b32_e32 v70, v2
	v_mov_b32_e32 v71, v2
	v_mov_b32_e32 v72, v2
	v_mov_b32_e32 v73, v2
	v_mov_b32_e32 v82, v2
	v_mov_b32_e32 v83, v2
	v_mov_b32_e32 v84, v2
	v_mov_b32_e32 v85, v2
	v_mov_b32_e32 v86, v2
	v_mov_b32_e32 v87, v2
	v_mov_b32_e32 v88, v2
	v_mov_b32_e32 v89, v2
	v_mov_b32_e32 v98, v2
	v_mov_b32_e32 v99, v2
	v_mov_b32_e32 v100, v2
	v_mov_b32_e32 v101, v2
	v_mov_b32_e32 v102, v2
	v_mov_b32_e32 v103, v2
	v_mov_b32_e32 v104, v2
	v_mov_b32_e32 v105, v2
	v_mov_b32_e32 v114, v2
	v_mov_b32_e32 v115, v2
	v_mov_b32_e32 v116, v2
	v_mov_b32_e32 v117, v2
	v_mov_b32_e32 v118, v2
	v_mov_b32_e32 v119, v2
	v_mov_b32_e32 v120, v2
	v_mov_b32_e32 v121, v2
	v_mov_b32_e32 v74, v2
	v_mov_b32_e32 v75, v2
	v_mov_b32_e32 v76, v2
	v_mov_b32_e32 v77, v2
	v_mov_b32_e32 v78, v2
	v_mov_b32_e32 v79, v2
	v_mov_b32_e32 v80, v2
	v_mov_b32_e32 v81, v2
	v_mov_b32_e32 v90, v2
	v_mov_b32_e32 v91, v2
	v_mov_b32_e32 v92, v2
	v_mov_b32_e32 v93, v2
	v_mov_b32_e32 v94, v2
	v_mov_b32_e32 v95, v2
	v_mov_b32_e32 v96, v2
	v_mov_b32_e32 v97, v2
	v_mov_b32_e32 v106, v2
	v_mov_b32_e32 v107, v2
	v_mov_b32_e32 v108, v2
	v_mov_b32_e32 v109, v2
	v_mov_b32_e32 v110, v2
	v_mov_b32_e32 v111, v2
	v_mov_b32_e32 v112, v2
	v_mov_b32_e32 v113, v2
	v_mov_b32_e32 v130, v2
	v_mov_b32_e32 v131, v2
	v_mov_b32_e32 v132, v2
	v_mov_b32_e32 v133, v2
	v_mov_b32_e32 v134, v2
	v_mov_b32_e32 v135, v2
	v_mov_b32_e32 v136, v2
	v_mov_b32_e32 v137, v2
	s_branch .LBB0_2459

.Lnobar_c6:
.LBB0_2626:
	s_add_u32 s26, s6, 0xfffc0080
	s_addc_u32 s27, s7, -1
	s_add_i32 s50, 0, 0x10000
	s_cmp_eq_u32 s49, 12
	s_cselect_b32 s29, s21, s27
	s_cselect_b32 s28, s33, s26
	v_add_u32_e32 v0, s50, v181
	s_cselect_b32 s27, s19, s48
	s_cselect_b32 s26, s40, s41
	s_add_i32 s58, 0, 0x14000
	ds_read_b128 v[130:133], v0
	ds_read_b128 v[134:137], v0 offset:1024
	ds_read_b128 v[138:141], v0 offset:2048
	ds_read_b128 v[142:145], v0 offset:3072
	v_add_u32_e32 v0, s58, v181
	ds_read_b128 v[146:149], v0
	ds_read_b128 v[150:153], v0 offset:1024
	ds_read_b128 v[154:157], v0 offset:2048
	ds_read_b128 v[170:173], v0 offset:3072
	v_lshl_add_u64 v[178:179], s[6:7], 0, v[168:169]
	s_add_i32 m0, s36, 0xc000
	ds_read_b128 v[174:177], v183
	ds_read_b128 v[184:187], v183 offset:1024
	ds_read_b128 v[188:191], v183 offset:2048
	ds_read_b128 v[192:195], v183 offset:3072
	ds_read_b128 v[196:199], v183 offset:4096
	ds_read_b128 v[200:203], v183 offset:5120
	ds_read_b128 v[204:207], v183 offset:6144
	ds_read_b128 v[216:219], v183 offset:7168
	global_load_lds_dwordx4 v[178:179], off
	s_add_i32 m0, s36, 0xe000
	v_lshl_add_u64 v[178:179], s[6:7], 0, v[166:167]
	global_load_lds_dwordx4 v[178:179], off
	s_waitcnt vmcnt(8)
	s_waitcnt lgkmcnt(0)
	s_barrier
	s_waitcnt lgkmcnt(0)
	v_mfma_f32_16x16x32_bf16 v[126:129], v[130:133], v[174:177], v[126:129]
	v_mfma_f32_16x16x32_bf16 v[122:125], v[138:141], v[174:177], v[122:125]
	v_mfma_f32_16x16x32_bf16 v[110:113], v[130:133], v[188:191], v[110:113]
	v_mfma_f32_16x16x32_bf16 v[106:109], v[138:141], v[188:191], v[106:109]
	v_mfma_f32_16x16x32_bf16 v[94:97], v[130:133], v[196:199], v[94:97]
	v_mfma_f32_16x16x32_bf16 v[90:93], v[138:141], v[196:199], v[90:93]
	v_mfma_f32_16x16x32_bf16 v[78:81], v[130:133], v[204:207], v[78:81]
	v_mfma_f32_16x16x32_bf16 v[74:77], v[138:141], v[204:207], v[74:77]
	v_mfma_f32_16x16x32_bf16 v[126:129], v[134:137], v[184:187], v[126:129]
	v_mfma_f32_16x16x32_bf16 v[122:125], v[142:145], v[184:187], v[122:125]
	v_mfma_f32_16x16x32_bf16 v[110:113], v[134:137], v[192:195], v[110:113]
	v_mfma_f32_16x16x32_bf16 v[106:109], v[142:145], v[192:195], v[106:109]
	v_mfma_f32_16x16x32_bf16 v[94:97], v[134:137], v[200:203], v[94:97]
	v_mfma_f32_16x16x32_bf16 v[90:93], v[142:145], v[200:203], v[90:93]
	v_mfma_f32_16x16x32_bf16 v[78:81], v[134:137], v[216:219], v[78:81]
	v_mfma_f32_16x16x32_bf16 v[74:77], v[142:145], v[216:219], v[74:77]
	v_mfma_f32_16x16x32_bf16 v[118:121], v[146:149], v[174:177], v[118:121]
	v_mfma_f32_16x16x32_bf16 v[114:117], v[154:157], v[174:177], v[114:117]
	v_mfma_f32_16x16x32_bf16 v[102:105], v[146:149], v[188:191], v[102:105]
	v_mfma_f32_16x16x32_bf16 v[98:101], v[154:157], v[188:191], v[98:101]
	v_mfma_f32_16x16x32_bf16 v[86:89], v[146:149], v[196:199], v[86:89]
	v_mfma_f32_16x16x32_bf16 v[82:85], v[154:157], v[196:199], v[82:85]
	v_mfma_f32_16x16x32_bf16 v[70:73], v[146:149], v[204:207], v[70:73]
	v_mfma_f32_16x16x32_bf16 v[66:69], v[154:157], v[204:207], v[66:69]
	v_mfma_f32_16x16x32_bf16 v[118:121], v[150:153], v[184:187], v[118:121]
	v_mfma_f32_16x16x32_bf16 v[114:117], v[170:173], v[184:187], v[114:117]
	v_mfma_f32_16x16x32_bf16 v[102:105], v[150:153], v[192:195], v[102:105]
	v_mfma_f32_16x16x32_bf16 v[98:101], v[170:173], v[192:195], v[98:101]
	v_mfma_f32_16x16x32_bf16 v[86:89], v[150:153], v[200:203], v[86:89]
	v_mfma_f32_16x16x32_bf16 v[82:85], v[170:173], v[200:203], v[82:85]
	v_mfma_f32_16x16x32_bf16 v[70:73], v[150:153], v[216:219], v[70:73]
	v_mfma_f32_16x16x32_bf16 v[66:69], v[170:173], v[216:219], v[66:69]
	s_barrier
	s_add_i32 s50, s50, s35
	v_lshl_add_u64 v[178:179], s[26:27], 0, v[162:163]
	s_mov_b32 m0, s50
	ds_read_b128 v[174:177], v183 offset:16384
	ds_read_b128 v[184:187], v183 offset:17408
	ds_read_b128 v[188:191], v183 offset:18432
	ds_read_b128 v[192:195], v183 offset:19456
	ds_read_b128 v[196:199], v183 offset:20480
	ds_read_b128 v[200:203], v183 offset:21504
	ds_read_b128 v[204:207], v183 offset:22528
	ds_read_b128 v[216:219], v183 offset:23552
	global_load_lds_dwordx4 v[178:179], off
	s_add_i32 m0, s50, 0x2000
	s_add_u32 s52, s26, 0x40000
	v_lshl_add_u64 v[208:209], s[26:27], 0, v[158:159]
	s_addc_u32 s53, s27, 0
	s_add_i32 s50, s58, s35
	global_load_lds_dwordx4 v[208:209], off
	v_lshl_add_u64 v[220:221], s[52:53], 0, v[162:163]
	s_mov_b32 m0, s50
	v_lshl_add_u64 v[222:223], s[28:29], 0, v[160:161]
	global_load_lds_dwordx4 v[220:221], off
	s_add_i32 m0, s50, 0x2000
	v_lshl_add_u64 v[220:221], s[52:53], 0, v[158:159]
	global_load_lds_dwordx4 v[220:221], off
	s_mov_b32 m0, s36
	v_lshl_add_u64 v[220:221], s[28:29], 0, v[164:165]
	global_load_lds_dwordx4 v[220:221], off
	s_mov_b32 m0, s37
	s_nop 0
	global_load_lds_dwordx4 v[222:223], off
	s_waitcnt vmcnt(8)
	s_waitcnt lgkmcnt(0)
	s_barrier
	s_waitcnt lgkmcnt(0)
	v_mfma_f32_16x16x32_bf16 v[62:65], v[130:133], v[174:177], v[62:65]
	v_mfma_f32_16x16x32_bf16 v[58:61], v[138:141], v[174:177], v[58:61]
	v_mfma_f32_16x16x32_bf16 v[46:49], v[130:133], v[188:191], v[46:49]
	v_mfma_f32_16x16x32_bf16 v[42:45], v[138:141], v[188:191], v[42:45]
	v_mfma_f32_16x16x32_bf16 v[30:33], v[130:133], v[196:199], v[30:33]
	v_mfma_f32_16x16x32_bf16 v[26:29], v[138:141], v[196:199], v[26:29]
	v_mfma_f32_16x16x32_bf16 v[14:17], v[130:133], v[204:207], v[14:17]
	v_mfma_f32_16x16x32_bf16 v[10:13], v[138:141], v[204:207], v[10:13]
	v_mfma_f32_16x16x32_bf16 v[62:65], v[134:137], v[184:187], v[62:65]
	v_mfma_f32_16x16x32_bf16 v[58:61], v[142:145], v[184:187], v[58:61]
	v_mfma_f32_16x16x32_bf16 v[46:49], v[134:137], v[192:195], v[46:49]
	v_mfma_f32_16x16x32_bf16 v[42:45], v[142:145], v[192:195], v[42:45]
	v_mfma_f32_16x16x32_bf16 v[30:33], v[134:137], v[200:203], v[30:33]
	v_mfma_f32_16x16x32_bf16 v[26:29], v[142:145], v[200:203], v[26:29]
	v_mfma_f32_16x16x32_bf16 v[14:17], v[134:137], v[216:219], v[14:17]
	v_mfma_f32_16x16x32_bf16 v[10:13], v[142:145], v[216:219], v[10:13]
	v_mfma_f32_16x16x32_bf16 v[54:57], v[146:149], v[174:177], v[54:57]
	v_mfma_f32_16x16x32_bf16 v[50:53], v[154:157], v[174:177], v[50:53]
	v_mfma_f32_16x16x32_bf16 v[38:41], v[146:149], v[188:191], v[38:41]
	v_mfma_f32_16x16x32_bf16 v[34:37], v[154:157], v[188:191], v[34:37]
	v_mfma_f32_16x16x32_bf16 v[22:25], v[146:149], v[196:199], v[22:25]
	v_mfma_f32_16x16x32_bf16 v[18:21], v[154:157], v[196:199], v[18:21]
	v_mfma_f32_16x16x32_bf16 v[6:9], v[146:149], v[204:207], v[6:9]
	v_mfma_f32_16x16x32_bf16 v[2:5], v[154:157], v[204:207], v[2:5]
	v_mfma_f32_16x16x32_bf16 v[54:57], v[150:153], v[184:187], v[54:57]
	v_mfma_f32_16x16x32_bf16 v[50:53], v[170:173], v[184:187], v[50:53]
	v_mfma_f32_16x16x32_bf16 v[38:41], v[150:153], v[192:195], v[38:41]
	v_mfma_f32_16x16x32_bf16 v[34:37], v[170:173], v[192:195], v[34:37]
	v_mfma_f32_16x16x32_bf16 v[22:25], v[150:153], v[200:203], v[22:25]
	v_mfma_f32_16x16x32_bf16 v[18:21], v[170:173], v[200:203], v[18:21]
	v_mfma_f32_16x16x32_bf16 v[6:9], v[150:153], v[216:219], v[6:9]
	v_mfma_f32_16x16x32_bf16 v[2:5], v[170:173], v[216:219], v[2:5]
	s_barrier
	s_add_i32 s50, 0, 0x18000
	v_add_u32_e32 v0, s50, v181
	s_add_i32 s52, 0, 0x1c000
	ds_read_b128 v[130:133], v0
	ds_read_b128 v[134:137], v0 offset:1024
	ds_read_b128 v[138:141], v0 offset:2048
	ds_read_b128 v[142:145], v0 offset:3072
	v_add_u32_e32 v0, s52, v181
	ds_read_b128 v[146:149], v0
	ds_read_b128 v[150:153], v0 offset:1024
	ds_read_b128 v[154:157], v0 offset:2048
	ds_read_b128 v[170:173], v0 offset:3072
	s_add_u32 s28, s28, 0x40000
	s_addc_u32 s29, s29, 0
	s_mov_b32 m0, s42
	v_lshl_add_u64 v[224:225], s[28:29], 0, v[164:165]
	ds_read_b128 v[174:177], v183 offset:32768
	ds_read_b128 v[184:187], v183 offset:33792
	ds_read_b128 v[188:191], v183 offset:34816
	ds_read_b128 v[192:195], v183 offset:35840
	ds_read_b128 v[196:199], v183 offset:36864
	ds_read_b128 v[200:203], v183 offset:37888
	ds_read_b128 v[204:207], v183 offset:38912
	ds_read_b128 v[216:219], v183 offset:39936
	global_load_lds_dwordx4 v[224:225], off
	s_mov_b32 m0, s43
	v_lshl_add_u64 v[224:225], s[28:29], 0, v[160:161]
	global_load_lds_dwordx4 v[224:225], off
	s_waitcnt vmcnt(8)
	s_waitcnt lgkmcnt(0)
	s_barrier
	s_waitcnt lgkmcnt(0)
	v_mfma_f32_16x16x32_bf16 v[126:129], v[130:133], v[174:177], v[126:129]
	v_mfma_f32_16x16x32_bf16 v[122:125], v[138:141], v[174:177], v[122:125]
	v_mfma_f32_16x16x32_bf16 v[110:113], v[130:133], v[188:191], v[110:113]
	v_mfma_f32_16x16x32_bf16 v[106:109], v[138:141], v[188:191], v[106:109]
	v_mfma_f32_16x16x32_bf16 v[94:97], v[130:133], v[196:199], v[94:97]
	v_mfma_f32_16x16x32_bf16 v[90:93], v[138:141], v[196:199], v[90:93]
	v_mfma_f32_16x16x32_bf16 v[78:81], v[130:133], v[204:207], v[78:81]
	v_mfma_f32_16x16x32_bf16 v[74:77], v[138:141], v[204:207], v[74:77]
	v_mfma_f32_16x16x32_bf16 v[126:129], v[134:137], v[184:187], v[126:129]
	v_mfma_f32_16x16x32_bf16 v[122:125], v[142:145], v[184:187], v[122:125]
	v_mfma_f32_16x16x32_bf16 v[110:113], v[134:137], v[192:195], v[110:113]
	v_mfma_f32_16x16x32_bf16 v[106:109], v[142:145], v[192:195], v[106:109]
	v_mfma_f32_16x16x32_bf16 v[94:97], v[134:137], v[200:203], v[94:97]
	v_mfma_f32_16x16x32_bf16 v[90:93], v[142:145], v[200:203], v[90:93]
	v_mfma_f32_16x16x32_bf16 v[78:81], v[134:137], v[216:219], v[78:81]
	v_mfma_f32_16x16x32_bf16 v[74:77], v[142:145], v[216:219], v[74:77]
	v_mfma_f32_16x16x32_bf16 v[118:121], v[146:149], v[174:177], v[118:121]
	v_mfma_f32_16x16x32_bf16 v[114:117], v[154:157], v[174:177], v[114:117]
	v_mfma_f32_16x16x32_bf16 v[102:105], v[146:149], v[188:191], v[102:105]
	v_mfma_f32_16x16x32_bf16 v[98:101], v[154:157], v[188:191], v[98:101]
	v_mfma_f32_16x16x32_bf16 v[86:89], v[146:149], v[196:199], v[86:89]
	v_mfma_f32_16x16x32_bf16 v[82:85], v[154:157], v[196:199], v[82:85]
	v_mfma_f32_16x16x32_bf16 v[70:73], v[146:149], v[204:207], v[70:73]
	v_mfma_f32_16x16x32_bf16 v[66:69], v[154:157], v[204:207], v[66:69]
	v_mfma_f32_16x16x32_bf16 v[118:121], v[150:153], v[184:187], v[118:121]
	v_mfma_f32_16x16x32_bf16 v[114:117], v[170:173], v[184:187], v[114:117]
	v_mfma_f32_16x16x32_bf16 v[102:105], v[150:153], v[192:195], v[102:105]
	v_mfma_f32_16x16x32_bf16 v[98:101], v[170:173], v[192:195], v[98:101]
	v_mfma_f32_16x16x32_bf16 v[86:89], v[150:153], v[200:203], v[86:89]
	v_mfma_f32_16x16x32_bf16 v[82:85], v[170:173], v[200:203], v[82:85]
	v_mfma_f32_16x16x32_bf16 v[70:73], v[150:153], v[216:219], v[70:73]
	v_mfma_f32_16x16x32_bf16 v[66:69], v[170:173], v[216:219], v[66:69]
	s_barrier
	s_add_i32 s28, s50, s35
	v_lshl_add_u64 v[178:179], v[178:179], 0, s[56:57]
	s_mov_b32 m0, s28
	ds_read_b128 v[174:177], v183 offset:49152
	ds_read_b128 v[184:187], v183 offset:50176
	ds_read_b128 v[188:191], v183 offset:51200
	ds_read_b128 v[192:195], v183 offset:52224
	ds_read_b128 v[196:199], v183 offset:53248
	ds_read_b128 v[200:203], v183 offset:54272
	ds_read_b128 v[204:207], v183 offset:55296
	ds_read_b128 v[216:219], v183 offset:56320
	global_load_lds_dwordx4 v[178:179], off
	s_add_i32 m0, s28, 0x2000
	s_add_u32 s26, s26, 0x40080
	v_lshl_add_u64 v[178:179], v[208:209], 0, s[56:57]
	s_addc_u32 s27, s27, 0
	s_add_i32 s28, s52, s35
	global_load_lds_dwordx4 v[178:179], off
	s_mov_b32 m0, s28
	v_lshl_add_u64 v[178:179], s[26:27], 0, v[162:163]
	global_load_lds_dwordx4 v[178:179], off
	s_add_i32 m0, s28, 0x2000
	v_lshl_add_u64 v[178:179], s[26:27], 0, v[158:159]
	global_load_lds_dwordx4 v[178:179], off
	s_mov_b32 m0, s44
	v_lshl_add_u64 v[178:179], v[220:221], 0, s[56:57]
	global_load_lds_dwordx4 v[178:179], off
	s_mov_b32 m0, s45
	v_lshl_add_u64 v[178:179], v[222:223], 0, s[56:57]
	global_load_lds_dwordx4 v[178:179], off
	s_waitcnt vmcnt(8)
	s_waitcnt lgkmcnt(0)
	s_barrier
	s_waitcnt lgkmcnt(0)
	v_mfma_f32_16x16x32_bf16 v[62:65], v[130:133], v[174:177], v[62:65]
	v_mfma_f32_16x16x32_bf16 v[58:61], v[138:141], v[174:177], v[58:61]
	v_mfma_f32_16x16x32_bf16 v[46:49], v[130:133], v[188:191], v[46:49]
	v_mfma_f32_16x16x32_bf16 v[42:45], v[138:141], v[188:191], v[42:45]
	v_mfma_f32_16x16x32_bf16 v[30:33], v[130:133], v[196:199], v[30:33]
	v_mfma_f32_16x16x32_bf16 v[26:29], v[138:141], v[196:199], v[26:29]
	v_mfma_f32_16x16x32_bf16 v[14:17], v[130:133], v[204:207], v[14:17]
	v_mfma_f32_16x16x32_bf16 v[10:13], v[138:141], v[204:207], v[10:13]
	v_mfma_f32_16x16x32_bf16 v[62:65], v[134:137], v[184:187], v[62:65]
	v_mfma_f32_16x16x32_bf16 v[58:61], v[142:145], v[184:187], v[58:61]
	v_mfma_f32_16x16x32_bf16 v[46:49], v[134:137], v[192:195], v[46:49]
	v_mfma_f32_16x16x32_bf16 v[42:45], v[142:145], v[192:195], v[42:45]
	v_mfma_f32_16x16x32_bf16 v[30:33], v[134:137], v[200:203], v[30:33]
	v_mfma_f32_16x16x32_bf16 v[26:29], v[142:145], v[200:203], v[26:29]
	v_mfma_f32_16x16x32_bf16 v[14:17], v[134:137], v[216:219], v[14:17]
	v_mfma_f32_16x16x32_bf16 v[10:13], v[142:145], v[216:219], v[10:13]
	v_mfma_f32_16x16x32_bf16 v[54:57], v[146:149], v[174:177], v[54:57]
	v_mfma_f32_16x16x32_bf16 v[50:53], v[154:157], v[174:177], v[50:53]
	v_mfma_f32_16x16x32_bf16 v[38:41], v[146:149], v[188:191], v[38:41]
	v_mfma_f32_16x16x32_bf16 v[34:37], v[154:157], v[188:191], v[34:37]
	v_mfma_f32_16x16x32_bf16 v[22:25], v[146:149], v[196:199], v[22:25]
	v_mfma_f32_16x16x32_bf16 v[18:21], v[154:157], v[196:199], v[18:21]
	v_mfma_f32_16x16x32_bf16 v[6:9], v[146:149], v[204:207], v[6:9]
	v_mfma_f32_16x16x32_bf16 v[2:5], v[154:157], v[204:207], v[2:5]
	v_mfma_f32_16x16x32_bf16 v[54:57], v[150:153], v[184:187], v[54:57]
	v_mfma_f32_16x16x32_bf16 v[50:53], v[170:173], v[184:187], v[50:53]
	v_mfma_f32_16x16x32_bf16 v[38:41], v[150:153], v[192:195], v[38:41]
	v_mfma_f32_16x16x32_bf16 v[34:37], v[170:173], v[192:195], v[34:37]
	v_mfma_f32_16x16x32_bf16 v[22:25], v[150:153], v[200:203], v[22:25]
	v_mfma_f32_16x16x32_bf16 v[18:21], v[170:173], v[200:203], v[18:21]
	v_mfma_f32_16x16x32_bf16 v[6:9], v[150:153], v[216:219], v[6:9]
	v_mfma_f32_16x16x32_bf16 v[2:5], v[170:173], v[216:219], v[2:5]
	s_barrier
	s_add_i32 s49, s49, 2
	s_add_u32 s41, s41, 0x100
	s_addc_u32 s48, s48, 0
	s_add_u32 s6, s6, 0x100
	s_addc_u32 s7, s7, 0
	s_cmp_gt_u32 s49, 13
	s_cbranch_scc0 .LBB0_2626
	s_and_b64 vcc, exec, s[16:17]
	s_cbranch_vccz .LBB0_2629
	s_barrier

.LBB0_2703:
	s_add_u32 s44, s24, s36
	s_addc_u32 s45, s25, s37
	s_add_u32 s44, s44, 0x100
	s_addc_u32 s45, s45, 0
	s_add_u32 s50, s59, s36
	s_addc_u32 s64, s82, s37
	s_add_i32 s65, 0, 0x10000
	s_cmpk_eq_i32 s36, 0x1f00
	s_cselect_b32 s47, s29, s45
	s_cselect_b32 s46, s83, s44
	s_cselect_b32 s45, s27, s64
	s_cselect_b32 s44, s84, s50
	s_add_i32 s50, 0, 0x14000
	v_add_u32_e32 v160, s65, v146
	v_add_u32_e32 v164, s50, v146
	ds_read_b128 v[148:151], v160
	ds_read_b128 v[152:155], v160 offset:1024
	ds_read_b128 v[156:159], v160 offset:2048
	ds_read_b128 v[160:163], v160 offset:3072
	ds_read_b128 v[168:171], v164
	ds_read_b128 v[172:175], v164 offset:1024
	ds_read_b128 v[176:179], v164 offset:2048
	ds_read_b128 v[180:183], v164 offset:3072
	v_lshl_add_u64 v[164:165], v[144:145], 0, s[36:37]
	s_add_i32 m0, s4, 0xc000
	ds_read_b128 v[184:187], v147
	ds_read_b128 v[188:191], v147 offset:1024
	ds_read_b128 v[192:195], v147 offset:2048
	ds_read_b128 v[196:199], v147 offset:3072
	ds_read_b128 v[200:203], v147 offset:4096
	ds_read_b128 v[204:207], v147 offset:5120
	ds_read_b128 v[216:219], v147 offset:6144
	ds_read_b128 v[220:223], v147 offset:7168
	global_load_lds_dwordx4 v[164:165], off
	s_add_i32 m0, s4, 0xe000
	v_lshl_add_u64 v[164:165], v[142:143], 0, s[36:37]
	global_load_lds_dwordx4 v[164:165], off
	s_waitcnt vmcnt(8)
	s_waitcnt lgkmcnt(0)
	s_barrier
	s_waitcnt lgkmcnt(0)
	v_mfma_f32_16x16x32_bf16 v[134:137], v[148:151], v[184:187], v[134:137]
	v_mfma_f32_16x16x32_bf16 v[130:133], v[156:159], v[184:187], v[130:133]
	v_mfma_f32_16x16x32_bf16 v[110:113], v[148:151], v[192:195], v[110:113]
	v_mfma_f32_16x16x32_bf16 v[106:109], v[156:159], v[192:195], v[106:109]
	v_mfma_f32_16x16x32_bf16 v[94:97], v[148:151], v[200:203], v[94:97]
	v_mfma_f32_16x16x32_bf16 v[90:93], v[156:159], v[200:203], v[90:93]
	v_mfma_f32_16x16x32_bf16 v[78:81], v[148:151], v[216:219], v[78:81]
	v_mfma_f32_16x16x32_bf16 v[74:77], v[156:159], v[216:219], v[74:77]
	v_mfma_f32_16x16x32_bf16 v[134:137], v[152:155], v[188:191], v[134:137]
	v_mfma_f32_16x16x32_bf16 v[130:133], v[160:163], v[188:191], v[130:133]
	v_mfma_f32_16x16x32_bf16 v[110:113], v[152:155], v[196:199], v[110:113]
	v_mfma_f32_16x16x32_bf16 v[106:109], v[160:163], v[196:199], v[106:109]
	v_mfma_f32_16x16x32_bf16 v[94:97], v[152:155], v[204:207], v[94:97]
	v_mfma_f32_16x16x32_bf16 v[90:93], v[160:163], v[204:207], v[90:93]
	v_mfma_f32_16x16x32_bf16 v[78:81], v[152:155], v[220:223], v[78:81]
	v_mfma_f32_16x16x32_bf16 v[74:77], v[160:163], v[220:223], v[74:77]
	v_mfma_f32_16x16x32_bf16 v[122:125], v[168:171], v[184:187], v[122:125]
	v_mfma_f32_16x16x32_bf16 v[114:117], v[176:179], v[184:187], v[114:117]
	v_mfma_f32_16x16x32_bf16 v[102:105], v[168:171], v[192:195], v[102:105]
	v_mfma_f32_16x16x32_bf16 v[98:101], v[176:179], v[192:195], v[98:101]
	v_mfma_f32_16x16x32_bf16 v[86:89], v[168:171], v[200:203], v[86:89]
	v_mfma_f32_16x16x32_bf16 v[82:85], v[176:179], v[200:203], v[82:85]
	v_mfma_f32_16x16x32_bf16 v[70:73], v[168:171], v[216:219], v[70:73]
	v_mfma_f32_16x16x32_bf16 v[66:69], v[176:179], v[216:219], v[66:69]
	v_mfma_f32_16x16x32_bf16 v[122:125], v[172:175], v[188:191], v[122:125]
	v_mfma_f32_16x16x32_bf16 v[114:117], v[180:183], v[188:191], v[114:117]
	v_mfma_f32_16x16x32_bf16 v[102:105], v[172:175], v[196:199], v[102:105]
	v_mfma_f32_16x16x32_bf16 v[98:101], v[180:183], v[196:199], v[98:101]
	v_mfma_f32_16x16x32_bf16 v[86:89], v[172:175], v[204:207], v[86:89]
	v_mfma_f32_16x16x32_bf16 v[82:85], v[180:183], v[204:207], v[82:85]
	v_mfma_f32_16x16x32_bf16 v[70:73], v[172:175], v[220:223], v[70:73]
	v_mfma_f32_16x16x32_bf16 v[66:69], v[180:183], v[220:223], v[66:69]
	s_barrier
	s_add_i32 s64, s65, s77
	v_lshl_add_u64 v[164:165], s[44:45], 0, v[126:127]
	s_mov_b32 m0, s64
	ds_read_b128 v[184:187], v147 offset:16384
	ds_read_b128 v[188:191], v147 offset:17408
	ds_read_b128 v[192:195], v147 offset:18432
	ds_read_b128 v[196:199], v147 offset:19456
	ds_read_b128 v[200:203], v147 offset:20480
	ds_read_b128 v[204:207], v147 offset:21504
	ds_read_b128 v[216:219], v147 offset:22528
	ds_read_b128 v[220:223], v147 offset:23552
	global_load_lds_dwordx4 v[164:165], off
	s_add_i32 m0, s64, 0x2000
	s_add_u32 s92, s44, 0x100000
	v_lshl_add_u64 v[208:209], s[44:45], 0, v[118:119]
	s_addc_u32 s93, s45, 0
	s_add_i32 s50, s50, s77
	global_load_lds_dwordx4 v[208:209], off
	v_lshl_add_u64 v[224:225], s[92:93], 0, v[126:127]
	s_mov_b32 m0, s50
	v_lshl_add_u64 v[242:243], s[46:47], 0, v[120:121]
	global_load_lds_dwordx4 v[224:225], off
	s_add_i32 m0, s50, 0x2000
	v_lshl_add_u64 v[224:225], s[92:93], 0, v[118:119]
	global_load_lds_dwordx4 v[224:225], off
	s_mov_b32 m0, s4
	v_lshl_add_u64 v[224:225], s[46:47], 0, v[128:129]
	global_load_lds_dwordx4 v[224:225], off
	s_mov_b32 m0, s33
	s_nop 0
	global_load_lds_dwordx4 v[242:243], off
	s_waitcnt vmcnt(8)
	s_waitcnt lgkmcnt(0)
	s_barrier
	s_waitcnt lgkmcnt(0)
	v_mfma_f32_16x16x32_bf16 v[62:65], v[148:151], v[184:187], v[62:65]
	v_mfma_f32_16x16x32_bf16 v[58:61], v[156:159], v[184:187], v[58:61]
	v_mfma_f32_16x16x32_bf16 v[46:49], v[148:151], v[192:195], v[46:49]
	v_mfma_f32_16x16x32_bf16 v[42:45], v[156:159], v[192:195], v[42:45]
	v_mfma_f32_16x16x32_bf16 v[30:33], v[148:151], v[200:203], v[30:33]
	v_mfma_f32_16x16x32_bf16 v[26:29], v[156:159], v[200:203], v[26:29]
	v_mfma_f32_16x16x32_bf16 v[14:17], v[148:151], v[216:219], v[14:17]
	v_mfma_f32_16x16x32_bf16 v[10:13], v[156:159], v[216:219], v[10:13]
	v_mfma_f32_16x16x32_bf16 v[62:65], v[152:155], v[188:191], v[62:65]
	v_mfma_f32_16x16x32_bf16 v[58:61], v[160:163], v[188:191], v[58:61]
	v_mfma_f32_16x16x32_bf16 v[46:49], v[152:155], v[196:199], v[46:49]
	v_mfma_f32_16x16x32_bf16 v[42:45], v[160:163], v[196:199], v[42:45]
	v_mfma_f32_16x16x32_bf16 v[30:33], v[152:155], v[204:207], v[30:33]
	v_mfma_f32_16x16x32_bf16 v[26:29], v[160:163], v[204:207], v[26:29]
	v_mfma_f32_16x16x32_bf16 v[14:17], v[152:155], v[220:223], v[14:17]
	v_mfma_f32_16x16x32_bf16 v[10:13], v[160:163], v[220:223], v[10:13]
	v_mfma_f32_16x16x32_bf16 v[54:57], v[168:171], v[184:187], v[54:57]
	v_mfma_f32_16x16x32_bf16 v[50:53], v[176:179], v[184:187], v[50:53]
	v_mfma_f32_16x16x32_bf16 v[38:41], v[168:171], v[192:195], v[38:41]
	v_mfma_f32_16x16x32_bf16 v[34:37], v[176:179], v[192:195], v[34:37]
	v_mfma_f32_16x16x32_bf16 v[22:25], v[168:171], v[200:203], v[22:25]
	v_mfma_f32_16x16x32_bf16 v[18:21], v[176:179], v[200:203], v[18:21]
	v_mfma_f32_16x16x32_bf16 v[6:9], v[168:171], v[216:219], v[6:9]
	v_mfma_f32_16x16x32_bf16 v[2:5], v[176:179], v[216:219], v[2:5]
	v_mfma_f32_16x16x32_bf16 v[54:57], v[172:175], v[188:191], v[54:57]
	v_mfma_f32_16x16x32_bf16 v[50:53], v[180:183], v[188:191], v[50:53]
	v_mfma_f32_16x16x32_bf16 v[38:41], v[172:175], v[196:199], v[38:41]
	v_mfma_f32_16x16x32_bf16 v[34:37], v[180:183], v[196:199], v[34:37]
	v_mfma_f32_16x16x32_bf16 v[22:25], v[172:175], v[204:207], v[22:25]
	v_mfma_f32_16x16x32_bf16 v[18:21], v[180:183], v[204:207], v[18:21]
	v_mfma_f32_16x16x32_bf16 v[6:9], v[172:175], v[220:223], v[6:9]
	v_mfma_f32_16x16x32_bf16 v[2:5], v[180:183], v[220:223], v[2:5]
	s_barrier
	s_add_i32 s50, 0, 0x18000
	s_add_i32 s64, 0, 0x1c000
	v_add_u32_e32 v160, s50, v146
	v_add_u32_e32 v167, s64, v146
	ds_read_b128 v[148:151], v160
	ds_read_b128 v[152:155], v160 offset:1024
	ds_read_b128 v[156:159], v160 offset:2048
	ds_read_b128 v[160:163], v160 offset:3072
	ds_read_b128 v[168:171], v167
	ds_read_b128 v[172:175], v167 offset:1024
	ds_read_b128 v[176:179], v167 offset:2048
	ds_read_b128 v[180:183], v167 offset:3072
	s_add_u32 s46, s46, 0x100000
	s_addc_u32 s47, s47, 0
	s_mov_b32 m0, s78
	v_lshl_add_u64 v[244:245], s[46:47], 0, v[128:129]
	ds_read_b128 v[184:187], v147 offset:32768
	ds_read_b128 v[188:191], v147 offset:33792
	ds_read_b128 v[192:195], v147 offset:34816
	ds_read_b128 v[196:199], v147 offset:35840
	ds_read_b128 v[200:203], v147 offset:36864
	ds_read_b128 v[204:207], v147 offset:37888
	ds_read_b128 v[216:219], v147 offset:38912
	ds_read_b128 v[220:223], v147 offset:39936
	global_load_lds_dwordx4 v[244:245], off
	s_mov_b32 m0, s79
	v_lshl_add_u64 v[244:245], s[46:47], 0, v[120:121]
	global_load_lds_dwordx4 v[244:245], off
	s_waitcnt vmcnt(8)
	s_waitcnt lgkmcnt(0)
	s_barrier
	s_waitcnt lgkmcnt(0)
	v_mfma_f32_16x16x32_bf16 v[134:137], v[148:151], v[184:187], v[134:137]
	v_mfma_f32_16x16x32_bf16 v[130:133], v[156:159], v[184:187], v[130:133]
	v_mfma_f32_16x16x32_bf16 v[110:113], v[148:151], v[192:195], v[110:113]
	v_mfma_f32_16x16x32_bf16 v[106:109], v[156:159], v[192:195], v[106:109]
	v_mfma_f32_16x16x32_bf16 v[94:97], v[148:151], v[200:203], v[94:97]
	v_mfma_f32_16x16x32_bf16 v[90:93], v[156:159], v[200:203], v[90:93]
	v_mfma_f32_16x16x32_bf16 v[78:81], v[148:151], v[216:219], v[78:81]
	v_mfma_f32_16x16x32_bf16 v[74:77], v[156:159], v[216:219], v[74:77]
	v_mfma_f32_16x16x32_bf16 v[134:137], v[152:155], v[188:191], v[134:137]
	v_mfma_f32_16x16x32_bf16 v[130:133], v[160:163], v[188:191], v[130:133]
	v_mfma_f32_16x16x32_bf16 v[110:113], v[152:155], v[196:199], v[110:113]
	v_mfma_f32_16x16x32_bf16 v[106:109], v[160:163], v[196:199], v[106:109]
	v_mfma_f32_16x16x32_bf16 v[94:97], v[152:155], v[204:207], v[94:97]
	v_mfma_f32_16x16x32_bf16 v[90:93], v[160:163], v[204:207], v[90:93]
	v_mfma_f32_16x16x32_bf16 v[78:81], v[152:155], v[220:223], v[78:81]
	v_mfma_f32_16x16x32_bf16 v[74:77], v[160:163], v[220:223], v[74:77]
	v_mfma_f32_16x16x32_bf16 v[122:125], v[168:171], v[184:187], v[122:125]
	v_mfma_f32_16x16x32_bf16 v[114:117], v[176:179], v[184:187], v[114:117]
	v_mfma_f32_16x16x32_bf16 v[102:105], v[168:171], v[192:195], v[102:105]
	v_mfma_f32_16x16x32_bf16 v[98:101], v[176:179], v[192:195], v[98:101]
	v_mfma_f32_16x16x32_bf16 v[86:89], v[168:171], v[200:203], v[86:89]
	v_mfma_f32_16x16x32_bf16 v[82:85], v[176:179], v[200:203], v[82:85]
	v_mfma_f32_16x16x32_bf16 v[70:73], v[168:171], v[216:219], v[70:73]
	v_mfma_f32_16x16x32_bf16 v[66:69], v[176:179], v[216:219], v[66:69]
	v_mfma_f32_16x16x32_bf16 v[122:125], v[172:175], v[188:191], v[122:125]
	v_mfma_f32_16x16x32_bf16 v[114:117], v[180:183], v[188:191], v[114:117]
	v_mfma_f32_16x16x32_bf16 v[102:105], v[172:175], v[196:199], v[102:105]
	v_mfma_f32_16x16x32_bf16 v[98:101], v[180:183], v[196:199], v[98:101]
	v_mfma_f32_16x16x32_bf16 v[86:89], v[172:175], v[204:207], v[86:89]
	v_mfma_f32_16x16x32_bf16 v[82:85], v[180:183], v[204:207], v[82:85]
	v_mfma_f32_16x16x32_bf16 v[70:73], v[172:175], v[220:223], v[70:73]
	v_mfma_f32_16x16x32_bf16 v[66:69], v[180:183], v[220:223], v[66:69]
	s_barrier
	s_add_i32 s46, s50, s77
	v_lshl_add_u64 v[164:165], v[164:165], 0, s[56:57]
	s_mov_b32 m0, s46
	ds_read_b128 v[184:187], v147 offset:49152
	ds_read_b128 v[188:191], v147 offset:50176
	ds_read_b128 v[192:195], v147 offset:51200
	ds_read_b128 v[196:199], v147 offset:52224
	ds_read_b128 v[200:203], v147 offset:53248
	ds_read_b128 v[204:207], v147 offset:54272
	ds_read_b128 v[216:219], v147 offset:55296
	ds_read_b128 v[220:223], v147 offset:56320
	global_load_lds_dwordx4 v[164:165], off
	s_add_i32 m0, s46, 0x2000
	s_add_u32 s44, s44, 0x100080
	v_lshl_add_u64 v[164:165], v[208:209], 0, s[56:57]
	s_addc_u32 s45, s45, 0
	s_add_i32 s46, s64, s77
	global_load_lds_dwordx4 v[164:165], off
	s_mov_b32 m0, s46
	v_lshl_add_u64 v[164:165], s[44:45], 0, v[126:127]
	global_load_lds_dwordx4 v[164:165], off
	s_add_i32 m0, s46, 0x2000
	v_lshl_add_u64 v[164:165], s[44:45], 0, v[118:119]
	global_load_lds_dwordx4 v[164:165], off
	s_mov_b32 m0, s80
	v_lshl_add_u64 v[164:165], v[224:225], 0, s[56:57]
	global_load_lds_dwordx4 v[164:165], off
	s_mov_b32 m0, s81
	v_lshl_add_u64 v[164:165], v[242:243], 0, s[56:57]
	global_load_lds_dwordx4 v[164:165], off
	s_waitcnt vmcnt(8)
	s_waitcnt lgkmcnt(0)
	s_barrier
	s_waitcnt lgkmcnt(0)
	v_mfma_f32_16x16x32_bf16 v[62:65], v[148:151], v[184:187], v[62:65]
	v_mfma_f32_16x16x32_bf16 v[58:61], v[156:159], v[184:187], v[58:61]
	v_mfma_f32_16x16x32_bf16 v[46:49], v[148:151], v[192:195], v[46:49]
	v_mfma_f32_16x16x32_bf16 v[42:45], v[156:159], v[192:195], v[42:45]
	v_mfma_f32_16x16x32_bf16 v[30:33], v[148:151], v[200:203], v[30:33]
	v_mfma_f32_16x16x32_bf16 v[26:29], v[156:159], v[200:203], v[26:29]
	v_mfma_f32_16x16x32_bf16 v[14:17], v[148:151], v[216:219], v[14:17]
	v_mfma_f32_16x16x32_bf16 v[10:13], v[156:159], v[216:219], v[10:13]
	v_mfma_f32_16x16x32_bf16 v[62:65], v[152:155], v[188:191], v[62:65]
	v_mfma_f32_16x16x32_bf16 v[58:61], v[160:163], v[188:191], v[58:61]
	v_mfma_f32_16x16x32_bf16 v[46:49], v[152:155], v[196:199], v[46:49]
	v_mfma_f32_16x16x32_bf16 v[42:45], v[160:163], v[196:199], v[42:45]
	v_mfma_f32_16x16x32_bf16 v[30:33], v[152:155], v[204:207], v[30:33]
	v_mfma_f32_16x16x32_bf16 v[26:29], v[160:163], v[204:207], v[26:29]
	v_mfma_f32_16x16x32_bf16 v[14:17], v[152:155], v[220:223], v[14:17]
	v_mfma_f32_16x16x32_bf16 v[10:13], v[160:163], v[220:223], v[10:13]
	v_mfma_f32_16x16x32_bf16 v[54:57], v[168:171], v[184:187], v[54:57]
	v_mfma_f32_16x16x32_bf16 v[50:53], v[176:179], v[184:187], v[50:53]
	v_mfma_f32_16x16x32_bf16 v[38:41], v[168:171], v[192:195], v[38:41]
	v_mfma_f32_16x16x32_bf16 v[34:37], v[176:179], v[192:195], v[34:37]
	v_mfma_f32_16x16x32_bf16 v[22:25], v[168:171], v[200:203], v[22:25]
	v_mfma_f32_16x16x32_bf16 v[18:21], v[176:179], v[200:203], v[18:21]
	v_mfma_f32_16x16x32_bf16 v[6:9], v[168:171], v[216:219], v[6:9]
	v_mfma_f32_16x16x32_bf16 v[2:5], v[176:179], v[216:219], v[2:5]
	v_mfma_f32_16x16x32_bf16 v[54:57], v[172:175], v[188:191], v[54:57]
	v_mfma_f32_16x16x32_bf16 v[50:53], v[180:183], v[188:191], v[50:53]
	v_mfma_f32_16x16x32_bf16 v[38:41], v[172:175], v[196:199], v[38:41]
	v_mfma_f32_16x16x32_bf16 v[34:37], v[180:183], v[196:199], v[34:37]
	v_mfma_f32_16x16x32_bf16 v[22:25], v[172:175], v[204:207], v[22:25]
	v_mfma_f32_16x16x32_bf16 v[18:21], v[180:183], v[204:207], v[18:21]
	v_mfma_f32_16x16x32_bf16 v[6:9], v[172:175], v[220:223], v[6:9]
	v_mfma_f32_16x16x32_bf16 v[2:5], v[180:183], v[220:223], v[2:5]
	s_barrier
	s_add_i32 s85, s85, 2
	s_add_u32 s36, s36, 0x100
	s_addc_u32 s37, s37, 0
	s_cmp_gt_u32 s85, 61
	s_cbranch_scc0 .LBB0_2703
	s_add_u32 s36, s59, 0xffffff00
	s_addc_u32 s37, s82, -1
	s_andn2_b64 vcc, exec, s[42:43]
	s_cbranch_vccnz .LBB0_2706
	v_mov_b32_e32 v2, 0
	s_mov_b32 s12, s26
	s_mov_b32 s53, s28
	s_mov_b64 s[24:25], s[34:35]
	s_mov_b32 s68, s58
	v_mov_b32_e32 v3, v2
	v_mov_b32_e32 v4, v2
	v_mov_b32_e32 v5, v2
	v_mov_b32_e32 v6, v2
	v_mov_b32_e32 v7, v2
	v_mov_b32_e32 v8, v2
	v_mov_b32_e32 v9, v2
	v_mov_b32_e32 v18, v2
	v_mov_b32_e32 v19, v2
	v_mov_b32_e32 v20, v2
	v_mov_b32_e32 v21, v2
	v_mov_b32_e32 v22, v2
	v_mov_b32_e32 v23, v2
	v_mov_b32_e32 v24, v2
	v_mov_b32_e32 v25, v2
	v_mov_b32_e32 v34, v2
	v_mov_b32_e32 v35, v2
	v_mov_b32_e32 v36, v2
	v_mov_b32_e32 v37, v2
	v_mov_b32_e32 v38, v2
	v_mov_b32_e32 v39, v2
	v_mov_b32_e32 v40, v2
	v_mov_b32_e32 v41, v2
	v_mov_b32_e32 v50, v2
	v_mov_b32_e32 v51, v2
	v_mov_b32_e32 v52, v2
	v_mov_b32_e32 v53, v2
	v_mov_b32_e32 v54, v2
	v_mov_b32_e32 v55, v2
	v_mov_b32_e32 v56, v2
	v_mov_b32_e32 v57, v2
	v_mov_b32_e32 v10, v2
	v_mov_b32_e32 v11, v2
	v_mov_b32_e32 v12, v2
	v_mov_b32_e32 v13, v2
	v_mov_b32_e32 v14, v2
	v_mov_b32_e32 v15, v2
	v_mov_b32_e32 v16, v2
	v_mov_b32_e32 v17, v2
	v_mov_b32_e32 v26, v2
	v_mov_b32_e32 v27, v2
	v_mov_b32_e32 v28, v2
	v_mov_b32_e32 v29, v2
	v_mov_b32_e32 v30, v2
	v_mov_b32_e32 v31, v2
	v_mov_b32_e32 v32, v2
	v_mov_b32_e32 v33, v2
	v_mov_b32_e32 v42, v2
	v_mov_b32_e32 v43, v2
	v_mov_b32_e32 v44, v2
	v_mov_b32_e32 v45, v2
	v_mov_b32_e32 v46, v2
	v_mov_b32_e32 v47, v2
	v_mov_b32_e32 v48, v2
	v_mov_b32_e32 v49, v2
	v_mov_b32_e32 v58, v2
	v_mov_b32_e32 v59, v2
	v_mov_b32_e32 v60, v2
	v_mov_b32_e32 v61, v2
	v_mov_b32_e32 v62, v2
	v_mov_b32_e32 v63, v2
	v_mov_b32_e32 v64, v2
	v_mov_b32_e32 v65, v2
	v_mov_b32_e32 v66, v2
	v_mov_b32_e32 v67, v2
	v_mov_b32_e32 v68, v2
	v_mov_b32_e32 v69, v2
	v_mov_b32_e32 v70, v2
	v_mov_b32_e32 v71, v2
	v_mov_b32_e32 v72, v2
	v_mov_b32_e32 v73, v2
	v_mov_b32_e32 v82, v2
	v_mov_b32_e32 v83, v2
	v_mov_b32_e32 v84, v2
	v_mov_b32_e32 v85, v2
	v_mov_b32_e32 v86, v2
	v_mov_b32_e32 v87, v2
	v_mov_b32_e32 v88, v2
	v_mov_b32_e32 v89, v2
	v_mov_b32_e32 v98, v2
	v_mov_b32_e32 v99, v2
	v_mov_b32_e32 v100, v2
	v_mov_b32_e32 v101, v2
	v_mov_b32_e32 v102, v2
	v_mov_b32_e32 v103, v2
	v_mov_b32_e32 v104, v2
	v_mov_b32_e32 v105, v2
	v_mov_b32_e32 v114, v2
	v_mov_b32_e32 v115, v2
	v_mov_b32_e32 v116, v2
	v_mov_b32_e32 v117, v2
	v_mov_b32_e32 v122, v2
	v_mov_b32_e32 v123, v2
	v_mov_b32_e32 v124, v2
	v_mov_b32_e32 v125, v2
	v_mov_b32_e32 v74, v2
	v_mov_b32_e32 v75, v2
	v_mov_b32_e32 v76, v2
	v_mov_b32_e32 v77, v2
	v_mov_b32_e32 v78, v2
	v_mov_b32_e32 v79, v2
	v_mov_b32_e32 v80, v2
	v_mov_b32_e32 v81, v2
	v_mov_b32_e32 v90, v2
	v_mov_b32_e32 v91, v2
	v_mov_b32_e32 v92, v2
	v_mov_b32_e32 v93, v2
	v_mov_b32_e32 v94, v2
	v_mov_b32_e32 v95, v2
	v_mov_b32_e32 v96, v2
	v_mov_b32_e32 v97, v2
	v_mov_b32_e32 v106, v2
	v_mov_b32_e32 v107, v2
	v_mov_b32_e32 v108, v2
	v_mov_b32_e32 v109, v2
	v_mov_b32_e32 v110, v2
	v_mov_b32_e32 v111, v2
	v_mov_b32_e32 v112, v2
	v_mov_b32_e32 v113, v2
	v_mov_b32_e32 v130, v2
	v_mov_b32_e32 v131, v2
	v_mov_b32_e32 v132, v2
	v_mov_b32_e32 v133, v2
	v_mov_b32_e32 v134, v2
	v_mov_b32_e32 v135, v2
	v_mov_b32_e32 v136, v2
	v_mov_b32_e32 v137, v2
	s_movk_i32 s92, 0x2b20
	s_andn2_b64 vcc, exec, s[40:41]
	s_cbranch_vccnz .LBB0_2707
	s_branch .LBB0_2708

.LBB0_2796:
	s_add_u32 s44, s24, s36
	s_addc_u32 s45, s25, s37
	s_add_u32 s44, s44, 0x100
	s_addc_u32 s45, s45, 0
	s_add_u32 s50, s59, s36
	s_addc_u32 s64, s81, s37
	s_add_i32 s65, 0, 0x10000
	s_cmpk_eq_i32 s36, 0x1f00
	s_cselect_b32 s47, s29, s45
	s_cselect_b32 s46, s82, s44
	s_cselect_b32 s45, s27, s64
	s_cselect_b32 s44, s83, s50
	s_add_i32 s50, 0, 0x14000
	v_add_u32_e32 v160, s65, v146
	v_add_u32_e32 v164, s50, v146
	ds_read_b128 v[148:151], v160
	ds_read_b128 v[152:155], v160 offset:1024
	ds_read_b128 v[156:159], v160 offset:2048
	ds_read_b128 v[160:163], v160 offset:3072
	ds_read_b128 v[168:171], v164
	ds_read_b128 v[172:175], v164 offset:1024
	ds_read_b128 v[176:179], v164 offset:2048
	ds_read_b128 v[180:183], v164 offset:3072
	v_lshl_add_u64 v[164:165], v[144:145], 0, s[36:37]
	s_add_i32 m0, s4, 0xc000
	ds_read_b128 v[184:187], v147
	ds_read_b128 v[188:191], v147 offset:1024
	ds_read_b128 v[192:195], v147 offset:2048
	ds_read_b128 v[196:199], v147 offset:3072
	ds_read_b128 v[200:203], v147 offset:4096
	ds_read_b128 v[204:207], v147 offset:5120
	ds_read_b128 v[216:219], v147 offset:6144
	ds_read_b128 v[220:223], v147 offset:7168
	global_load_lds_dwordx4 v[164:165], off
	s_add_i32 m0, s4, 0xe000
	v_lshl_add_u64 v[164:165], v[142:143], 0, s[36:37]
	global_load_lds_dwordx4 v[164:165], off
	s_waitcnt vmcnt(8)
	s_waitcnt lgkmcnt(0)
	s_barrier
	s_waitcnt lgkmcnt(0)
	v_mfma_f32_16x16x32_bf16 v[134:137], v[148:151], v[184:187], v[134:137]
	v_mfma_f32_16x16x32_bf16 v[130:133], v[156:159], v[184:187], v[130:133]
	v_mfma_f32_16x16x32_bf16 v[110:113], v[148:151], v[192:195], v[110:113]
	v_mfma_f32_16x16x32_bf16 v[106:109], v[156:159], v[192:195], v[106:109]
	v_mfma_f32_16x16x32_bf16 v[94:97], v[148:151], v[200:203], v[94:97]
	v_mfma_f32_16x16x32_bf16 v[90:93], v[156:159], v[200:203], v[90:93]
	v_mfma_f32_16x16x32_bf16 v[78:81], v[148:151], v[216:219], v[78:81]
	v_mfma_f32_16x16x32_bf16 v[74:77], v[156:159], v[216:219], v[74:77]
	v_mfma_f32_16x16x32_bf16 v[134:137], v[152:155], v[188:191], v[134:137]
	v_mfma_f32_16x16x32_bf16 v[130:133], v[160:163], v[188:191], v[130:133]
	v_mfma_f32_16x16x32_bf16 v[110:113], v[152:155], v[196:199], v[110:113]
	v_mfma_f32_16x16x32_bf16 v[106:109], v[160:163], v[196:199], v[106:109]
	v_mfma_f32_16x16x32_bf16 v[94:97], v[152:155], v[204:207], v[94:97]
	v_mfma_f32_16x16x32_bf16 v[90:93], v[160:163], v[204:207], v[90:93]
	v_mfma_f32_16x16x32_bf16 v[78:81], v[152:155], v[220:223], v[78:81]
	v_mfma_f32_16x16x32_bf16 v[74:77], v[160:163], v[220:223], v[74:77]
	v_mfma_f32_16x16x32_bf16 v[122:125], v[168:171], v[184:187], v[122:125]
	v_mfma_f32_16x16x32_bf16 v[114:117], v[176:179], v[184:187], v[114:117]
	v_mfma_f32_16x16x32_bf16 v[102:105], v[168:171], v[192:195], v[102:105]
	v_mfma_f32_16x16x32_bf16 v[98:101], v[176:179], v[192:195], v[98:101]
	v_mfma_f32_16x16x32_bf16 v[86:89], v[168:171], v[200:203], v[86:89]
	v_mfma_f32_16x16x32_bf16 v[82:85], v[176:179], v[200:203], v[82:85]
	v_mfma_f32_16x16x32_bf16 v[70:73], v[168:171], v[216:219], v[70:73]
	v_mfma_f32_16x16x32_bf16 v[66:69], v[176:179], v[216:219], v[66:69]
	v_mfma_f32_16x16x32_bf16 v[122:125], v[172:175], v[188:191], v[122:125]
	v_mfma_f32_16x16x32_bf16 v[114:117], v[180:183], v[188:191], v[114:117]
	v_mfma_f32_16x16x32_bf16 v[102:105], v[172:175], v[196:199], v[102:105]
	v_mfma_f32_16x16x32_bf16 v[98:101], v[180:183], v[196:199], v[98:101]
	v_mfma_f32_16x16x32_bf16 v[86:89], v[172:175], v[204:207], v[86:89]
	v_mfma_f32_16x16x32_bf16 v[82:85], v[180:183], v[204:207], v[82:85]
	v_mfma_f32_16x16x32_bf16 v[70:73], v[172:175], v[220:223], v[70:73]
	v_mfma_f32_16x16x32_bf16 v[66:69], v[180:183], v[220:223], v[66:69]
	s_barrier
	s_add_i32 s64, s65, s71
	v_lshl_add_u64 v[164:165], s[44:45], 0, v[126:127]
	s_mov_b32 m0, s64
	ds_read_b128 v[184:187], v147 offset:16384
	ds_read_b128 v[188:191], v147 offset:17408
	ds_read_b128 v[192:195], v147 offset:18432
	ds_read_b128 v[196:199], v147 offset:19456
	ds_read_b128 v[200:203], v147 offset:20480
	ds_read_b128 v[204:207], v147 offset:21504
	ds_read_b128 v[216:219], v147 offset:22528
	ds_read_b128 v[220:223], v147 offset:23552
	global_load_lds_dwordx4 v[164:165], off
	s_add_i32 m0, s64, 0x2000
	s_add_u32 s92, s44, 0x100000
	v_lshl_add_u64 v[208:209], s[44:45], 0, v[118:119]
	s_addc_u32 s93, s45, 0
	s_add_i32 s50, s50, s71
	global_load_lds_dwordx4 v[208:209], off
	v_lshl_add_u64 v[224:225], s[92:93], 0, v[126:127]
	s_mov_b32 m0, s50
	v_lshl_add_u64 v[242:243], s[46:47], 0, v[120:121]
	global_load_lds_dwordx4 v[224:225], off
	s_add_i32 m0, s50, 0x2000
	v_lshl_add_u64 v[224:225], s[92:93], 0, v[118:119]
	global_load_lds_dwordx4 v[224:225], off
	s_mov_b32 m0, s4
	v_lshl_add_u64 v[224:225], s[46:47], 0, v[128:129]
	global_load_lds_dwordx4 v[224:225], off
	s_mov_b32 m0, s33
	s_nop 0
	global_load_lds_dwordx4 v[242:243], off
	s_waitcnt vmcnt(8)
	s_waitcnt lgkmcnt(0)
	s_barrier
	s_waitcnt lgkmcnt(0)
	v_mfma_f32_16x16x32_bf16 v[62:65], v[148:151], v[184:187], v[62:65]
	v_mfma_f32_16x16x32_bf16 v[58:61], v[156:159], v[184:187], v[58:61]
	v_mfma_f32_16x16x32_bf16 v[46:49], v[148:151], v[192:195], v[46:49]
	v_mfma_f32_16x16x32_bf16 v[42:45], v[156:159], v[192:195], v[42:45]
	v_mfma_f32_16x16x32_bf16 v[30:33], v[148:151], v[200:203], v[30:33]
	v_mfma_f32_16x16x32_bf16 v[26:29], v[156:159], v[200:203], v[26:29]
	v_mfma_f32_16x16x32_bf16 v[14:17], v[148:151], v[216:219], v[14:17]
	v_mfma_f32_16x16x32_bf16 v[10:13], v[156:159], v[216:219], v[10:13]
	v_mfma_f32_16x16x32_bf16 v[62:65], v[152:155], v[188:191], v[62:65]
	v_mfma_f32_16x16x32_bf16 v[58:61], v[160:163], v[188:191], v[58:61]
	v_mfma_f32_16x16x32_bf16 v[46:49], v[152:155], v[196:199], v[46:49]
	v_mfma_f32_16x16x32_bf16 v[42:45], v[160:163], v[196:199], v[42:45]
	v_mfma_f32_16x16x32_bf16 v[30:33], v[152:155], v[204:207], v[30:33]
	v_mfma_f32_16x16x32_bf16 v[26:29], v[160:163], v[204:207], v[26:29]
	v_mfma_f32_16x16x32_bf16 v[14:17], v[152:155], v[220:223], v[14:17]
	v_mfma_f32_16x16x32_bf16 v[10:13], v[160:163], v[220:223], v[10:13]
	v_mfma_f32_16x16x32_bf16 v[54:57], v[168:171], v[184:187], v[54:57]
	v_mfma_f32_16x16x32_bf16 v[50:53], v[176:179], v[184:187], v[50:53]
	v_mfma_f32_16x16x32_bf16 v[38:41], v[168:171], v[192:195], v[38:41]
	v_mfma_f32_16x16x32_bf16 v[34:37], v[176:179], v[192:195], v[34:37]
	v_mfma_f32_16x16x32_bf16 v[22:25], v[168:171], v[200:203], v[22:25]
	v_mfma_f32_16x16x32_bf16 v[18:21], v[176:179], v[200:203], v[18:21]
	v_mfma_f32_16x16x32_bf16 v[6:9], v[168:171], v[216:219], v[6:9]
	v_mfma_f32_16x16x32_bf16 v[2:5], v[176:179], v[216:219], v[2:5]
	v_mfma_f32_16x16x32_bf16 v[54:57], v[172:175], v[188:191], v[54:57]
	v_mfma_f32_16x16x32_bf16 v[50:53], v[180:183], v[188:191], v[50:53]
	v_mfma_f32_16x16x32_bf16 v[38:41], v[172:175], v[196:199], v[38:41]
	v_mfma_f32_16x16x32_bf16 v[34:37], v[180:183], v[196:199], v[34:37]
	v_mfma_f32_16x16x32_bf16 v[22:25], v[172:175], v[204:207], v[22:25]
	v_mfma_f32_16x16x32_bf16 v[18:21], v[180:183], v[204:207], v[18:21]
	v_mfma_f32_16x16x32_bf16 v[6:9], v[172:175], v[220:223], v[6:9]
	v_mfma_f32_16x16x32_bf16 v[2:5], v[180:183], v[220:223], v[2:5]
	s_barrier
	s_add_i32 s50, 0, 0x18000
	s_add_i32 s64, 0, 0x1c000
	v_add_u32_e32 v160, s50, v146
	v_add_u32_e32 v167, s64, v146
	ds_read_b128 v[148:151], v160
	ds_read_b128 v[152:155], v160 offset:1024
	ds_read_b128 v[156:159], v160 offset:2048
	ds_read_b128 v[160:163], v160 offset:3072
	ds_read_b128 v[168:171], v167
	ds_read_b128 v[172:175], v167 offset:1024
	ds_read_b128 v[176:179], v167 offset:2048
	ds_read_b128 v[180:183], v167 offset:3072
	s_add_u32 s46, s46, 0x100000
	s_addc_u32 s47, s47, 0
	s_mov_b32 m0, s76
	v_lshl_add_u64 v[244:245], s[46:47], 0, v[128:129]
	ds_read_b128 v[184:187], v147 offset:32768
	ds_read_b128 v[188:191], v147 offset:33792
	ds_read_b128 v[192:195], v147 offset:34816
	ds_read_b128 v[196:199], v147 offset:35840
	ds_read_b128 v[200:203], v147 offset:36864
	ds_read_b128 v[204:207], v147 offset:37888
	ds_read_b128 v[216:219], v147 offset:38912
	ds_read_b128 v[220:223], v147 offset:39936
	global_load_lds_dwordx4 v[244:245], off
	s_mov_b32 m0, s77
	v_lshl_add_u64 v[244:245], s[46:47], 0, v[120:121]
	global_load_lds_dwordx4 v[244:245], off
	s_waitcnt vmcnt(8)
	s_waitcnt lgkmcnt(0)
	s_barrier
	s_waitcnt lgkmcnt(0)
	v_mfma_f32_16x16x32_bf16 v[134:137], v[148:151], v[184:187], v[134:137]
	v_mfma_f32_16x16x32_bf16 v[130:133], v[156:159], v[184:187], v[130:133]
	v_mfma_f32_16x16x32_bf16 v[110:113], v[148:151], v[192:195], v[110:113]
	v_mfma_f32_16x16x32_bf16 v[106:109], v[156:159], v[192:195], v[106:109]
	v_mfma_f32_16x16x32_bf16 v[94:97], v[148:151], v[200:203], v[94:97]
	v_mfma_f32_16x16x32_bf16 v[90:93], v[156:159], v[200:203], v[90:93]
	v_mfma_f32_16x16x32_bf16 v[78:81], v[148:151], v[216:219], v[78:81]
	v_mfma_f32_16x16x32_bf16 v[74:77], v[156:159], v[216:219], v[74:77]
	v_mfma_f32_16x16x32_bf16 v[134:137], v[152:155], v[188:191], v[134:137]
	v_mfma_f32_16x16x32_bf16 v[130:133], v[160:163], v[188:191], v[130:133]
	v_mfma_f32_16x16x32_bf16 v[110:113], v[152:155], v[196:199], v[110:113]
	v_mfma_f32_16x16x32_bf16 v[106:109], v[160:163], v[196:199], v[106:109]
	v_mfma_f32_16x16x32_bf16 v[94:97], v[152:155], v[204:207], v[94:97]
	v_mfma_f32_16x16x32_bf16 v[90:93], v[160:163], v[204:207], v[90:93]
	v_mfma_f32_16x16x32_bf16 v[78:81], v[152:155], v[220:223], v[78:81]
	v_mfma_f32_16x16x32_bf16 v[74:77], v[160:163], v[220:223], v[74:77]
	v_mfma_f32_16x16x32_bf16 v[122:125], v[168:171], v[184:187], v[122:125]
	v_mfma_f32_16x16x32_bf16 v[114:117], v[176:179], v[184:187], v[114:117]
	v_mfma_f32_16x16x32_bf16 v[102:105], v[168:171], v[192:195], v[102:105]
	v_mfma_f32_16x16x32_bf16 v[98:101], v[176:179], v[192:195], v[98:101]
	v_mfma_f32_16x16x32_bf16 v[86:89], v[168:171], v[200:203], v[86:89]
	v_mfma_f32_16x16x32_bf16 v[82:85], v[176:179], v[200:203], v[82:85]
	v_mfma_f32_16x16x32_bf16 v[70:73], v[168:171], v[216:219], v[70:73]
	v_mfma_f32_16x16x32_bf16 v[66:69], v[176:179], v[216:219], v[66:69]
	v_mfma_f32_16x16x32_bf16 v[122:125], v[172:175], v[188:191], v[122:125]
	v_mfma_f32_16x16x32_bf16 v[114:117], v[180:183], v[188:191], v[114:117]
	v_mfma_f32_16x16x32_bf16 v[102:105], v[172:175], v[196:199], v[102:105]
	v_mfma_f32_16x16x32_bf16 v[98:101], v[180:183], v[196:199], v[98:101]
	v_mfma_f32_16x16x32_bf16 v[86:89], v[172:175], v[204:207], v[86:89]
	v_mfma_f32_16x16x32_bf16 v[82:85], v[180:183], v[204:207], v[82:85]
	v_mfma_f32_16x16x32_bf16 v[70:73], v[172:175], v[220:223], v[70:73]
	v_mfma_f32_16x16x32_bf16 v[66:69], v[180:183], v[220:223], v[66:69]
	s_barrier
	s_add_i32 s46, s50, s71
	v_lshl_add_u64 v[164:165], v[164:165], 0, s[56:57]
	s_mov_b32 m0, s46
	ds_read_b128 v[184:187], v147 offset:49152
	ds_read_b128 v[188:191], v147 offset:50176
	ds_read_b128 v[192:195], v147 offset:51200
	ds_read_b128 v[196:199], v147 offset:52224
	ds_read_b128 v[200:203], v147 offset:53248
	ds_read_b128 v[204:207], v147 offset:54272
	ds_read_b128 v[216:219], v147 offset:55296
	ds_read_b128 v[220:223], v147 offset:56320
	global_load_lds_dwordx4 v[164:165], off
	s_add_i32 m0, s46, 0x2000
	s_add_u32 s44, s44, 0x100080
	v_lshl_add_u64 v[164:165], v[208:209], 0, s[56:57]
	s_addc_u32 s45, s45, 0
	s_add_i32 s46, s64, s71
	global_load_lds_dwordx4 v[164:165], off
	s_mov_b32 m0, s46
	v_lshl_add_u64 v[164:165], s[44:45], 0, v[126:127]
	global_load_lds_dwordx4 v[164:165], off
	s_add_i32 m0, s46, 0x2000
	v_lshl_add_u64 v[164:165], s[44:45], 0, v[118:119]
	global_load_lds_dwordx4 v[164:165], off
	s_mov_b32 m0, s78
	v_lshl_add_u64 v[164:165], v[224:225], 0, s[56:57]
	global_load_lds_dwordx4 v[164:165], off
	s_mov_b32 m0, s79
	v_lshl_add_u64 v[164:165], v[242:243], 0, s[56:57]
	global_load_lds_dwordx4 v[164:165], off
	s_waitcnt vmcnt(8)
	s_waitcnt lgkmcnt(0)
	s_barrier
	s_waitcnt lgkmcnt(0)
	v_mfma_f32_16x16x32_bf16 v[62:65], v[148:151], v[184:187], v[62:65]
	v_mfma_f32_16x16x32_bf16 v[58:61], v[156:159], v[184:187], v[58:61]
	v_mfma_f32_16x16x32_bf16 v[46:49], v[148:151], v[192:195], v[46:49]
	v_mfma_f32_16x16x32_bf16 v[42:45], v[156:159], v[192:195], v[42:45]
	v_mfma_f32_16x16x32_bf16 v[30:33], v[148:151], v[200:203], v[30:33]
	v_mfma_f32_16x16x32_bf16 v[26:29], v[156:159], v[200:203], v[26:29]
	v_mfma_f32_16x16x32_bf16 v[14:17], v[148:151], v[216:219], v[14:17]
	v_mfma_f32_16x16x32_bf16 v[10:13], v[156:159], v[216:219], v[10:13]
	v_mfma_f32_16x16x32_bf16 v[62:65], v[152:155], v[188:191], v[62:65]
	v_mfma_f32_16x16x32_bf16 v[58:61], v[160:163], v[188:191], v[58:61]
	v_mfma_f32_16x16x32_bf16 v[46:49], v[152:155], v[196:199], v[46:49]
	v_mfma_f32_16x16x32_bf16 v[42:45], v[160:163], v[196:199], v[42:45]
	v_mfma_f32_16x16x32_bf16 v[30:33], v[152:155], v[204:207], v[30:33]
	v_mfma_f32_16x16x32_bf16 v[26:29], v[160:163], v[204:207], v[26:29]
	v_mfma_f32_16x16x32_bf16 v[14:17], v[152:155], v[220:223], v[14:17]
	v_mfma_f32_16x16x32_bf16 v[10:13], v[160:163], v[220:223], v[10:13]
	v_mfma_f32_16x16x32_bf16 v[54:57], v[168:171], v[184:187], v[54:57]
	v_mfma_f32_16x16x32_bf16 v[50:53], v[176:179], v[184:187], v[50:53]
	v_mfma_f32_16x16x32_bf16 v[38:41], v[168:171], v[192:195], v[38:41]
	v_mfma_f32_16x16x32_bf16 v[34:37], v[176:179], v[192:195], v[34:37]
	v_mfma_f32_16x16x32_bf16 v[22:25], v[168:171], v[200:203], v[22:25]
	v_mfma_f32_16x16x32_bf16 v[18:21], v[176:179], v[200:203], v[18:21]
	v_mfma_f32_16x16x32_bf16 v[6:9], v[168:171], v[216:219], v[6:9]
	v_mfma_f32_16x16x32_bf16 v[2:5], v[176:179], v[216:219], v[2:5]
	v_mfma_f32_16x16x32_bf16 v[54:57], v[172:175], v[188:191], v[54:57]
	v_mfma_f32_16x16x32_bf16 v[50:53], v[180:183], v[188:191], v[50:53]
	v_mfma_f32_16x16x32_bf16 v[38:41], v[172:175], v[196:199], v[38:41]
	v_mfma_f32_16x16x32_bf16 v[34:37], v[180:183], v[196:199], v[34:37]
	v_mfma_f32_16x16x32_bf16 v[22:25], v[172:175], v[204:207], v[22:25]
	v_mfma_f32_16x16x32_bf16 v[18:21], v[180:183], v[204:207], v[18:21]
	v_mfma_f32_16x16x32_bf16 v[6:9], v[172:175], v[220:223], v[6:9]
	v_mfma_f32_16x16x32_bf16 v[2:5], v[180:183], v[220:223], v[2:5]
	s_barrier
	s_add_i32 s84, s84, 2
	s_add_u32 s36, s36, 0x100
	s_addc_u32 s37, s37, 0
	s_cmp_gt_u32 s84, 61
	s_cbranch_scc0 .LBB0_2796
	s_add_u32 s36, s59, 0xffffff00
	s_addc_u32 s37, s81, -1
	s_andn2_b64 vcc, exec, s[42:43]
	s_cbranch_vccnz .LBB0_2799
	v_mov_b32_e32 v2, 0
	s_mov_b32 s12, s26
	s_mov_b32 s80, s28
	s_mov_b64 s[24:25], s[34:35]
	s_mov_b32 s68, s58
	v_mov_b32_e32 v3, v2
	v_mov_b32_e32 v4, v2
	v_mov_b32_e32 v5, v2
	v_mov_b32_e32 v6, v2
	v_mov_b32_e32 v7, v2
	v_mov_b32_e32 v8, v2
	v_mov_b32_e32 v9, v2
	v_mov_b32_e32 v18, v2
	v_mov_b32_e32 v19, v2
	v_mov_b32_e32 v20, v2
	v_mov_b32_e32 v21, v2
	v_mov_b32_e32 v22, v2
	v_mov_b32_e32 v23, v2
	v_mov_b32_e32 v24, v2
	v_mov_b32_e32 v25, v2
	v_mov_b32_e32 v34, v2
	v_mov_b32_e32 v35, v2
	v_mov_b32_e32 v36, v2
	v_mov_b32_e32 v37, v2
	v_mov_b32_e32 v38, v2
	v_mov_b32_e32 v39, v2
	v_mov_b32_e32 v40, v2
	v_mov_b32_e32 v41, v2
	v_mov_b32_e32 v50, v2
	v_mov_b32_e32 v51, v2
	v_mov_b32_e32 v52, v2
	v_mov_b32_e32 v53, v2
	v_mov_b32_e32 v54, v2
	v_mov_b32_e32 v55, v2
	v_mov_b32_e32 v56, v2
	v_mov_b32_e32 v57, v2
	v_mov_b32_e32 v10, v2
	v_mov_b32_e32 v11, v2
	v_mov_b32_e32 v12, v2
	v_mov_b32_e32 v13, v2
	v_mov_b32_e32 v14, v2
	v_mov_b32_e32 v15, v2
	v_mov_b32_e32 v16, v2
	v_mov_b32_e32 v17, v2
	v_mov_b32_e32 v26, v2
	v_mov_b32_e32 v27, v2
	v_mov_b32_e32 v28, v2
	v_mov_b32_e32 v29, v2
	v_mov_b32_e32 v30, v2
	v_mov_b32_e32 v31, v2
	v_mov_b32_e32 v32, v2
	v_mov_b32_e32 v33, v2
	v_mov_b32_e32 v42, v2
	v_mov_b32_e32 v43, v2
	v_mov_b32_e32 v44, v2
	v_mov_b32_e32 v45, v2
	v_mov_b32_e32 v46, v2
	v_mov_b32_e32 v47, v2
	v_mov_b32_e32 v48, v2
	v_mov_b32_e32 v49, v2
	v_mov_b32_e32 v58, v2
	v_mov_b32_e32 v59, v2
	v_mov_b32_e32 v60, v2
	v_mov_b32_e32 v61, v2
	v_mov_b32_e32 v62, v2
	v_mov_b32_e32 v63, v2
	v_mov_b32_e32 v64, v2
	v_mov_b32_e32 v65, v2
	v_mov_b32_e32 v66, v2
	v_mov_b32_e32 v67, v2
	v_mov_b32_e32 v68, v2
	v_mov_b32_e32 v69, v2
	v_mov_b32_e32 v70, v2
	v_mov_b32_e32 v71, v2
	v_mov_b32_e32 v72, v2
	v_mov_b32_e32 v73, v2
	v_mov_b32_e32 v82, v2
	v_mov_b32_e32 v83, v2
	v_mov_b32_e32 v84, v2
	v_mov_b32_e32 v85, v2
	v_mov_b32_e32 v86, v2
	v_mov_b32_e32 v87, v2
	v_mov_b32_e32 v88, v2
	v_mov_b32_e32 v89, v2
	v_mov_b32_e32 v98, v2
	v_mov_b32_e32 v99, v2
	v_mov_b32_e32 v100, v2
	v_mov_b32_e32 v101, v2
	v_mov_b32_e32 v102, v2
	v_mov_b32_e32 v103, v2
	v_mov_b32_e32 v104, v2
	v_mov_b32_e32 v105, v2
	v_mov_b32_e32 v114, v2
	v_mov_b32_e32 v115, v2
	v_mov_b32_e32 v116, v2
	v_mov_b32_e32 v117, v2
	v_mov_b32_e32 v122, v2
	v_mov_b32_e32 v123, v2
	v_mov_b32_e32 v124, v2
	v_mov_b32_e32 v125, v2
	v_mov_b32_e32 v74, v2
	v_mov_b32_e32 v75, v2
	v_mov_b32_e32 v76, v2
	v_mov_b32_e32 v77, v2
	v_mov_b32_e32 v78, v2
	v_mov_b32_e32 v79, v2
	v_mov_b32_e32 v80, v2
	v_mov_b32_e32 v81, v2
	v_mov_b32_e32 v90, v2
	v_mov_b32_e32 v91, v2
	v_mov_b32_e32 v92, v2
	v_mov_b32_e32 v93, v2
	v_mov_b32_e32 v94, v2
	v_mov_b32_e32 v95, v2
	v_mov_b32_e32 v96, v2
	v_mov_b32_e32 v97, v2
	v_mov_b32_e32 v106, v2
	v_mov_b32_e32 v107, v2
	v_mov_b32_e32 v108, v2
	v_mov_b32_e32 v109, v2
	v_mov_b32_e32 v110, v2
	v_mov_b32_e32 v111, v2
	v_mov_b32_e32 v112, v2
	v_mov_b32_e32 v113, v2
	v_mov_b32_e32 v130, v2
	v_mov_b32_e32 v131, v2
	v_mov_b32_e32 v132, v2
	v_mov_b32_e32 v133, v2
	v_mov_b32_e32 v134, v2
	v_mov_b32_e32 v135, v2
	v_mov_b32_e32 v136, v2
	v_mov_b32_e32 v137, v2
	s_movk_i32 s92, 0x2b20
	s_andn2_b64 vcc, exec, s[40:41]
	s_cbranch_vccnz .LBB0_2800
	s_branch .LBB0_2801

.LBB0_2891:
	s_add_u32 s44, s24, s36
	s_addc_u32 s45, s25, s37
	s_add_u32 s44, s44, 0x100
	s_addc_u32 s45, s45, 0
	s_add_u32 s50, s59, s36
	s_addc_u32 s64, s81, s37
	s_add_i32 s65, 0, 0x10000
	s_cmpk_eq_i32 s36, 0x1f00
	s_cselect_b32 s47, s29, s45
	s_cselect_b32 s46, s82, s44
	s_cselect_b32 s45, s27, s64
	s_cselect_b32 s44, s83, s50
	s_add_i32 s50, 0, 0x14000
	v_add_u32_e32 v160, s65, v146
	v_add_u32_e32 v164, s50, v146
	ds_read_b128 v[148:151], v160
	ds_read_b128 v[152:155], v160 offset:1024
	ds_read_b128 v[156:159], v160 offset:2048
	ds_read_b128 v[160:163], v160 offset:3072
	ds_read_b128 v[168:171], v164
	ds_read_b128 v[172:175], v164 offset:1024
	ds_read_b128 v[176:179], v164 offset:2048
	ds_read_b128 v[180:183], v164 offset:3072
	v_lshl_add_u64 v[164:165], v[144:145], 0, s[36:37]
	s_add_i32 m0, s4, 0xc000
	ds_read_b128 v[184:187], v147
	ds_read_b128 v[188:191], v147 offset:1024
	ds_read_b128 v[192:195], v147 offset:2048
	ds_read_b128 v[196:199], v147 offset:3072
	ds_read_b128 v[200:203], v147 offset:4096
	ds_read_b128 v[204:207], v147 offset:5120
	ds_read_b128 v[216:219], v147 offset:6144
	ds_read_b128 v[220:223], v147 offset:7168
	global_load_lds_dwordx4 v[164:165], off
	s_add_i32 m0, s4, 0xe000
	v_lshl_add_u64 v[164:165], v[142:143], 0, s[36:37]
	global_load_lds_dwordx4 v[164:165], off
	s_waitcnt vmcnt(8)
	s_waitcnt lgkmcnt(0)
	s_barrier
	s_waitcnt lgkmcnt(0)
	v_mfma_f32_16x16x32_bf16 v[134:137], v[148:151], v[184:187], v[134:137]
	v_mfma_f32_16x16x32_bf16 v[130:133], v[156:159], v[184:187], v[130:133]
	v_mfma_f32_16x16x32_bf16 v[110:113], v[148:151], v[192:195], v[110:113]
	v_mfma_f32_16x16x32_bf16 v[106:109], v[156:159], v[192:195], v[106:109]
	v_mfma_f32_16x16x32_bf16 v[94:97], v[148:151], v[200:203], v[94:97]
	v_mfma_f32_16x16x32_bf16 v[90:93], v[156:159], v[200:203], v[90:93]
	v_mfma_f32_16x16x32_bf16 v[78:81], v[148:151], v[216:219], v[78:81]
	v_mfma_f32_16x16x32_bf16 v[74:77], v[156:159], v[216:219], v[74:77]
	v_mfma_f32_16x16x32_bf16 v[134:137], v[152:155], v[188:191], v[134:137]
	v_mfma_f32_16x16x32_bf16 v[130:133], v[160:163], v[188:191], v[130:133]
	v_mfma_f32_16x16x32_bf16 v[110:113], v[152:155], v[196:199], v[110:113]
	v_mfma_f32_16x16x32_bf16 v[106:109], v[160:163], v[196:199], v[106:109]
	v_mfma_f32_16x16x32_bf16 v[94:97], v[152:155], v[204:207], v[94:97]
	v_mfma_f32_16x16x32_bf16 v[90:93], v[160:163], v[204:207], v[90:93]
	v_mfma_f32_16x16x32_bf16 v[78:81], v[152:155], v[220:223], v[78:81]
	v_mfma_f32_16x16x32_bf16 v[74:77], v[160:163], v[220:223], v[74:77]
	v_mfma_f32_16x16x32_bf16 v[118:121], v[168:171], v[184:187], v[118:121]
	v_mfma_f32_16x16x32_bf16 v[114:117], v[176:179], v[184:187], v[114:117]
	v_mfma_f32_16x16x32_bf16 v[102:105], v[168:171], v[192:195], v[102:105]
	v_mfma_f32_16x16x32_bf16 v[98:101], v[176:179], v[192:195], v[98:101]
	v_mfma_f32_16x16x32_bf16 v[86:89], v[168:171], v[200:203], v[86:89]
	v_mfma_f32_16x16x32_bf16 v[82:85], v[176:179], v[200:203], v[82:85]
	v_mfma_f32_16x16x32_bf16 v[70:73], v[168:171], v[216:219], v[70:73]
	v_mfma_f32_16x16x32_bf16 v[66:69], v[176:179], v[216:219], v[66:69]
	v_mfma_f32_16x16x32_bf16 v[118:121], v[172:175], v[188:191], v[118:121]
	v_mfma_f32_16x16x32_bf16 v[114:117], v[180:183], v[188:191], v[114:117]
	v_mfma_f32_16x16x32_bf16 v[102:105], v[172:175], v[196:199], v[102:105]
	v_mfma_f32_16x16x32_bf16 v[98:101], v[180:183], v[196:199], v[98:101]
	v_mfma_f32_16x16x32_bf16 v[86:89], v[172:175], v[204:207], v[86:89]
	v_mfma_f32_16x16x32_bf16 v[82:85], v[180:183], v[204:207], v[82:85]
	v_mfma_f32_16x16x32_bf16 v[70:73], v[172:175], v[220:223], v[70:73]
	v_mfma_f32_16x16x32_bf16 v[66:69], v[180:183], v[220:223], v[66:69]
	s_barrier
	s_add_i32 s64, s65, s76
	v_lshl_add_u64 v[164:165], s[44:45], 0, v[126:127]
	s_mov_b32 m0, s64
	ds_read_b128 v[184:187], v147 offset:16384
	ds_read_b128 v[188:191], v147 offset:17408
	ds_read_b128 v[192:195], v147 offset:18432
	ds_read_b128 v[196:199], v147 offset:19456
	ds_read_b128 v[200:203], v147 offset:20480
	ds_read_b128 v[204:207], v147 offset:21504
	ds_read_b128 v[216:219], v147 offset:22528
	ds_read_b128 v[220:223], v147 offset:23552
	global_load_lds_dwordx4 v[164:165], off
	s_add_i32 m0, s64, 0x2000
	s_add_u32 s92, s44, 0x100000
	v_lshl_add_u64 v[208:209], s[44:45], 0, v[122:123]
	s_addc_u32 s93, s45, 0
	s_add_i32 s50, s50, s76
	global_load_lds_dwordx4 v[208:209], off
	v_lshl_add_u64 v[240:241], s[92:93], 0, v[126:127]
	s_mov_b32 m0, s50
	v_lshl_add_u64 v[242:243], s[46:47], 0, v[124:125]
	global_load_lds_dwordx4 v[240:241], off
	s_add_i32 m0, s50, 0x2000
	v_lshl_add_u64 v[240:241], s[92:93], 0, v[122:123]
	global_load_lds_dwordx4 v[240:241], off
	s_mov_b32 m0, s4
	v_lshl_add_u64 v[240:241], s[46:47], 0, v[128:129]
	global_load_lds_dwordx4 v[240:241], off
	s_mov_b32 m0, s33
	s_nop 0
	global_load_lds_dwordx4 v[242:243], off
	s_waitcnt vmcnt(8)
	s_waitcnt lgkmcnt(0)
	s_barrier
	s_waitcnt lgkmcnt(0)
	v_mfma_f32_16x16x32_bf16 v[62:65], v[148:151], v[184:187], v[62:65]
	v_mfma_f32_16x16x32_bf16 v[58:61], v[156:159], v[184:187], v[58:61]
	v_mfma_f32_16x16x32_bf16 v[46:49], v[148:151], v[192:195], v[46:49]
	v_mfma_f32_16x16x32_bf16 v[42:45], v[156:159], v[192:195], v[42:45]
	v_mfma_f32_16x16x32_bf16 v[30:33], v[148:151], v[200:203], v[30:33]
	v_mfma_f32_16x16x32_bf16 v[26:29], v[156:159], v[200:203], v[26:29]
	v_mfma_f32_16x16x32_bf16 v[14:17], v[148:151], v[216:219], v[14:17]
	v_mfma_f32_16x16x32_bf16 v[10:13], v[156:159], v[216:219], v[10:13]
	v_mfma_f32_16x16x32_bf16 v[62:65], v[152:155], v[188:191], v[62:65]
	v_mfma_f32_16x16x32_bf16 v[58:61], v[160:163], v[188:191], v[58:61]
	v_mfma_f32_16x16x32_bf16 v[46:49], v[152:155], v[196:199], v[46:49]
	v_mfma_f32_16x16x32_bf16 v[42:45], v[160:163], v[196:199], v[42:45]
	v_mfma_f32_16x16x32_bf16 v[30:33], v[152:155], v[204:207], v[30:33]
	v_mfma_f32_16x16x32_bf16 v[26:29], v[160:163], v[204:207], v[26:29]
	v_mfma_f32_16x16x32_bf16 v[14:17], v[152:155], v[220:223], v[14:17]
	v_mfma_f32_16x16x32_bf16 v[10:13], v[160:163], v[220:223], v[10:13]
	v_mfma_f32_16x16x32_bf16 v[54:57], v[168:171], v[184:187], v[54:57]
	v_mfma_f32_16x16x32_bf16 v[50:53], v[176:179], v[184:187], v[50:53]
	v_mfma_f32_16x16x32_bf16 v[38:41], v[168:171], v[192:195], v[38:41]
	v_mfma_f32_16x16x32_bf16 v[34:37], v[176:179], v[192:195], v[34:37]
	v_mfma_f32_16x16x32_bf16 v[22:25], v[168:171], v[200:203], v[22:25]
	v_mfma_f32_16x16x32_bf16 v[18:21], v[176:179], v[200:203], v[18:21]
	v_mfma_f32_16x16x32_bf16 v[6:9], v[168:171], v[216:219], v[6:9]
	v_mfma_f32_16x16x32_bf16 v[2:5], v[176:179], v[216:219], v[2:5]
	v_mfma_f32_16x16x32_bf16 v[54:57], v[172:175], v[188:191], v[54:57]
	v_mfma_f32_16x16x32_bf16 v[50:53], v[180:183], v[188:191], v[50:53]
	v_mfma_f32_16x16x32_bf16 v[38:41], v[172:175], v[196:199], v[38:41]
	v_mfma_f32_16x16x32_bf16 v[34:37], v[180:183], v[196:199], v[34:37]
	v_mfma_f32_16x16x32_bf16 v[22:25], v[172:175], v[204:207], v[22:25]
	v_mfma_f32_16x16x32_bf16 v[18:21], v[180:183], v[204:207], v[18:21]
	v_mfma_f32_16x16x32_bf16 v[6:9], v[172:175], v[220:223], v[6:9]
	v_mfma_f32_16x16x32_bf16 v[2:5], v[180:183], v[220:223], v[2:5]
	s_barrier
	s_add_i32 s50, 0, 0x18000
	s_add_i32 s64, 0, 0x1c000
	v_add_u32_e32 v160, s50, v146
	v_add_u32_e32 v167, s64, v146
	ds_read_b128 v[148:151], v160
	ds_read_b128 v[152:155], v160 offset:1024
	ds_read_b128 v[156:159], v160 offset:2048
	ds_read_b128 v[160:163], v160 offset:3072
	ds_read_b128 v[168:171], v167
	ds_read_b128 v[172:175], v167 offset:1024
	ds_read_b128 v[176:179], v167 offset:2048
	ds_read_b128 v[180:183], v167 offset:3072
	s_add_u32 s46, s46, 0x100000
	s_addc_u32 s47, s47, 0
	s_mov_b32 m0, s77
	v_lshl_add_u64 v[244:245], s[46:47], 0, v[128:129]
	ds_read_b128 v[184:187], v147 offset:32768
	ds_read_b128 v[188:191], v147 offset:33792
	ds_read_b128 v[192:195], v147 offset:34816
	ds_read_b128 v[196:199], v147 offset:35840
	ds_read_b128 v[200:203], v147 offset:36864
	ds_read_b128 v[204:207], v147 offset:37888
	ds_read_b128 v[216:219], v147 offset:38912
	ds_read_b128 v[220:223], v147 offset:39936
	global_load_lds_dwordx4 v[244:245], off
	s_mov_b32 m0, s78
	v_lshl_add_u64 v[244:245], s[46:47], 0, v[124:125]
	global_load_lds_dwordx4 v[244:245], off
	s_waitcnt vmcnt(8)
	s_waitcnt lgkmcnt(0)
	s_barrier
	s_waitcnt lgkmcnt(0)
	v_mfma_f32_16x16x32_bf16 v[134:137], v[148:151], v[184:187], v[134:137]
	v_mfma_f32_16x16x32_bf16 v[130:133], v[156:159], v[184:187], v[130:133]
	v_mfma_f32_16x16x32_bf16 v[110:113], v[148:151], v[192:195], v[110:113]
	v_mfma_f32_16x16x32_bf16 v[106:109], v[156:159], v[192:195], v[106:109]
	v_mfma_f32_16x16x32_bf16 v[94:97], v[148:151], v[200:203], v[94:97]
	v_mfma_f32_16x16x32_bf16 v[90:93], v[156:159], v[200:203], v[90:93]
	v_mfma_f32_16x16x32_bf16 v[78:81], v[148:151], v[216:219], v[78:81]
	v_mfma_f32_16x16x32_bf16 v[74:77], v[156:159], v[216:219], v[74:77]
	v_mfma_f32_16x16x32_bf16 v[134:137], v[152:155], v[188:191], v[134:137]
	v_mfma_f32_16x16x32_bf16 v[130:133], v[160:163], v[188:191], v[130:133]
	v_mfma_f32_16x16x32_bf16 v[110:113], v[152:155], v[196:199], v[110:113]
	v_mfma_f32_16x16x32_bf16 v[106:109], v[160:163], v[196:199], v[106:109]
	v_mfma_f32_16x16x32_bf16 v[94:97], v[152:155], v[204:207], v[94:97]
	v_mfma_f32_16x16x32_bf16 v[90:93], v[160:163], v[204:207], v[90:93]
	v_mfma_f32_16x16x32_bf16 v[78:81], v[152:155], v[220:223], v[78:81]
	v_mfma_f32_16x16x32_bf16 v[74:77], v[160:163], v[220:223], v[74:77]
	v_mfma_f32_16x16x32_bf16 v[118:121], v[168:171], v[184:187], v[118:121]
	v_mfma_f32_16x16x32_bf16 v[114:117], v[176:179], v[184:187], v[114:117]
	v_mfma_f32_16x16x32_bf16 v[102:105], v[168:171], v[192:195], v[102:105]
	v_mfma_f32_16x16x32_bf16 v[98:101], v[176:179], v[192:195], v[98:101]
	v_mfma_f32_16x16x32_bf16 v[86:89], v[168:171], v[200:203], v[86:89]
	v_mfma_f32_16x16x32_bf16 v[82:85], v[176:179], v[200:203], v[82:85]
	v_mfma_f32_16x16x32_bf16 v[70:73], v[168:171], v[216:219], v[70:73]
	v_mfma_f32_16x16x32_bf16 v[66:69], v[176:179], v[216:219], v[66:69]
	v_mfma_f32_16x16x32_bf16 v[118:121], v[172:175], v[188:191], v[118:121]
	v_mfma_f32_16x16x32_bf16 v[114:117], v[180:183], v[188:191], v[114:117]
	v_mfma_f32_16x16x32_bf16 v[102:105], v[172:175], v[196:199], v[102:105]
	v_mfma_f32_16x16x32_bf16 v[98:101], v[180:183], v[196:199], v[98:101]
	v_mfma_f32_16x16x32_bf16 v[86:89], v[172:175], v[204:207], v[86:89]
	v_mfma_f32_16x16x32_bf16 v[82:85], v[180:183], v[204:207], v[82:85]
	v_mfma_f32_16x16x32_bf16 v[70:73], v[172:175], v[220:223], v[70:73]
	v_mfma_f32_16x16x32_bf16 v[66:69], v[180:183], v[220:223], v[66:69]
	s_barrier
	s_add_i32 s46, s50, s76
	v_lshl_add_u64 v[164:165], v[164:165], 0, s[56:57]
	s_mov_b32 m0, s46
	ds_read_b128 v[184:187], v147 offset:49152
	ds_read_b128 v[188:191], v147 offset:50176
	ds_read_b128 v[192:195], v147 offset:51200
	ds_read_b128 v[196:199], v147 offset:52224
	ds_read_b128 v[200:203], v147 offset:53248
	ds_read_b128 v[204:207], v147 offset:54272
	ds_read_b128 v[216:219], v147 offset:55296
	ds_read_b128 v[220:223], v147 offset:56320
	global_load_lds_dwordx4 v[164:165], off
	s_add_i32 m0, s46, 0x2000
	s_add_u32 s44, s44, 0x100080
	v_lshl_add_u64 v[164:165], v[208:209], 0, s[56:57]
	s_addc_u32 s45, s45, 0
	s_add_i32 s46, s64, s76
	global_load_lds_dwordx4 v[164:165], off
	s_mov_b32 m0, s46
	v_lshl_add_u64 v[164:165], s[44:45], 0, v[126:127]
	global_load_lds_dwordx4 v[164:165], off
	s_add_i32 m0, s46, 0x2000
	v_lshl_add_u64 v[164:165], s[44:45], 0, v[122:123]
	global_load_lds_dwordx4 v[164:165], off
	s_mov_b32 m0, s79
	v_lshl_add_u64 v[164:165], v[240:241], 0, s[56:57]
	global_load_lds_dwordx4 v[164:165], off
	s_mov_b32 m0, s80
	v_lshl_add_u64 v[164:165], v[242:243], 0, s[56:57]
	global_load_lds_dwordx4 v[164:165], off
	s_waitcnt vmcnt(8)
	s_waitcnt lgkmcnt(0)
	s_barrier
	s_waitcnt lgkmcnt(0)
	v_mfma_f32_16x16x32_bf16 v[62:65], v[148:151], v[184:187], v[62:65]
	v_mfma_f32_16x16x32_bf16 v[58:61], v[156:159], v[184:187], v[58:61]
	v_mfma_f32_16x16x32_bf16 v[46:49], v[148:151], v[192:195], v[46:49]
	v_mfma_f32_16x16x32_bf16 v[42:45], v[156:159], v[192:195], v[42:45]
	v_mfma_f32_16x16x32_bf16 v[30:33], v[148:151], v[200:203], v[30:33]
	v_mfma_f32_16x16x32_bf16 v[26:29], v[156:159], v[200:203], v[26:29]
	v_mfma_f32_16x16x32_bf16 v[14:17], v[148:151], v[216:219], v[14:17]
	v_mfma_f32_16x16x32_bf16 v[10:13], v[156:159], v[216:219], v[10:13]
	v_mfma_f32_16x16x32_bf16 v[62:65], v[152:155], v[188:191], v[62:65]
	v_mfma_f32_16x16x32_bf16 v[58:61], v[160:163], v[188:191], v[58:61]
	v_mfma_f32_16x16x32_bf16 v[46:49], v[152:155], v[196:199], v[46:49]
	v_mfma_f32_16x16x32_bf16 v[42:45], v[160:163], v[196:199], v[42:45]
	v_mfma_f32_16x16x32_bf16 v[30:33], v[152:155], v[204:207], v[30:33]
	v_mfma_f32_16x16x32_bf16 v[26:29], v[160:163], v[204:207], v[26:29]
	v_mfma_f32_16x16x32_bf16 v[14:17], v[152:155], v[220:223], v[14:17]
	v_mfma_f32_16x16x32_bf16 v[10:13], v[160:163], v[220:223], v[10:13]
	v_mfma_f32_16x16x32_bf16 v[54:57], v[168:171], v[184:187], v[54:57]
	v_mfma_f32_16x16x32_bf16 v[50:53], v[176:179], v[184:187], v[50:53]
	v_mfma_f32_16x16x32_bf16 v[38:41], v[168:171], v[192:195], v[38:41]
	v_mfma_f32_16x16x32_bf16 v[34:37], v[176:179], v[192:195], v[34:37]
	v_mfma_f32_16x16x32_bf16 v[22:25], v[168:171], v[200:203], v[22:25]
	v_mfma_f32_16x16x32_bf16 v[18:21], v[176:179], v[200:203], v[18:21]
	v_mfma_f32_16x16x32_bf16 v[6:9], v[168:171], v[216:219], v[6:9]
	v_mfma_f32_16x16x32_bf16 v[2:5], v[176:179], v[216:219], v[2:5]
	v_mfma_f32_16x16x32_bf16 v[54:57], v[172:175], v[188:191], v[54:57]
	v_mfma_f32_16x16x32_bf16 v[50:53], v[180:183], v[188:191], v[50:53]
	v_mfma_f32_16x16x32_bf16 v[38:41], v[172:175], v[196:199], v[38:41]
	v_mfma_f32_16x16x32_bf16 v[34:37], v[180:183], v[196:199], v[34:37]
	v_mfma_f32_16x16x32_bf16 v[22:25], v[172:175], v[204:207], v[22:25]
	v_mfma_f32_16x16x32_bf16 v[18:21], v[180:183], v[204:207], v[18:21]
	v_mfma_f32_16x16x32_bf16 v[6:9], v[172:175], v[220:223], v[6:9]
	v_mfma_f32_16x16x32_bf16 v[2:5], v[180:183], v[220:223], v[2:5]
	s_barrier
	s_add_i32 s84, s84, 2
	s_add_u32 s36, s36, 0x100
	s_addc_u32 s37, s37, 0
	s_cmp_gt_u32 s84, 61
	s_cbranch_scc0 .LBB0_2891
	s_add_u32 s36, s59, 0xffffff00
	s_addc_u32 s37, s81, -1
	s_andn2_b64 vcc, exec, s[42:43]
	s_cbranch_vccnz .LBB0_2894
	v_mov_b32_e32 v2, 0
	s_mov_b32 s20, s26
	s_mov_b32 s52, s28
	s_mov_b64 s[24:25], s[34:35]
	s_mov_b32 s68, s58
	v_mov_b32_e32 v3, v2
	v_mov_b32_e32 v4, v2
	v_mov_b32_e32 v5, v2
	v_mov_b32_e32 v6, v2
	v_mov_b32_e32 v7, v2
	v_mov_b32_e32 v8, v2
	v_mov_b32_e32 v9, v2
	v_mov_b32_e32 v18, v2
	v_mov_b32_e32 v19, v2
	v_mov_b32_e32 v20, v2
	v_mov_b32_e32 v21, v2
	v_mov_b32_e32 v22, v2
	v_mov_b32_e32 v23, v2
	v_mov_b32_e32 v24, v2
	v_mov_b32_e32 v25, v2
	v_mov_b32_e32 v34, v2
	v_mov_b32_e32 v35, v2
	v_mov_b32_e32 v36, v2
	v_mov_b32_e32 v37, v2
	v_mov_b32_e32 v38, v2
	v_mov_b32_e32 v39, v2
	v_mov_b32_e32 v40, v2
	v_mov_b32_e32 v41, v2
	v_mov_b32_e32 v50, v2
	v_mov_b32_e32 v51, v2
	v_mov_b32_e32 v52, v2
	v_mov_b32_e32 v53, v2
	v_mov_b32_e32 v54, v2
	v_mov_b32_e32 v55, v2
	v_mov_b32_e32 v56, v2
	v_mov_b32_e32 v57, v2
	v_mov_b32_e32 v10, v2
	v_mov_b32_e32 v11, v2
	v_mov_b32_e32 v12, v2
	v_mov_b32_e32 v13, v2
	v_mov_b32_e32 v14, v2
	v_mov_b32_e32 v15, v2
	v_mov_b32_e32 v16, v2
	v_mov_b32_e32 v17, v2
	v_mov_b32_e32 v26, v2
	v_mov_b32_e32 v27, v2
	v_mov_b32_e32 v28, v2
	v_mov_b32_e32 v29, v2
	v_mov_b32_e32 v30, v2
	v_mov_b32_e32 v31, v2
	v_mov_b32_e32 v32, v2
	v_mov_b32_e32 v33, v2
	v_mov_b32_e32 v42, v2
	v_mov_b32_e32 v43, v2
	v_mov_b32_e32 v44, v2
	v_mov_b32_e32 v45, v2
	v_mov_b32_e32 v46, v2
	v_mov_b32_e32 v47, v2
	v_mov_b32_e32 v48, v2
	v_mov_b32_e32 v49, v2
	v_mov_b32_e32 v58, v2
	v_mov_b32_e32 v59, v2
	v_mov_b32_e32 v60, v2
	v_mov_b32_e32 v61, v2
	v_mov_b32_e32 v62, v2
	v_mov_b32_e32 v63, v2
	v_mov_b32_e32 v64, v2
	v_mov_b32_e32 v65, v2
	v_mov_b32_e32 v66, v2
	v_mov_b32_e32 v67, v2
	v_mov_b32_e32 v68, v2
	v_mov_b32_e32 v69, v2
	v_mov_b32_e32 v70, v2
	v_mov_b32_e32 v71, v2
	v_mov_b32_e32 v72, v2
	v_mov_b32_e32 v73, v2
	v_mov_b32_e32 v82, v2
	v_mov_b32_e32 v83, v2
	v_mov_b32_e32 v84, v2
	v_mov_b32_e32 v85, v2
	v_mov_b32_e32 v86, v2
	v_mov_b32_e32 v87, v2
	v_mov_b32_e32 v88, v2
	v_mov_b32_e32 v89, v2
	v_mov_b32_e32 v98, v2
	v_mov_b32_e32 v99, v2
	v_mov_b32_e32 v100, v2
	v_mov_b32_e32 v101, v2
	v_mov_b32_e32 v102, v2
	v_mov_b32_e32 v103, v2
	v_mov_b32_e32 v104, v2
	v_mov_b32_e32 v105, v2
	v_mov_b32_e32 v114, v2
	v_mov_b32_e32 v115, v2
	v_mov_b32_e32 v116, v2
	v_mov_b32_e32 v117, v2
	v_mov_b32_e32 v118, v2
	v_mov_b32_e32 v119, v2
	v_mov_b32_e32 v120, v2
	v_mov_b32_e32 v121, v2
	v_mov_b32_e32 v74, v2
	v_mov_b32_e32 v75, v2
	v_mov_b32_e32 v76, v2
	v_mov_b32_e32 v77, v2
	v_mov_b32_e32 v78, v2
	v_mov_b32_e32 v79, v2
	v_mov_b32_e32 v80, v2
	v_mov_b32_e32 v81, v2
	v_mov_b32_e32 v90, v2
	v_mov_b32_e32 v91, v2
	v_mov_b32_e32 v92, v2
	v_mov_b32_e32 v93, v2
	v_mov_b32_e32 v94, v2
	v_mov_b32_e32 v95, v2
	v_mov_b32_e32 v96, v2
	v_mov_b32_e32 v97, v2
	v_mov_b32_e32 v106, v2
	v_mov_b32_e32 v107, v2
	v_mov_b32_e32 v108, v2
	v_mov_b32_e32 v109, v2
	v_mov_b32_e32 v110, v2
	v_mov_b32_e32 v111, v2
	v_mov_b32_e32 v112, v2
	v_mov_b32_e32 v113, v2
	v_mov_b32_e32 v130, v2
	v_mov_b32_e32 v131, v2
	v_mov_b32_e32 v132, v2
	v_mov_b32_e32 v133, v2
	v_mov_b32_e32 v134, v2
	v_mov_b32_e32 v135, v2
	v_mov_b32_e32 v136, v2
	v_mov_b32_e32 v137, v2
	s_movk_i32 s92, 0x2b20
	s_andn2_b64 vcc, exec, s[40:41]
	s_cbranch_vccnz .LBB0_2895
	s_branch .LBB0_2896

.LBB0_2982:
	s_add_u32 s42, s24, s36
	s_addc_u32 s43, s25, s37
	s_add_u32 s42, s42, 0x100
	s_addc_u32 s43, s43, 0
	s_add_u32 s50, s59, s36
	s_addc_u32 s64, s79, s37
	s_add_i32 s65, 0, 0x10000
	s_cmpk_eq_i32 s36, 0x1f00
	s_cselect_b32 s45, s29, s43
	s_cselect_b32 s44, s80, s42
	s_cselect_b32 s43, s27, s64
	s_cselect_b32 s42, s81, s50
	s_add_i32 s50, 0, 0x14000
	v_add_u32_e32 v160, s65, v146
	v_add_u32_e32 v176, s50, v146
	ds_read_b128 v[148:151], v160
	ds_read_b128 v[152:155], v160 offset:1024
	ds_read_b128 v[156:159], v160 offset:2048
	ds_read_b128 v[160:163], v160 offset:3072
	ds_read_b128 v[164:167], v176
	ds_read_b128 v[168:171], v176 offset:1024
	ds_read_b128 v[172:175], v176 offset:2048
	ds_read_b128 v[176:179], v176 offset:3072
	v_lshl_add_u64 v[208:209], v[144:145], 0, s[36:37]
	s_add_i32 m0, s4, 0xc000
	ds_read_b128 v[180:183], v147
	ds_read_b128 v[184:187], v147 offset:1024
	ds_read_b128 v[188:191], v147 offset:2048
	ds_read_b128 v[192:195], v147 offset:3072
	ds_read_b128 v[196:199], v147 offset:4096
	ds_read_b128 v[200:203], v147 offset:5120
	ds_read_b128 v[204:207], v147 offset:6144
	ds_read_b128 v[216:219], v147 offset:7168
	global_load_lds_dwordx4 v[208:209], off
	s_add_i32 m0, s4, 0xe000
	v_lshl_add_u64 v[208:209], v[142:143], 0, s[36:37]
	global_load_lds_dwordx4 v[208:209], off
	s_waitcnt vmcnt(8)
	s_waitcnt lgkmcnt(0)
	s_barrier
	s_waitcnt lgkmcnt(0)
	v_mfma_f32_16x16x32_bf16 v[134:137], v[148:151], v[180:183], v[134:137]
	v_mfma_f32_16x16x32_bf16 v[130:133], v[156:159], v[180:183], v[130:133]
	v_mfma_f32_16x16x32_bf16 v[110:113], v[148:151], v[188:191], v[110:113]
	v_mfma_f32_16x16x32_bf16 v[106:109], v[156:159], v[188:191], v[106:109]
	v_mfma_f32_16x16x32_bf16 v[94:97], v[148:151], v[196:199], v[94:97]
	v_mfma_f32_16x16x32_bf16 v[90:93], v[156:159], v[196:199], v[90:93]
	v_mfma_f32_16x16x32_bf16 v[78:81], v[148:151], v[204:207], v[78:81]
	v_mfma_f32_16x16x32_bf16 v[74:77], v[156:159], v[204:207], v[74:77]
	v_mfma_f32_16x16x32_bf16 v[134:137], v[152:155], v[184:187], v[134:137]
	v_mfma_f32_16x16x32_bf16 v[130:133], v[160:163], v[184:187], v[130:133]
	v_mfma_f32_16x16x32_bf16 v[110:113], v[152:155], v[192:195], v[110:113]
	v_mfma_f32_16x16x32_bf16 v[106:109], v[160:163], v[192:195], v[106:109]
	v_mfma_f32_16x16x32_bf16 v[94:97], v[152:155], v[200:203], v[94:97]
	v_mfma_f32_16x16x32_bf16 v[90:93], v[160:163], v[200:203], v[90:93]
	v_mfma_f32_16x16x32_bf16 v[78:81], v[152:155], v[216:219], v[78:81]
	v_mfma_f32_16x16x32_bf16 v[74:77], v[160:163], v[216:219], v[74:77]
	v_mfma_f32_16x16x32_bf16 v[118:121], v[164:167], v[180:183], v[118:121]
	v_mfma_f32_16x16x32_bf16 v[114:117], v[172:175], v[180:183], v[114:117]
	v_mfma_f32_16x16x32_bf16 v[102:105], v[164:167], v[188:191], v[102:105]
	v_mfma_f32_16x16x32_bf16 v[98:101], v[172:175], v[188:191], v[98:101]
	v_mfma_f32_16x16x32_bf16 v[86:89], v[164:167], v[196:199], v[86:89]
	v_mfma_f32_16x16x32_bf16 v[82:85], v[172:175], v[196:199], v[82:85]
	v_mfma_f32_16x16x32_bf16 v[70:73], v[164:167], v[204:207], v[70:73]
	v_mfma_f32_16x16x32_bf16 v[66:69], v[172:175], v[204:207], v[66:69]
	v_mfma_f32_16x16x32_bf16 v[118:121], v[168:171], v[184:187], v[118:121]
	v_mfma_f32_16x16x32_bf16 v[114:117], v[176:179], v[184:187], v[114:117]
	v_mfma_f32_16x16x32_bf16 v[102:105], v[168:171], v[192:195], v[102:105]
	v_mfma_f32_16x16x32_bf16 v[98:101], v[176:179], v[192:195], v[98:101]
	v_mfma_f32_16x16x32_bf16 v[86:89], v[168:171], v[200:203], v[86:89]
	v_mfma_f32_16x16x32_bf16 v[82:85], v[176:179], v[200:203], v[82:85]
	v_mfma_f32_16x16x32_bf16 v[70:73], v[168:171], v[216:219], v[70:73]
	v_mfma_f32_16x16x32_bf16 v[66:69], v[176:179], v[216:219], v[66:69]
	s_barrier
	s_add_i32 s64, s65, s63
	v_lshl_add_u64 v[208:209], s[42:43], 0, v[126:127]
	s_mov_b32 m0, s64
	ds_read_b128 v[180:183], v147 offset:16384
	ds_read_b128 v[184:187], v147 offset:17408
	ds_read_b128 v[188:191], v147 offset:18432
	ds_read_b128 v[192:195], v147 offset:19456
	ds_read_b128 v[196:199], v147 offset:20480
	ds_read_b128 v[200:203], v147 offset:21504
	ds_read_b128 v[204:207], v147 offset:22528
	ds_read_b128 v[216:219], v147 offset:23552
	global_load_lds_dwordx4 v[208:209], off
	s_add_i32 m0, s64, 0x2000
	s_add_u32 s84, s42, 0x100000
	v_lshl_add_u64 v[220:221], s[42:43], 0, v[122:123]
	s_addc_u32 s85, s43, 0
	s_add_i32 s50, s50, s63
	global_load_lds_dwordx4 v[220:221], off
	v_lshl_add_u64 v[222:223], s[84:85], 0, v[126:127]
	s_mov_b32 m0, s50
	v_lshl_add_u64 v[240:241], s[44:45], 0, v[124:125]
	global_load_lds_dwordx4 v[222:223], off
	s_add_i32 m0, s50, 0x2000
	v_lshl_add_u64 v[222:223], s[84:85], 0, v[122:123]
	global_load_lds_dwordx4 v[222:223], off
	s_mov_b32 m0, s4
	v_lshl_add_u64 v[222:223], s[44:45], 0, v[128:129]
	global_load_lds_dwordx4 v[222:223], off
	s_mov_b32 m0, s33
	s_nop 0
	global_load_lds_dwordx4 v[240:241], off
	s_waitcnt vmcnt(8)
	s_waitcnt lgkmcnt(0)
	s_barrier
	s_waitcnt lgkmcnt(0)
	v_mfma_f32_16x16x32_bf16 v[62:65], v[148:151], v[180:183], v[62:65]
	v_mfma_f32_16x16x32_bf16 v[58:61], v[156:159], v[180:183], v[58:61]
	v_mfma_f32_16x16x32_bf16 v[46:49], v[148:151], v[188:191], v[46:49]
	v_mfma_f32_16x16x32_bf16 v[42:45], v[156:159], v[188:191], v[42:45]
	v_mfma_f32_16x16x32_bf16 v[30:33], v[148:151], v[196:199], v[30:33]
	v_mfma_f32_16x16x32_bf16 v[26:29], v[156:159], v[196:199], v[26:29]
	v_mfma_f32_16x16x32_bf16 v[14:17], v[148:151], v[204:207], v[14:17]
	v_mfma_f32_16x16x32_bf16 v[10:13], v[156:159], v[204:207], v[10:13]
	v_mfma_f32_16x16x32_bf16 v[62:65], v[152:155], v[184:187], v[62:65]
	v_mfma_f32_16x16x32_bf16 v[58:61], v[160:163], v[184:187], v[58:61]
	v_mfma_f32_16x16x32_bf16 v[46:49], v[152:155], v[192:195], v[46:49]
	v_mfma_f32_16x16x32_bf16 v[42:45], v[160:163], v[192:195], v[42:45]
	v_mfma_f32_16x16x32_bf16 v[30:33], v[152:155], v[200:203], v[30:33]
	v_mfma_f32_16x16x32_bf16 v[26:29], v[160:163], v[200:203], v[26:29]
	v_mfma_f32_16x16x32_bf16 v[14:17], v[152:155], v[216:219], v[14:17]
	v_mfma_f32_16x16x32_bf16 v[10:13], v[160:163], v[216:219], v[10:13]
	v_mfma_f32_16x16x32_bf16 v[54:57], v[164:167], v[180:183], v[54:57]
	v_mfma_f32_16x16x32_bf16 v[50:53], v[172:175], v[180:183], v[50:53]
	v_mfma_f32_16x16x32_bf16 v[38:41], v[164:167], v[188:191], v[38:41]
	v_mfma_f32_16x16x32_bf16 v[34:37], v[172:175], v[188:191], v[34:37]
	v_mfma_f32_16x16x32_bf16 v[22:25], v[164:167], v[196:199], v[22:25]
	v_mfma_f32_16x16x32_bf16 v[18:21], v[172:175], v[196:199], v[18:21]
	v_mfma_f32_16x16x32_bf16 v[6:9], v[164:167], v[204:207], v[6:9]
	v_mfma_f32_16x16x32_bf16 v[2:5], v[172:175], v[204:207], v[2:5]
	v_mfma_f32_16x16x32_bf16 v[54:57], v[168:171], v[184:187], v[54:57]
	v_mfma_f32_16x16x32_bf16 v[50:53], v[176:179], v[184:187], v[50:53]
	v_mfma_f32_16x16x32_bf16 v[38:41], v[168:171], v[192:195], v[38:41]
	v_mfma_f32_16x16x32_bf16 v[34:37], v[176:179], v[192:195], v[34:37]
	v_mfma_f32_16x16x32_bf16 v[22:25], v[168:171], v[200:203], v[22:25]
	v_mfma_f32_16x16x32_bf16 v[18:21], v[176:179], v[200:203], v[18:21]
	v_mfma_f32_16x16x32_bf16 v[6:9], v[168:171], v[216:219], v[6:9]
	v_mfma_f32_16x16x32_bf16 v[2:5], v[176:179], v[216:219], v[2:5]
	s_barrier
	s_add_i32 s50, 0, 0x18000
	s_add_i32 s64, 0, 0x1c000
	v_add_u32_e32 v160, s50, v146
	v_add_u32_e32 v176, s64, v146
	ds_read_b128 v[148:151], v160
	ds_read_b128 v[152:155], v160 offset:1024
	ds_read_b128 v[156:159], v160 offset:2048
	ds_read_b128 v[160:163], v160 offset:3072
	ds_read_b128 v[164:167], v176
	ds_read_b128 v[168:171], v176 offset:1024
	ds_read_b128 v[172:175], v176 offset:2048
	ds_read_b128 v[176:179], v176 offset:3072
	s_add_u32 s44, s44, 0x100000
	s_addc_u32 s45, s45, 0
	s_mov_b32 m0, s70
	v_lshl_add_u64 v[242:243], s[44:45], 0, v[128:129]
	ds_read_b128 v[180:183], v147 offset:32768
	ds_read_b128 v[184:187], v147 offset:33792
	ds_read_b128 v[188:191], v147 offset:34816
	ds_read_b128 v[192:195], v147 offset:35840
	ds_read_b128 v[196:199], v147 offset:36864
	ds_read_b128 v[200:203], v147 offset:37888
	ds_read_b128 v[204:207], v147 offset:38912
	ds_read_b128 v[216:219], v147 offset:39936
	global_load_lds_dwordx4 v[242:243], off
	s_mov_b32 m0, s71
	v_lshl_add_u64 v[242:243], s[44:45], 0, v[124:125]
	global_load_lds_dwordx4 v[242:243], off
	s_waitcnt vmcnt(8)
	s_waitcnt lgkmcnt(0)
	s_barrier
	s_waitcnt lgkmcnt(0)
	v_mfma_f32_16x16x32_bf16 v[134:137], v[148:151], v[180:183], v[134:137]
	v_mfma_f32_16x16x32_bf16 v[130:133], v[156:159], v[180:183], v[130:133]
	v_mfma_f32_16x16x32_bf16 v[110:113], v[148:151], v[188:191], v[110:113]
	v_mfma_f32_16x16x32_bf16 v[106:109], v[156:159], v[188:191], v[106:109]
	v_mfma_f32_16x16x32_bf16 v[94:97], v[148:151], v[196:199], v[94:97]
	v_mfma_f32_16x16x32_bf16 v[90:93], v[156:159], v[196:199], v[90:93]
	v_mfma_f32_16x16x32_bf16 v[78:81], v[148:151], v[204:207], v[78:81]
	v_mfma_f32_16x16x32_bf16 v[74:77], v[156:159], v[204:207], v[74:77]
	v_mfma_f32_16x16x32_bf16 v[134:137], v[152:155], v[184:187], v[134:137]
	v_mfma_f32_16x16x32_bf16 v[130:133], v[160:163], v[184:187], v[130:133]
	v_mfma_f32_16x16x32_bf16 v[110:113], v[152:155], v[192:195], v[110:113]
	v_mfma_f32_16x16x32_bf16 v[106:109], v[160:163], v[192:195], v[106:109]
	v_mfma_f32_16x16x32_bf16 v[94:97], v[152:155], v[200:203], v[94:97]
	v_mfma_f32_16x16x32_bf16 v[90:93], v[160:163], v[200:203], v[90:93]
	v_mfma_f32_16x16x32_bf16 v[78:81], v[152:155], v[216:219], v[78:81]
	v_mfma_f32_16x16x32_bf16 v[74:77], v[160:163], v[216:219], v[74:77]
	v_mfma_f32_16x16x32_bf16 v[118:121], v[164:167], v[180:183], v[118:121]
	v_mfma_f32_16x16x32_bf16 v[114:117], v[172:175], v[180:183], v[114:117]
	v_mfma_f32_16x16x32_bf16 v[102:105], v[164:167], v[188:191], v[102:105]
	v_mfma_f32_16x16x32_bf16 v[98:101], v[172:175], v[188:191], v[98:101]
	v_mfma_f32_16x16x32_bf16 v[86:89], v[164:167], v[196:199], v[86:89]
	v_mfma_f32_16x16x32_bf16 v[82:85], v[172:175], v[196:199], v[82:85]
	v_mfma_f32_16x16x32_bf16 v[70:73], v[164:167], v[204:207], v[70:73]
	v_mfma_f32_16x16x32_bf16 v[66:69], v[172:175], v[204:207], v[66:69]
	v_mfma_f32_16x16x32_bf16 v[118:121], v[168:171], v[184:187], v[118:121]
	v_mfma_f32_16x16x32_bf16 v[114:117], v[176:179], v[184:187], v[114:117]
	v_mfma_f32_16x16x32_bf16 v[102:105], v[168:171], v[192:195], v[102:105]
	v_mfma_f32_16x16x32_bf16 v[98:101], v[176:179], v[192:195], v[98:101]
	v_mfma_f32_16x16x32_bf16 v[86:89], v[168:171], v[200:203], v[86:89]
	v_mfma_f32_16x16x32_bf16 v[82:85], v[176:179], v[200:203], v[82:85]
	v_mfma_f32_16x16x32_bf16 v[70:73], v[168:171], v[216:219], v[70:73]
	v_mfma_f32_16x16x32_bf16 v[66:69], v[176:179], v[216:219], v[66:69]
	s_barrier
	s_add_i32 s44, s50, s63
	v_lshl_add_u64 v[208:209], v[208:209], 0, s[56:57]
	s_mov_b32 m0, s44
	ds_read_b128 v[180:183], v147 offset:49152
	ds_read_b128 v[184:187], v147 offset:50176
	ds_read_b128 v[188:191], v147 offset:51200
	ds_read_b128 v[192:195], v147 offset:52224
	ds_read_b128 v[196:199], v147 offset:53248
	ds_read_b128 v[200:203], v147 offset:54272
	ds_read_b128 v[204:207], v147 offset:55296
	ds_read_b128 v[216:219], v147 offset:56320
	global_load_lds_dwordx4 v[208:209], off
	s_add_i32 m0, s44, 0x2000
	s_add_u32 s42, s42, 0x100080
	v_lshl_add_u64 v[208:209], v[220:221], 0, s[56:57]
	s_addc_u32 s43, s43, 0
	s_add_i32 s44, s64, s63
	global_load_lds_dwordx4 v[208:209], off
	s_mov_b32 m0, s44
	v_lshl_add_u64 v[208:209], s[42:43], 0, v[126:127]
	global_load_lds_dwordx4 v[208:209], off
	s_add_i32 m0, s44, 0x2000
	v_lshl_add_u64 v[208:209], s[42:43], 0, v[122:123]
	global_load_lds_dwordx4 v[208:209], off
	s_mov_b32 m0, s76
	v_lshl_add_u64 v[208:209], v[222:223], 0, s[56:57]
	global_load_lds_dwordx4 v[208:209], off
	s_mov_b32 m0, s77
	v_lshl_add_u64 v[208:209], v[240:241], 0, s[56:57]
	global_load_lds_dwordx4 v[208:209], off
	s_waitcnt vmcnt(8)
	s_waitcnt lgkmcnt(0)
	s_barrier
	s_waitcnt lgkmcnt(0)
	v_mfma_f32_16x16x32_bf16 v[62:65], v[148:151], v[180:183], v[62:65]
	v_mfma_f32_16x16x32_bf16 v[58:61], v[156:159], v[180:183], v[58:61]
	v_mfma_f32_16x16x32_bf16 v[46:49], v[148:151], v[188:191], v[46:49]
	v_mfma_f32_16x16x32_bf16 v[42:45], v[156:159], v[188:191], v[42:45]
	v_mfma_f32_16x16x32_bf16 v[30:33], v[148:151], v[196:199], v[30:33]
	v_mfma_f32_16x16x32_bf16 v[26:29], v[156:159], v[196:199], v[26:29]
	v_mfma_f32_16x16x32_bf16 v[14:17], v[148:151], v[204:207], v[14:17]
	v_mfma_f32_16x16x32_bf16 v[10:13], v[156:159], v[204:207], v[10:13]
	v_mfma_f32_16x16x32_bf16 v[62:65], v[152:155], v[184:187], v[62:65]
	v_mfma_f32_16x16x32_bf16 v[58:61], v[160:163], v[184:187], v[58:61]
	v_mfma_f32_16x16x32_bf16 v[46:49], v[152:155], v[192:195], v[46:49]
	v_mfma_f32_16x16x32_bf16 v[42:45], v[160:163], v[192:195], v[42:45]
	v_mfma_f32_16x16x32_bf16 v[30:33], v[152:155], v[200:203], v[30:33]
	v_mfma_f32_16x16x32_bf16 v[26:29], v[160:163], v[200:203], v[26:29]
	v_mfma_f32_16x16x32_bf16 v[14:17], v[152:155], v[216:219], v[14:17]
	v_mfma_f32_16x16x32_bf16 v[10:13], v[160:163], v[216:219], v[10:13]
	v_mfma_f32_16x16x32_bf16 v[54:57], v[164:167], v[180:183], v[54:57]
	v_mfma_f32_16x16x32_bf16 v[50:53], v[172:175], v[180:183], v[50:53]
	v_mfma_f32_16x16x32_bf16 v[38:41], v[164:167], v[188:191], v[38:41]
	v_mfma_f32_16x16x32_bf16 v[34:37], v[172:175], v[188:191], v[34:37]
	v_mfma_f32_16x16x32_bf16 v[22:25], v[164:167], v[196:199], v[22:25]
	v_mfma_f32_16x16x32_bf16 v[18:21], v[172:175], v[196:199], v[18:21]
	v_mfma_f32_16x16x32_bf16 v[6:9], v[164:167], v[204:207], v[6:9]
	v_mfma_f32_16x16x32_bf16 v[2:5], v[172:175], v[204:207], v[2:5]
	v_mfma_f32_16x16x32_bf16 v[54:57], v[168:171], v[184:187], v[54:57]
	v_mfma_f32_16x16x32_bf16 v[50:53], v[176:179], v[184:187], v[50:53]
	v_mfma_f32_16x16x32_bf16 v[38:41], v[168:171], v[192:195], v[38:41]
	v_mfma_f32_16x16x32_bf16 v[34:37], v[176:179], v[192:195], v[34:37]
	v_mfma_f32_16x16x32_bf16 v[22:25], v[168:171], v[200:203], v[22:25]
	v_mfma_f32_16x16x32_bf16 v[18:21], v[176:179], v[200:203], v[18:21]
	v_mfma_f32_16x16x32_bf16 v[6:9], v[168:171], v[216:219], v[6:9]
	v_mfma_f32_16x16x32_bf16 v[2:5], v[176:179], v[216:219], v[2:5]
	s_barrier
	s_add_i32 s82, s82, 2
	s_add_u32 s36, s36, 0x100
	s_addc_u32 s37, s37, 0
	s_cmp_gt_u32 s82, 61
	s_cbranch_scc0 .LBB0_2982
	s_add_u32 s36, s59, 0xffffff00
	s_addc_u32 s37, s79, -1
	s_andn2_b64 vcc, exec, s[40:41]
	s_cbranch_vccnz .LBB0_2985
	v_mov_b32_e32 v2, 0
	s_mov_b32 s20, s26
	s_mov_b32 s78, s28
	s_mov_b64 s[24:25], s[34:35]
	s_mov_b32 s68, s58
	v_mov_b32_e32 v3, v2
	v_mov_b32_e32 v4, v2
	v_mov_b32_e32 v5, v2
	v_mov_b32_e32 v6, v2
	v_mov_b32_e32 v7, v2
	v_mov_b32_e32 v8, v2
	v_mov_b32_e32 v9, v2
	v_mov_b32_e32 v18, v2
	v_mov_b32_e32 v19, v2
	v_mov_b32_e32 v20, v2
	v_mov_b32_e32 v21, v2
	v_mov_b32_e32 v22, v2
	v_mov_b32_e32 v23, v2
	v_mov_b32_e32 v24, v2
	v_mov_b32_e32 v25, v2
	v_mov_b32_e32 v34, v2
	v_mov_b32_e32 v35, v2
	v_mov_b32_e32 v36, v2
	v_mov_b32_e32 v37, v2
	v_mov_b32_e32 v38, v2
	v_mov_b32_e32 v39, v2
	v_mov_b32_e32 v40, v2
	v_mov_b32_e32 v41, v2
	v_mov_b32_e32 v50, v2
	v_mov_b32_e32 v51, v2
	v_mov_b32_e32 v52, v2
	v_mov_b32_e32 v53, v2
	v_mov_b32_e32 v54, v2
	v_mov_b32_e32 v55, v2
	v_mov_b32_e32 v56, v2
	v_mov_b32_e32 v57, v2
	v_mov_b32_e32 v10, v2
	v_mov_b32_e32 v11, v2
	v_mov_b32_e32 v12, v2
	v_mov_b32_e32 v13, v2
	v_mov_b32_e32 v14, v2
	v_mov_b32_e32 v15, v2
	v_mov_b32_e32 v16, v2
	v_mov_b32_e32 v17, v2
	v_mov_b32_e32 v26, v2
	v_mov_b32_e32 v27, v2
	v_mov_b32_e32 v28, v2
	v_mov_b32_e32 v29, v2
	v_mov_b32_e32 v30, v2
	v_mov_b32_e32 v31, v2
	v_mov_b32_e32 v32, v2
	v_mov_b32_e32 v33, v2
	v_mov_b32_e32 v42, v2
	v_mov_b32_e32 v43, v2
	v_mov_b32_e32 v44, v2
	v_mov_b32_e32 v45, v2
	v_mov_b32_e32 v46, v2
	v_mov_b32_e32 v47, v2
	v_mov_b32_e32 v48, v2
	v_mov_b32_e32 v49, v2
	v_mov_b32_e32 v58, v2
	v_mov_b32_e32 v59, v2
	v_mov_b32_e32 v60, v2
	v_mov_b32_e32 v61, v2
	v_mov_b32_e32 v62, v2
	v_mov_b32_e32 v63, v2
	v_mov_b32_e32 v64, v2
	v_mov_b32_e32 v65, v2
	v_mov_b32_e32 v66, v2
	v_mov_b32_e32 v67, v2
	v_mov_b32_e32 v68, v2
	v_mov_b32_e32 v69, v2
	v_mov_b32_e32 v70, v2
	v_mov_b32_e32 v71, v2
	v_mov_b32_e32 v72, v2
	v_mov_b32_e32 v73, v2
	v_mov_b32_e32 v82, v2
	v_mov_b32_e32 v83, v2
	v_mov_b32_e32 v84, v2
	v_mov_b32_e32 v85, v2
	v_mov_b32_e32 v86, v2
	v_mov_b32_e32 v87, v2
	v_mov_b32_e32 v88, v2
	v_mov_b32_e32 v89, v2
	v_mov_b32_e32 v98, v2
	v_mov_b32_e32 v99, v2
	v_mov_b32_e32 v100, v2
	v_mov_b32_e32 v101, v2
	v_mov_b32_e32 v102, v2
	v_mov_b32_e32 v103, v2
	v_mov_b32_e32 v104, v2
	v_mov_b32_e32 v105, v2
	v_mov_b32_e32 v114, v2
	v_mov_b32_e32 v115, v2
	v_mov_b32_e32 v116, v2
	v_mov_b32_e32 v117, v2
	v_mov_b32_e32 v118, v2
	v_mov_b32_e32 v119, v2
	v_mov_b32_e32 v120, v2
	v_mov_b32_e32 v121, v2
	v_mov_b32_e32 v74, v2
	v_mov_b32_e32 v75, v2
	v_mov_b32_e32 v76, v2
	v_mov_b32_e32 v77, v2
	v_mov_b32_e32 v78, v2
	v_mov_b32_e32 v79, v2
	v_mov_b32_e32 v80, v2
	v_mov_b32_e32 v81, v2
	v_mov_b32_e32 v90, v2
	v_mov_b32_e32 v91, v2
	v_mov_b32_e32 v92, v2
	v_mov_b32_e32 v93, v2
	v_mov_b32_e32 v94, v2
	v_mov_b32_e32 v95, v2
	v_mov_b32_e32 v96, v2
	v_mov_b32_e32 v97, v2
	v_mov_b32_e32 v106, v2
	v_mov_b32_e32 v107, v2
	v_mov_b32_e32 v108, v2
	v_mov_b32_e32 v109, v2
	v_mov_b32_e32 v110, v2
	v_mov_b32_e32 v111, v2
	v_mov_b32_e32 v112, v2
	v_mov_b32_e32 v113, v2
	v_mov_b32_e32 v130, v2
	v_mov_b32_e32 v131, v2
	v_mov_b32_e32 v132, v2
	v_mov_b32_e32 v133, v2
	v_mov_b32_e32 v134, v2
	v_mov_b32_e32 v135, v2
	v_mov_b32_e32 v136, v2
	v_mov_b32_e32 v137, v2
	s_andn2_b64 vcc, exec, s[38:39]
	s_cbranch_vccnz .LBB0_2986
	s_branch .LBB0_2987
